# speedup vs baseline: 1.0102x; 1.0008x over previous
.LE_pok19:
	s_waitcnt lgkmcnt(0)
	s_barrier
	s_mov_b32 m0, s52
	s_add_u32 s44, s34, 0x0
	s_addc_u32 s45, s35, 0
	global_load_lds_dwordx4 v192, s[44:45] sc1
	global_load_lds_dwordx4 v192, s[44:45] offset:1024 sc1
	global_load_lds_dwordx4 v192, s[44:45] offset:2048 sc1
	global_load_lds_dwordx4 v192, s[44:45] offset:3072 sc1
	s_mov_b32 m0, s53
	s_add_u32 s44, s34, 0x1000
	s_addc_u32 s45, s35, 0
	global_load_lds_dwordx4 v192, s[44:45] sc1
	global_load_lds_dwordx4 v192, s[44:45] offset:1024 sc1
	global_load_lds_dwordx4 v192, s[44:45] offset:2048 sc1
	global_load_lds_dwordx4 v192, s[44:45] offset:3072 sc1
	s_mov_b32 m0, s54
	s_add_u32 s44, s34, 0x8000
	s_addc_u32 s45, s35, 0
	global_load_lds_dwordx4 v192, s[44:45] sc1
	global_load_lds_dwordx4 v192, s[44:45] offset:1024 sc1
	global_load_lds_dwordx4 v192, s[44:45] offset:2048 sc1
	global_load_lds_dwordx4 v192, s[44:45] offset:3072 sc1
	s_mov_b32 m0, s55
	s_add_u32 s44, s34, 0x9000
	s_addc_u32 s45, s35, 0
	global_load_lds_dwordx4 v192, s[44:45] sc1
	global_load_lds_dwordx4 v192, s[44:45] offset:1024 sc1
	global_load_lds_dwordx4 v192, s[44:45] offset:2048 sc1
	global_load_lds_dwordx4 v192, s[44:45] offset:3072 sc1
	s_waitcnt vmcnt(8)
	s_barrier
	s_mov_b32 m0, s56
	s_add_u32 s44, s34, 0x10000
	s_addc_u32 s45, s35, 0
	global_load_lds_dwordx4 v192, s[44:45] sc1
	ds_read_b128 v[160:163], v192 offset:0
	ds_read_b128 v[164:167], v192 offset:1024
	ds_read_b128 v[168:171], v192 offset:2048
	ds_read_b128 v[172:175], v192 offset:3072
	ds_read_b128 v[176:179], v192 offset:4096
	ds_read_b128 v[180:183], v192 offset:5120
	ds_read_b128 v[184:187], v192 offset:6144
	ds_read_b128 v[188:191], v192 offset:7168
.LE_loop16:
	s_sub_u32 s71, s33, 1
	s_add_u32 s61, s33, 1
	s_min_u32 s61, s61, s60
	s_and_b32 s64, s71, 1
	s_lshl_b32 s64, s64, 22
	s_add_u32 s64, s64, s50
	s_add_u32 s64, s64, 0x60000
	s_add_u32 s36, s6, s64
	s_addc_u32 s37, s7, 0
	s_lshl_b32 s64, s71, 3
	s_add_u32 s64, s64, s29
	s_lshl_b32 s64, s64, 5
	s_add_u32 s64, s64, s30
	s_lshl_b32 s64, s64, 2
	s_add_u32 s40, s8, s64
	s_addc_u32 s41, s9, 0
	s_lshl_b32 s64, s33, 11
	s_lshl_b32 s65, s29, 8
	s_add_u32 s64, s64, s65
	s_add_u32 s64, s64, 128
	s_lshl_b32 s64, s64, 3
	s_add_u32 s42, s12, s64
	s_addc_u32 s43, s13, 0
	s_nop 3
	global_load_dword v228, v249, s[42:43] offset:0
	global_load_dword v229, v249, s[42:43] offset:256
	s_waitcnt lgkmcnt(2)
	v_mfma_f32_32x32x16_f16 v[0:15], a[0:3], v[160:163], v[0:15]
	ds_read_b128 v[160:163], v192 offset:8192
	v_exp_f32_e32 v200, v96
	v_mfma_f32_32x32x16_f16 v[16:31], a[0:3], v[164:167], v[16:31]
	ds_read_b128 v[164:167], v192 offset:9216
	s_lshl_b32 s64, s71, 3
	s_add_u32 s64, s64, s29
	s_lshl_b32 s64, s64, 7
	s_add_u32 s38, s8, s64
	s_addc_u32 s39, s9, 0
	global_load_dword v251, v196, s[38:39] sc1
	v_exp_f32_e32 v201, v97
	v_add_f32_e32 v200, 1.0, v200
	v_mfma_f32_32x32x16_f16 v[0:15], a[4:7], v[168:171], v[0:15]
	ds_read_b128 v[168:171], v192 offset:10240
	v_exp_f32_e32 v202, v98
	v_add_f32_e32 v201, 1.0, v201
	v_mfma_f32_32x32x16_f16 v[16:31], a[4:7], v[172:175], v[16:31]
	ds_read_b128 v[172:175], v192 offset:11264
	global_load_lds_dwordx4 v192, s[44:45] offset:1024 sc1
	v_exp_f32_e32 v203, v99
	v_add_f32_e32 v202, 1.0, v202
	v_mfma_f32_32x32x16_f16 v[0:15], a[8:11], v[176:179], v[0:15]
	ds_read_b128 v[176:179], v192 offset:12288
	v_exp_f32_e32 v204, v100
	v_add_f32_e32 v203, 1.0, v203
	v_mfma_f32_32x32x16_f16 v[16:31], a[8:11], v[180:183], v[16:31]
	ds_read_b128 v[180:183], v192 offset:13312
	v_exp_f32_e32 v205, v101
	v_add_f32_e32 v204, 1.0, v204
	s_waitcnt lgkmcnt(2)
	v_mfma_f32_32x32x16_f16 v[0:15], a[12:15], v[184:187], v[0:15]
	ds_read_b128 v[184:187], v192 offset:14336
	v_exp_f32_e32 v206, v102
	v_add_f32_e32 v205, 1.0, v205
	v_mfma_f32_32x32x16_f16 v[16:31], a[12:15], v[188:191], v[16:31]
	ds_read_b128 v[188:191], v192 offset:15360
	global_load_lds_dwordx4 v192, s[44:45] offset:2048 sc1
	v_exp_f32_e32 v207, v103
	v_add_f32_e32 v206, 1.0, v206
	v_mfma_f32_32x32x16_f16 v[0:15], a[16:19], v[160:163], v[0:15]
	ds_read_b128 v[160:163], v192 offset:16384
	v_exp_f32_e32 v208, v104
	v_add_f32_e32 v207, 1.0, v207
	v_mfma_f32_32x32x16_f16 v[16:31], a[16:19], v[164:167], v[16:31]
	ds_read_b128 v[164:167], v192 offset:17408
	v_exp_f32_e32 v209, v105
	v_add_f32_e32 v208, 1.0, v208
	v_mfma_f32_32x32x16_f16 v[0:15], a[20:23], v[168:171], v[0:15]
	ds_read_b128 v[168:171], v192 offset:18432
	v_exp_f32_e32 v210, v106
	v_add_f32_e32 v209, 1.0, v209
	v_mfma_f32_32x32x16_f16 v[16:31], a[20:23], v[172:175], v[16:31]
	ds_read_b128 v[172:175], v192 offset:19456
	global_load_lds_dwordx4 v192, s[44:45] offset:3072 sc1
	v_exp_f32_e32 v211, v107
	v_add_f32_e32 v210, 1.0, v210
	s_waitcnt lgkmcnt(2)
	v_mfma_f32_32x32x16_f16 v[0:15], a[24:27], v[176:179], v[0:15]
	ds_read_b128 v[176:179], v192 offset:20480
	v_exp_f32_e32 v212, v108
	v_add_f32_e32 v211, 1.0, v211
	v_mfma_f32_32x32x16_f16 v[16:31], a[24:27], v[180:183], v[16:31]
	ds_read_b128 v[180:183], v192 offset:21504
	v_exp_f32_e32 v213, v109
	v_add_f32_e32 v212, 1.0, v212
	v_mfma_f32_32x32x16_f16 v[0:15], a[28:31], v[184:187], v[0:15]
	ds_read_b128 v[184:187], v192 offset:22528
	v_exp_f32_e32 v214, v110
	v_add_f32_e32 v213, 1.0, v213
	v_mfma_f32_32x32x16_f16 v[16:31], a[28:31], v[188:191], v[16:31]
	ds_read_b128 v[188:191], v192 offset:23552
	s_mov_b32 m0, s57
	s_add_u32 s44, s34, 0x11000
	s_addc_u32 s45, s35, 0
	global_load_lds_dwordx4 v192, s[44:45] sc1
	v_exp_f32_e32 v215, v111
	v_add_f32_e32 v214, 1.0, v214
	v_mfma_f32_32x32x16_f16 v[0:15], a[32:35], v[160:163], v[0:15]
	ds_read_b128 v[160:163], v192 offset:24576
	v_add_f32_e32 v215, 1.0, v215
	v_rcp_f32_e32 v200, v200
	v_mfma_f32_32x32x16_f16 v[16:31], a[32:35], v[164:167], v[16:31]
	ds_read_b128 v[164:167], v192 offset:25600
	v_rcp_f32_e32 v201, v201
	s_waitcnt lgkmcnt(2)
	v_mfma_f32_32x32x16_f16 v[0:15], a[36:39], v[168:171], v[0:15]
	ds_read_b128 v[168:171], v192 offset:26624
	v_rcp_f32_e32 v202, v202
	v_mfma_f32_32x32x16_f16 v[16:31], a[36:39], v[172:175], v[16:31]
	ds_read_b128 v[172:175], v192 offset:27648
	global_load_lds_dwordx4 v192, s[44:45] offset:1024 sc1
	v_rcp_f32_e32 v203, v203
	v_mfma_f32_32x32x16_f16 v[0:15], a[40:43], v[176:179], v[0:15]
	ds_read_b128 v[176:179], v192 offset:28672
	v_rcp_f32_e32 v204, v204
	v_mfma_f32_32x32x16_f16 v[16:31], a[40:43], v[180:183], v[16:31]
	ds_read_b128 v[180:183], v192 offset:29696
	v_rcp_f32_e32 v205, v205
	v_mul_f32_e32 v204, v204, v152
	v_mfma_f32_32x32x16_f16 v[0:15], a[44:47], v[184:187], v[0:15]
	ds_read_b128 v[184:187], v192 offset:30720
	v_rcp_f32_e32 v206, v206
	v_mul_f32_e32 v205, v205, v153
	v_mfma_f32_32x32x16_f16 v[16:31], a[44:47], v[188:191], v[16:31]
	ds_read_b128 v[188:191], v192 offset:31744
	global_load_lds_dwordx4 v192, s[44:45] offset:2048 sc1
	v_rcp_f32_e32 v207, v207
	v_mul_f32_e32 v206, v206, v154
	s_waitcnt vmcnt(10)
	s_barrier
	s_waitcnt lgkmcnt(2)
	v_mfma_f32_32x32x16_f16 v[0:15], a[48:51], v[160:163], v[0:15]
	ds_read_b128 v[160:163], v192 offset:32768
	v_rcp_f32_e32 v208, v208
	v_mul_f32_e32 v207, v207, v155
	v_mfma_f32_32x32x16_f16 v[16:31], a[48:51], v[164:167], v[16:31]
	ds_read_b128 v[164:167], v192 offset:33792
	v_rcp_f32_e32 v209, v209
	v_fmamk_f32 v208, v208, 0xc0b8aa3b, v198
	v_mfma_f32_32x32x16_f16 v[0:15], a[52:55], v[168:171], v[0:15]
	ds_read_b128 v[168:171], v192 offset:34816
	v_rcp_f32_e32 v210, v210
	v_fmamk_f32 v209, v209, 0xc0b8aa3b, v198
	v_fma_f32 v152, v200, v208, v204
	v_mfma_f32_32x32x16_f16 v[16:31], a[52:55], v[172:175], v[16:31]
	ds_read_b128 v[172:175], v192 offset:35840
	global_load_lds_dwordx4 v192, s[44:45] offset:3072 sc1
	v_rcp_f32_e32 v211, v211
	v_fmamk_f32 v210, v210, 0xc0b8aa3b, v198
	v_fma_f32 v153, v201, v209, v205
	v_mfma_f32_32x32x16_f16 v[0:15], a[56:59], v[176:179], v[0:15]
	ds_read_b128 v[176:179], v192 offset:36864
	v_rcp_f32_e32 v212, v212
	v_fmamk_f32 v211, v211, 0xc0b8aa3b, v198
	v_fma_f32 v154, v202, v210, v206
	v_mfma_f32_32x32x16_f16 v[16:31], a[56:59], v[180:183], v[16:31]
	ds_read_b128 v[180:183], v192 offset:37888
	v_rcp_f32_e32 v213, v213
	v_fma_f32 v155, v203, v211, v207
	s_waitcnt lgkmcnt(2)
	v_mfma_f32_32x32x16_f16 v[0:15], a[60:63], v[184:187], v[0:15]
	ds_read_b128 v[184:187], v192 offset:38912
	v_rcp_f32_e32 v214, v214
	v_mfma_f32_32x32x16_f16 v[16:31], a[60:63], v[188:191], v[16:31]
	ds_read_b128 v[188:191], v192 offset:39936
	s_mov_b32 m0, s58
	s_add_u32 s44, s34, 0x18000
	s_addc_u32 s45, s35, 0
	global_load_lds_dwordx4 v192, s[44:45] sc1
	v_rcp_f32_e32 v215, v215
	v_mfma_f32_32x32x16_f16 v[0:15], a[64:67], v[160:163], v[0:15]
	ds_read_b128 v[160:163], v192 offset:40960
	v_exp_f32_e32 v200, v152
	v_mfma_f32_32x32x16_f16 v[16:31], a[64:67], v[164:167], v[16:31]
	ds_read_b128 v[164:167], v192 offset:41984
	v_exp_f32_e32 v201, v153
	v_add_f32_e32 v200, 1.0, v200
	v_mfma_f32_32x32x16_f16 v[0:15], a[68:71], v[168:171], v[0:15]
	ds_read_b128 v[168:171], v192 offset:43008
	v_exp_f32_e32 v202, v154
	v_add_f32_e32 v201, 1.0, v201
	v_mfma_f32_32x32x16_f16 v[16:31], a[68:71], v[172:175], v[16:31]
	ds_read_b128 v[172:175], v192 offset:44032
	global_load_lds_dwordx4 v192, s[44:45] offset:1024 sc1
	v_exp_f32_e32 v203, v155
	v_add_f32_e32 v202, 1.0, v202
	s_waitcnt lgkmcnt(2)
	v_mfma_f32_32x32x16_f16 v[0:15], a[72:75], v[176:179], v[0:15]
	ds_read_b128 v[176:179], v192 offset:45056
	v_add_f32_e32 v203, 1.0, v203
	v_rcp_f32_e32 v200, v200
	v_mfma_f32_32x32x16_f16 v[16:31], a[72:75], v[180:183], v[16:31]
	ds_read_b128 v[180:183], v192 offset:46080
	v_rcp_f32_e32 v201, v201
	v_fma_f32 v200, v200, 2.0, -1.0
	v_mfma_f32_32x32x16_f16 v[0:15], a[76:79], v[184:187], v[0:15]
	ds_read_b128 v[184:187], v192 offset:47104
	v_rcp_f32_e32 v202, v202
	v_fma_f32 v201, v201, 2.0, -1.0
	v_mul_f32_e32 v216, v212, v200
	v_mfma_f32_32x32x16_f16 v[16:31], a[76:79], v[188:191], v[16:31]
	ds_read_b128 v[188:191], v192 offset:48128
	global_load_lds_dwordx4 v192, s[44:45] offset:2048 sc1
	v_rcp_f32_e32 v203, v203
	v_fma_f32 v202, v202, 2.0, -1.0
	v_mul_f32_e32 v217, v213, v201
	v_mfma_f32_32x32x16_f16 v[0:15], a[80:83], v[160:163], v[0:15]
	ds_read_b128 v[160:163], v192 offset:49152
	v_fma_f32 v203, v203, 2.0, -1.0
	v_mul_f32_e32 v218, v214, v202
	v_exp_f32_e32 v200, v112
	v_mfma_f32_32x32x16_f16 v[16:31], a[80:83], v[164:167], v[16:31]
	ds_read_b128 v[164:167], v192 offset:50176
	v_mul_f32_e32 v219, v215, v203
	v_cvt_pk_f16_f32 v220, v216, v217
	v_exp_f32_e32 v201, v113
	s_waitcnt lgkmcnt(2)
	v_mfma_f32_32x32x16_f16 v[0:15], a[84:87], v[168:171], v[0:15]
	ds_read_b128 v[168:171], v192 offset:51200
	v_cvt_pk_f16_f32 v221, v218, v219
	v_exp_f32_e32 v202, v114
	v_add_f32_e32 v200, 1.0, v200
	v_mfma_f32_32x32x16_f16 v[16:31], a[84:87], v[172:175], v[16:31]
	ds_read_b128 v[172:175], v192 offset:52224
	global_load_lds_dwordx4 v192, s[44:45] offset:3072 sc1
	v_exp_f32_e32 v203, v115
	v_add_f32_e32 v201, 1.0, v201
	v_add_f32_e32 v202, 1.0, v202
	v_mfma_f32_32x32x16_f16 v[0:15], a[88:91], v[176:179], v[0:15]
	ds_read_b128 v[176:179], v192 offset:53248
	v_exp_f32_e32 v204, v116
	v_add_f32_e32 v203, 1.0, v203
	v_mfma_f32_32x32x16_f16 v[16:31], a[88:91], v[180:183], v[16:31]
	ds_read_b128 v[180:183], v192 offset:54272
	v_exp_f32_e32 v205, v117
	v_add_f32_e32 v204, 1.0, v204
	v_mfma_f32_32x32x16_f16 v[0:15], a[92:95], v[184:187], v[0:15]
	ds_read_b128 v[184:187], v192 offset:55296
	v_exp_f32_e32 v206, v118
	v_add_f32_e32 v205, 1.0, v205
	v_mfma_f32_32x32x16_f16 v[16:31], a[92:95], v[188:191], v[16:31]
	ds_read_b128 v[188:191], v192 offset:56320
	s_mov_b32 m0, s59
	s_add_u32 s44, s34, 0x19000
	s_addc_u32 s45, s35, 0
	global_load_lds_dwordx4 v192, s[44:45] sc1
	v_exp_f32_e32 v207, v119
	v_add_f32_e32 v206, 1.0, v206
	s_waitcnt lgkmcnt(2)
	v_mfma_f32_32x32x16_f16 v[0:15], a[96:99], v[160:163], v[0:15]
	ds_read_b128 v[160:163], v192 offset:57344
	v_exp_f32_e32 v208, v120
	v_add_f32_e32 v207, 1.0, v207
	v_mfma_f32_32x32x16_f16 v[16:31], a[96:99], v[164:167], v[16:31]
	ds_read_b128 v[164:167], v192 offset:58368
	v_exp_f32_e32 v209, v121
	v_add_f32_e32 v208, 1.0, v208
	v_mfma_f32_32x32x16_f16 v[0:15], a[100:103], v[168:171], v[0:15]
	ds_read_b128 v[168:171], v192 offset:59392
	v_exp_f32_e32 v210, v122
	v_add_f32_e32 v209, 1.0, v209
	v_mfma_f32_32x32x16_f16 v[16:31], a[100:103], v[172:175], v[16:31]
	ds_read_b128 v[172:175], v192 offset:60416
	global_load_lds_dwordx4 v192, s[44:45] offset:1024 sc1
	v_exp_f32_e32 v211, v123
	v_add_f32_e32 v210, 1.0, v210
	v_mfma_f32_32x32x16_f16 v[0:15], a[104:107], v[176:179], v[0:15]
	ds_read_b128 v[176:179], v192 offset:61440
	v_exp_f32_e32 v212, v124
	v_add_f32_e32 v211, 1.0, v211
	v_mfma_f32_32x32x16_f16 v[16:31], a[104:107], v[180:183], v[16:31]
	ds_read_b128 v[180:183], v192 offset:62464
	v_exp_f32_e32 v213, v125
	v_add_f32_e32 v212, 1.0, v212
	s_waitcnt lgkmcnt(2)
	v_mfma_f32_32x32x16_f16 v[0:15], a[108:111], v[184:187], v[0:15]
	ds_read_b128 v[184:187], v192 offset:63488
	v_exp_f32_e32 v214, v126
	v_add_f32_e32 v213, 1.0, v213
	v_mfma_f32_32x32x16_f16 v[16:31], a[108:111], v[188:191], v[16:31]
	ds_read_b128 v[188:191], v192 offset:64512
	global_load_lds_dwordx4 v192, s[44:45] offset:2048 sc1
	v_exp_f32_e32 v215, v127
	v_add_f32_e32 v214, 1.0, v214
	s_waitcnt vmcnt(7)
	s_barrier
	v_mfma_f32_32x32x16_f16 v[0:15], a[112:115], v[160:163], v[0:15]
	ds_read_b128 v[160:163], v193 offset:0
	v_add_f32_e32 v215, 1.0, v215
	v_rcp_f32_e32 v200, v200
	v_mfma_f32_32x32x16_f16 v[16:31], a[112:115], v[164:167], v[16:31]
	ds_read_b128 v[164:167], v193 offset:1024
	v_rcp_f32_e32 v201, v201
	v_mfma_f32_32x32x16_f16 v[0:15], a[116:119], v[168:171], v[0:15]
	ds_read_b128 v[168:171], v193 offset:2048
	v_rcp_f32_e32 v202, v202
	v_mfma_f32_32x32x16_f16 v[16:31], a[116:119], v[172:175], v[16:31]
	ds_read_b128 v[172:175], v193 offset:3072
	global_load_lds_dwordx4 v192, s[44:45] offset:3072 sc1
	v_rcp_f32_e32 v203, v203
	s_waitcnt lgkmcnt(2)
	v_mfma_f32_32x32x16_f16 v[0:15], a[120:123], v[176:179], v[0:15]
	ds_read_b128 v[176:179], v193 offset:4096
	v_rcp_f32_e32 v204, v204
	v_mfma_f32_32x32x16_f16 v[16:31], a[120:123], v[180:183], v[16:31]
	ds_read_b128 v[180:183], v193 offset:5120
	v_rcp_f32_e32 v205, v205
	v_mul_f32_e32 v204, v204, v156
	v_mfma_f32_32x32x2_f32 v[64:79], v248, v228, v[232:247]
	v_mfma_f32_32x32x16_f16 v[0:15], a[124:127], v[184:187], v[0:15]
	ds_read_b128 v[184:187], v193 offset:6144
	v_rcp_f32_e32 v206, v206
	v_mul_f32_e32 v205, v205, v157
	v_mfma_f32_32x32x2_f32 v[80:95], v248, v229, v[232:247]
	v_mfma_f32_32x32x16_f16 v[16:31], a[124:127], v[188:191], v[16:31]
	ds_read_b128 v[188:191], v193 offset:7168
	v_cmp_gt_u32_e32 vcc, 2, v251
	s_cbranch_vccnz .LE_tpoll21
.LE_tok20:
	s_and_b32 s64, s71, 1
	s_lshl_b32 s64, s64, 22
	s_add_u32 s64, s64, s49
	s_add_u32 s64, s64, 0x20000
	s_add_u32 s34, s6, s64
	s_addc_u32 s35, s7, 0
	s_mov_b32 m0, s52
	s_add_u32 s44, s34, 0x0
	s_addc_u32 s45, s35, 0
	global_load_lds_dwordx4 v192, s[44:45] sc1
	v_rcp_f32_e32 v207, v207
	v_mul_f32_e32 v206, v206, v158
	v_mfma_f32_32x32x16_f16 v[0:15], a[128:131], v[160:163], v[0:15]
	ds_read_b128 v[160:163], v193 offset:8192
	v_rcp_f32_e32 v208, v208
	v_mul_f32_e32 v207, v207, v159
	v_mfma_f32_32x32x16_f16 v[16:31], a[128:131], v[164:167], v[16:31]
	ds_read_b128 v[164:167], v193 offset:9216
	v_rcp_f32_e32 v209, v209
	v_fmamk_f32 v208, v208, 0xc0b8aa3b, v198
	s_waitcnt lgkmcnt(2)
	v_mfma_f32_32x32x16_f16 v[0:15], a[132:135], v[168:171], v[0:15]
	ds_read_b128 v[168:171], v193 offset:10240
	v_rcp_f32_e32 v210, v210
	v_fmamk_f32 v209, v209, 0xc0b8aa3b, v198
	v_fma_f32 v156, v200, v208, v204
	v_mfma_f32_32x32x16_f16 v[16:31], a[132:135], v[172:175], v[16:31]
	ds_read_b128 v[172:175], v193 offset:11264
	global_load_lds_dwordx4 v192, s[44:45] offset:1024 sc1
	v_rcp_f32_e32 v211, v211
	v_fmamk_f32 v210, v210, 0xc0b8aa3b, v198
	v_fma_f32 v157, v201, v209, v205
	v_mfma_f32_32x32x16_f16 v[0:15], a[136:139], v[176:179], v[0:15]
	ds_read_b128 v[176:179], v193 offset:12288
	v_rcp_f32_e32 v212, v212
	v_fmamk_f32 v211, v211, 0xc0b8aa3b, v198
	v_fma_f32 v158, v202, v210, v206
	v_mfma_f32_32x32x16_f16 v[16:31], a[136:139], v[180:183], v[16:31]
	ds_read_b128 v[180:183], v193 offset:13312
	v_rcp_f32_e32 v213, v213
	v_fma_f32 v159, v203, v211, v207
	v_mfma_f32_32x32x16_f16 v[0:15], a[140:143], v[184:187], v[0:15]
	ds_read_b128 v[184:187], v193 offset:14336
	v_rcp_f32_e32 v214, v214
	v_mfma_f32_32x32x16_f16 v[16:31], a[140:143], v[188:191], v[16:31]
	ds_read_b128 v[188:191], v193 offset:15360
	global_load_lds_dwordx4 v192, s[44:45] offset:2048 sc1
	v_rcp_f32_e32 v215, v215
	s_waitcnt lgkmcnt(2)
	v_mfma_f32_32x32x16_f16 v[0:15], a[144:147], v[160:163], v[0:15]
	ds_read_b128 v[160:163], v193 offset:16384
	v_exp_f32_e32 v200, v156
	v_mfma_f32_32x32x16_f16 v[16:31], a[144:147], v[164:167], v[16:31]
	ds_read_b128 v[164:167], v193 offset:17408
	v_exp_f32_e32 v201, v157
	v_add_f32_e32 v200, 1.0, v200
	v_mfma_f32_32x32x16_f16 v[0:15], a[148:151], v[168:171], v[0:15]
	ds_read_b128 v[168:171], v193 offset:18432
	v_exp_f32_e32 v202, v158
	v_add_f32_e32 v201, 1.0, v201
	v_mfma_f32_32x32x16_f16 v[16:31], a[148:151], v[172:175], v[16:31]
	ds_read_b128 v[172:175], v193 offset:19456
	global_load_lds_dwordx4 v192, s[44:45] offset:3072 sc1
	v_exp_f32_e32 v203, v159
	v_add_f32_e32 v202, 1.0, v202
	v_mfma_f32_32x32x16_f16 v[0:15], a[152:155], v[176:179], v[0:15]
	ds_read_b128 v[176:179], v193 offset:20480
	v_add_f32_e32 v203, 1.0, v203
	v_rcp_f32_e32 v200, v200
	v_mfma_f32_32x32x16_f16 v[16:31], a[152:155], v[180:183], v[16:31]
	ds_read_b128 v[180:183], v193 offset:21504
	v_rcp_f32_e32 v201, v201
	v_fma_f32 v200, v200, 2.0, -1.0
	s_waitcnt lgkmcnt(2)
	v_mfma_f32_32x32x16_f16 v[0:15], a[156:159], v[184:187], v[0:15]
	ds_read_b128 v[184:187], v193 offset:22528
	v_rcp_f32_e32 v202, v202
	v_fma_f32 v201, v201, 2.0, -1.0
	v_mul_f32_e32 v216, v212, v200
	v_mfma_f32_32x32x16_f16 v[16:31], a[156:159], v[188:191], v[16:31]
	ds_read_b128 v[188:191], v193 offset:23552
	s_mov_b32 m0, s53
	s_add_u32 s44, s34, 0x1000
	s_addc_u32 s45, s35, 0
	global_load_lds_dwordx4 v192, s[44:45] sc1
	v_rcp_f32_e32 v203, v203
	v_fma_f32 v202, v202, 2.0, -1.0
	v_mul_f32_e32 v217, v213, v201
	v_mfma_f32_32x32x16_f16 v[0:15], a[160:163], v[160:163], v[0:15]
	ds_read_b128 v[160:163], v193 offset:24576
	v_fma_f32 v203, v203, 2.0, -1.0
	v_mul_f32_e32 v218, v214, v202
	v_mfma_f32_32x32x16_f16 v[16:31], a[160:163], v[164:167], v[16:31]
	ds_read_b128 v[164:167], v193 offset:25600
	v_mul_f32_e32 v219, v215, v203
	v_cvt_pk_f16_f32 v222, v216, v217
	v_mfma_f32_32x32x16_f16 v[0:15], a[164:167], v[168:171], v[0:15]
	ds_read_b128 v[168:171], v193 offset:26624
	v_cvt_pk_f16_f32 v223, v218, v219
	v_mfma_f32_32x32x16_f16 v[16:31], a[164:167], v[172:175], v[16:31]
	ds_read_b128 v[172:175], v193 offset:27648
	global_load_lds_dwordx4 v192, s[44:45] offset:1024 sc1
	s_nop 1
	v_permlane32_swap_b32_e32 v220, v222
	v_permlane32_swap_b32_e32 v221, v223
	s_cmp_eq_u32 s31, 0
	s_cbranch_scc1 .LE_slow22
	global_store_dwordx4 v195, v[220:223], s[36:37] offset:0
.LE_join23:
	s_waitcnt lgkmcnt(2)
	v_mfma_f32_32x32x16_f16 v[0:15], a[168:171], v[176:179], v[0:15]
	ds_read_b128 v[176:179], v193 offset:28672
	v_mfma_f32_32x32x16_f16 v[16:31], a[168:171], v[180:183], v[16:31]
	ds_read_b128 v[180:183], v193 offset:29696
	v_mfma_f32_32x32x16_f16 v[0:15], a[172:175], v[184:187], v[0:15]
	ds_read_b128 v[184:187], v193 offset:30720
	v_mfma_f32_32x32x16_f16 v[16:31], a[172:175], v[188:191], v[16:31]
	ds_read_b128 v[188:191], v193 offset:31744
	global_load_lds_dwordx4 v192, s[44:45] offset:2048 sc1
	s_waitcnt vmcnt(8)
	s_barrier
	v_mfma_f32_32x32x16_f16 v[0:15], a[176:179], v[160:163], v[0:15]
	ds_read_b128 v[160:163], v193 offset:32768
	v_mfma_f32_32x32x16_f16 v[16:31], a[176:179], v[164:167], v[16:31]
	ds_read_b128 v[164:167], v193 offset:33792
	s_waitcnt lgkmcnt(2)
	v_mfma_f32_32x32x16_f16 v[0:15], a[180:183], v[168:171], v[0:15]
	ds_read_b128 v[168:171], v193 offset:34816
	v_mfma_f32_32x32x16_f16 v[16:31], a[180:183], v[172:175], v[16:31]
	ds_read_b128 v[172:175], v193 offset:35840
	global_load_lds_dwordx4 v192, s[44:45] offset:3072 sc1
	v_mfma_f32_32x32x16_f16 v[0:15], a[184:187], v[176:179], v[0:15]
	ds_read_b128 v[176:179], v193 offset:36864
	v_mfma_f32_32x32x16_f16 v[16:31], a[184:187], v[180:183], v[16:31]
	ds_read_b128 v[180:183], v193 offset:37888
	v_mfma_f32_32x32x16_f16 v[0:15], a[188:191], v[184:187], v[0:15]
	ds_read_b128 v[184:187], v193 offset:38912
	v_mfma_f32_32x32x16_f16 v[16:31], a[188:191], v[188:191], v[16:31]
	ds_read_b128 v[188:191], v193 offset:39936
	s_mov_b32 m0, s54
	s_add_u32 s44, s34, 0x8000
	s_addc_u32 s45, s35, 0
	global_load_lds_dwordx4 v192, s[44:45] sc1
	s_waitcnt lgkmcnt(2)
	v_mfma_f32_32x32x16_f16 v[0:15], a[192:195], v[160:163], v[0:15]
	ds_read_b128 v[160:163], v193 offset:40960
	s_waitcnt vmcnt(3)
	s_barrier
	v_mov_b32_e32 v199, 4
	s_cmp_eq_u32 s31, 0
	s_cbranch_scc1 .LE_slow24
	global_store_dword v197, v199, s[40:41]
.LE_join25:
	v_mfma_f32_32x32x16_f16 v[16:31], a[192:195], v[164:167], v[16:31]
	ds_read_b128 v[164:167], v193 offset:41984
	v_mfma_f32_32x32x16_f16 v[0:15], a[196:199], v[168:171], v[0:15]
	ds_read_b128 v[168:171], v193 offset:43008
	v_mfma_f32_32x32x16_f16 v[16:31], a[196:199], v[172:175], v[16:31]
	ds_read_b128 v[172:175], v193 offset:44032
	global_load_lds_dwordx4 v192, s[44:45] offset:1024 sc1
	v_mfma_f32_32x32x16_f16 v[0:15], a[200:203], v[176:179], v[0:15]
	ds_read_b128 v[176:179], v193 offset:45056
	s_and_b32 s64, s33, 1
	s_lshl_b32 s64, s64, 22
	s_add_u32 s64, s64, s50
	s_add_u32 s36, s6, s64
	s_addc_u32 s37, s7, 0
	s_lshl_b32 s64, s33, 3
	s_add_u32 s64, s64, s29
	s_lshl_b32 s64, s64, 5
	s_add_u32 s64, s64, s30
	s_lshl_b32 s64, s64, 2
	s_add_u32 s40, s8, s64
	s_addc_u32 s41, s9, 0
	s_lshl_b32 s64, s33, 11
	s_lshl_b32 s65, s29, 8
	s_add_u32 s64, s64, s65
	s_add_u32 s64, s64, 192
	s_lshl_b32 s64, s64, 3
	s_add_u32 s42, s12, s64
	s_addc_u32 s43, s13, 0
	v_mfma_f32_32x32x16_f16 v[16:31], a[200:203], v[180:183], v[16:31]
	ds_read_b128 v[180:183], v193 offset:46080
	s_waitcnt lgkmcnt(2)
	v_mfma_f32_32x32x16_f16 v[0:15], a[204:207], v[184:187], v[0:15]
	ds_read_b128 v[184:187], v193 offset:47104
	v_mfma_f32_32x32x16_f16 v[16:31], a[204:207], v[188:191], v[16:31]
	ds_read_b128 v[188:191], v193 offset:48128
	global_load_lds_dwordx4 v192, s[44:45] offset:2048 sc1
	v_mfma_f32_32x32x16_f16 v[0:15], a[208:211], v[160:163], v[0:15]
	ds_read_b128 v[160:163], v193 offset:49152
	v_mfma_f32_32x32x16_f16 v[16:31], a[208:211], v[164:167], v[16:31]
	ds_read_b128 v[164:167], v193 offset:50176
	v_mfma_f32_32x32x16_f16 v[0:15], a[212:215], v[168:171], v[0:15]
	ds_read_b128 v[168:171], v193 offset:51200
	v_mfma_f32_32x32x16_f16 v[16:31], a[212:215], v[172:175], v[16:31]
	ds_read_b128 v[172:175], v193 offset:52224
	global_load_lds_dwordx4 v192, s[44:45] offset:3072 sc1
	s_waitcnt lgkmcnt(2)
	v_mfma_f32_32x32x16_f16 v[0:15], a[216:219], v[176:179], v[0:15]
	ds_read_b128 v[176:179], v193 offset:53248
	v_mfma_f32_32x32x16_f16 v[16:31], a[216:219], v[180:183], v[16:31]
	ds_read_b128 v[180:183], v193 offset:54272
	v_mfma_f32_32x32x16_f16 v[0:15], a[220:223], v[184:187], v[0:15]
	ds_read_b128 v[184:187], v193 offset:55296
	v_mfma_f32_32x32x16_f16 v[16:31], a[220:223], v[188:191], v[16:31]
	ds_read_b128 v[188:191], v193 offset:56320
	s_mov_b32 m0, s55
	s_add_u32 s44, s34, 0x9000
	s_addc_u32 s45, s35, 0
	global_load_lds_dwordx4 v192, s[44:45] sc1
	v_mfma_f32_32x32x16_f16 v[0:15], a[224:227], v[160:163], v[0:15]
	ds_read_b128 v[160:163], v193 offset:57344
	v_mfma_f32_32x32x16_f16 v[16:31], a[224:227], v[164:167], v[16:31]
	ds_read_b128 v[164:167], v193 offset:58368
	s_waitcnt lgkmcnt(2)
	v_mfma_f32_32x32x16_f16 v[0:15], a[228:231], v[168:171], v[0:15]
	ds_read_b128 v[168:171], v193 offset:59392
	v_mfma_f32_32x32x16_f16 v[16:31], a[228:231], v[172:175], v[16:31]
	ds_read_b128 v[172:175], v193 offset:60416
	global_load_lds_dwordx4 v192, s[44:45] offset:1024 sc1
	v_mfma_f32_32x32x16_f16 v[0:15], a[232:235], v[176:179], v[0:15]
	ds_read_b128 v[176:179], v193 offset:61440
	v_mfma_f32_32x32x16_f16 v[16:31], a[232:235], v[180:183], v[16:31]
	ds_read_b128 v[180:183], v193 offset:62464
	v_mfma_f32_32x32x16_f16 v[0:15], a[236:239], v[184:187], v[0:15]
	ds_read_b128 v[184:187], v193 offset:63488
	v_mfma_f32_32x32x16_f16 v[16:31], a[236:239], v[188:191], v[16:31]
	ds_read_b128 v[188:191], v193 offset:64512
	global_load_lds_dwordx4 v192, s[44:45] offset:2048 sc1
	s_waitcnt vmcnt(8)
	s_barrier
	s_waitcnt lgkmcnt(2)
	v_mfma_f32_32x32x16_f16 v[0:15], a[240:243], v[160:163], v[0:15]
	ds_read_b128 v[160:163], v192 offset:0
	v_mfma_f32_32x32x16_f16 v[16:31], a[240:243], v[164:167], v[16:31]
	ds_read_b128 v[164:167], v192 offset:1024
	v_mfma_f32_32x32x16_f16 v[0:15], a[244:247], v[168:171], v[0:15]
	ds_read_b128 v[168:171], v192 offset:2048
	v_mfma_f32_32x32x16_f16 v[16:31], a[244:247], v[172:175], v[16:31]
	ds_read_b128 v[172:175], v192 offset:3072
	global_load_lds_dwordx4 v192, s[44:45] offset:3072 sc1
	v_mfma_f32_32x32x16_f16 v[0:15], a[248:251], v[176:179], v[0:15]
	ds_read_b128 v[176:179], v192 offset:4096
	v_mfma_f32_32x32x16_f16 v[16:31], a[248:251], v[180:183], v[16:31]
	ds_read_b128 v[180:183], v192 offset:5120
	s_waitcnt lgkmcnt(2)
	v_mfma_f32_32x32x16_f16 v[0:15], a[252:255], v[184:187], v[0:15]
	ds_read_b128 v[184:187], v192 offset:6144
	v_mfma_f32_32x32x16_f16 v[16:31], a[252:255], v[188:191], v[16:31]
	ds_read_b128 v[188:191], v192 offset:7168
	s_mov_b32 m0, s56
	s_add_u32 s44, s34, 0x10000
	s_addc_u32 s45, s35, 0
	global_load_lds_dwordx4 v192, s[44:45] sc1
	s_nop 3
	global_load_dword v228, v249, s[42:43] offset:0
	global_load_dword v229, v249, s[42:43] offset:256
	s_waitcnt lgkmcnt(2)
	v_mfma_f32_32x32x16_f16 v[32:47], a[0:3], v[160:163], v[32:47]
	ds_read_b128 v[160:163], v192 offset:8192
	v_exp_f32_e32 v200, v0
	v_mfma_f32_32x32x16_f16 v[48:63], a[0:3], v[164:167], v[48:63]
	ds_read_b128 v[164:167], v192 offset:9216
	s_lshl_b32 s64, s71, 3
	s_add_u32 s64, s64, s29
	s_lshl_b32 s64, s64, 7
	s_add_u32 s38, s8, s64
	s_addc_u32 s39, s9, 0
	global_load_dword v251, v196, s[38:39] sc1
	v_exp_f32_e32 v201, v1
	v_add_f32_e32 v200, 1.0, v200
	v_mfma_f32_32x32x16_f16 v[32:47], a[4:7], v[168:171], v[32:47]
	ds_read_b128 v[168:171], v192 offset:10240
	v_exp_f32_e32 v202, v2
	v_add_f32_e32 v201, 1.0, v201
	v_mfma_f32_32x32x16_f16 v[48:63], a[4:7], v[172:175], v[48:63]
	ds_read_b128 v[172:175], v192 offset:11264
	global_load_lds_dwordx4 v192, s[44:45] offset:1024 sc1
	v_exp_f32_e32 v203, v3
	v_add_f32_e32 v202, 1.0, v202
	v_mfma_f32_32x32x16_f16 v[32:47], a[8:11], v[176:179], v[32:47]
	ds_read_b128 v[176:179], v192 offset:12288
	v_exp_f32_e32 v204, v4
	v_add_f32_e32 v203, 1.0, v203
	v_mfma_f32_32x32x16_f16 v[48:63], a[8:11], v[180:183], v[48:63]
	ds_read_b128 v[180:183], v192 offset:13312
	v_exp_f32_e32 v205, v5
	v_add_f32_e32 v204, 1.0, v204
	s_waitcnt lgkmcnt(2)
	v_mfma_f32_32x32x16_f16 v[32:47], a[12:15], v[184:187], v[32:47]
	ds_read_b128 v[184:187], v192 offset:14336
	v_exp_f32_e32 v206, v6
	v_add_f32_e32 v205, 1.0, v205
	v_mfma_f32_32x32x16_f16 v[48:63], a[12:15], v[188:191], v[48:63]
	ds_read_b128 v[188:191], v192 offset:15360
	global_load_lds_dwordx4 v192, s[44:45] offset:2048 sc1
	v_exp_f32_e32 v207, v7
	v_add_f32_e32 v206, 1.0, v206
	v_mfma_f32_32x32x16_f16 v[32:47], a[16:19], v[160:163], v[32:47]
	ds_read_b128 v[160:163], v192 offset:16384
	v_exp_f32_e32 v208, v8
	v_add_f32_e32 v207, 1.0, v207
	v_mfma_f32_32x32x16_f16 v[48:63], a[16:19], v[164:167], v[48:63]
	ds_read_b128 v[164:167], v192 offset:17408
	v_exp_f32_e32 v209, v9
	v_add_f32_e32 v208, 1.0, v208
	v_mfma_f32_32x32x16_f16 v[32:47], a[20:23], v[168:171], v[32:47]
	ds_read_b128 v[168:171], v192 offset:18432
	v_exp_f32_e32 v210, v10
	v_add_f32_e32 v209, 1.0, v209
	v_mfma_f32_32x32x16_f16 v[48:63], a[20:23], v[172:175], v[48:63]
	ds_read_b128 v[172:175], v192 offset:19456
	global_load_lds_dwordx4 v192, s[44:45] offset:3072 sc1
	v_exp_f32_e32 v211, v11
	v_add_f32_e32 v210, 1.0, v210
	s_waitcnt lgkmcnt(2)
	v_mfma_f32_32x32x16_f16 v[32:47], a[24:27], v[176:179], v[32:47]
	ds_read_b128 v[176:179], v192 offset:20480
	v_exp_f32_e32 v212, v12
	v_add_f32_e32 v211, 1.0, v211
	v_mfma_f32_32x32x16_f16 v[48:63], a[24:27], v[180:183], v[48:63]
	ds_read_b128 v[180:183], v192 offset:21504
	v_exp_f32_e32 v213, v13
	v_add_f32_e32 v212, 1.0, v212
	v_mfma_f32_32x32x16_f16 v[32:47], a[28:31], v[184:187], v[32:47]
	ds_read_b128 v[184:187], v192 offset:22528
	v_exp_f32_e32 v214, v14
	v_add_f32_e32 v213, 1.0, v213
	v_mfma_f32_32x32x16_f16 v[48:63], a[28:31], v[188:191], v[48:63]
	ds_read_b128 v[188:191], v192 offset:23552
	s_mov_b32 m0, s57
	s_add_u32 s44, s34, 0x11000
	s_addc_u32 s45, s35, 0
	global_load_lds_dwordx4 v192, s[44:45] sc1
	v_exp_f32_e32 v215, v15
	v_add_f32_e32 v214, 1.0, v214
	v_mfma_f32_32x32x16_f16 v[32:47], a[32:35], v[160:163], v[32:47]
	ds_read_b128 v[160:163], v192 offset:24576
	v_add_f32_e32 v215, 1.0, v215
	v_rcp_f32_e32 v200, v200
	v_mfma_f32_32x32x16_f16 v[48:63], a[32:35], v[164:167], v[48:63]
	ds_read_b128 v[164:167], v192 offset:25600
	v_rcp_f32_e32 v201, v201
	s_waitcnt lgkmcnt(2)
	v_mfma_f32_32x32x16_f16 v[32:47], a[36:39], v[168:171], v[32:47]
	ds_read_b128 v[168:171], v192 offset:26624
	v_rcp_f32_e32 v202, v202
	v_mfma_f32_32x32x16_f16 v[48:63], a[36:39], v[172:175], v[48:63]
	ds_read_b128 v[172:175], v192 offset:27648
	global_load_lds_dwordx4 v192, s[44:45] offset:1024 sc1
	v_rcp_f32_e32 v203, v203
	v_mfma_f32_32x32x16_f16 v[32:47], a[40:43], v[176:179], v[32:47]
	ds_read_b128 v[176:179], v192 offset:28672
	v_rcp_f32_e32 v204, v204
	v_mfma_f32_32x32x16_f16 v[48:63], a[40:43], v[180:183], v[48:63]
	ds_read_b128 v[180:183], v192 offset:29696
	v_rcp_f32_e32 v205, v205
	v_mul_f32_e32 v204, v204, v128
	v_mfma_f32_32x32x16_f16 v[32:47], a[44:47], v[184:187], v[32:47]
	ds_read_b128 v[184:187], v192 offset:30720
	v_rcp_f32_e32 v206, v206
	v_mul_f32_e32 v205, v205, v129
	v_mfma_f32_32x32x16_f16 v[48:63], a[44:47], v[188:191], v[48:63]
	ds_read_b128 v[188:191], v192 offset:31744
	global_load_lds_dwordx4 v192, s[44:45] offset:2048 sc1
	v_rcp_f32_e32 v207, v207
	v_mul_f32_e32 v206, v206, v130
	s_waitcnt vmcnt(10)
	s_barrier
	s_waitcnt lgkmcnt(2)
	v_mfma_f32_32x32x16_f16 v[32:47], a[48:51], v[160:163], v[32:47]
	ds_read_b128 v[160:163], v192 offset:32768
	v_rcp_f32_e32 v208, v208
	v_mul_f32_e32 v207, v207, v131
	v_mfma_f32_32x32x16_f16 v[48:63], a[48:51], v[164:167], v[48:63]
	ds_read_b128 v[164:167], v192 offset:33792
	v_rcp_f32_e32 v209, v209
	v_fmamk_f32 v208, v208, 0xc0b8aa3b, v198
	v_mfma_f32_32x32x16_f16 v[32:47], a[52:55], v[168:171], v[32:47]
	ds_read_b128 v[168:171], v192 offset:34816
	v_rcp_f32_e32 v210, v210
	v_fmamk_f32 v209, v209, 0xc0b8aa3b, v198
	v_fma_f32 v128, v200, v208, v204
	v_mfma_f32_32x32x16_f16 v[48:63], a[52:55], v[172:175], v[48:63]
	ds_read_b128 v[172:175], v192 offset:35840
	global_load_lds_dwordx4 v192, s[44:45] offset:3072 sc1
	v_rcp_f32_e32 v211, v211
	v_fmamk_f32 v210, v210, 0xc0b8aa3b, v198
	v_fma_f32 v129, v201, v209, v205
	v_mfma_f32_32x32x16_f16 v[32:47], a[56:59], v[176:179], v[32:47]
	ds_read_b128 v[176:179], v192 offset:36864
	v_rcp_f32_e32 v212, v212
	v_fmamk_f32 v211, v211, 0xc0b8aa3b, v198
	v_fma_f32 v130, v202, v210, v206
	v_mfma_f32_32x32x16_f16 v[48:63], a[56:59], v[180:183], v[48:63]
	ds_read_b128 v[180:183], v192 offset:37888
	v_rcp_f32_e32 v213, v213
	v_fma_f32 v131, v203, v211, v207
	s_waitcnt lgkmcnt(2)
	v_mfma_f32_32x32x16_f16 v[32:47], a[60:63], v[184:187], v[32:47]
	ds_read_b128 v[184:187], v192 offset:38912
	v_rcp_f32_e32 v214, v214
	v_mfma_f32_32x32x16_f16 v[48:63], a[60:63], v[188:191], v[48:63]
	ds_read_b128 v[188:191], v192 offset:39936
	s_mov_b32 m0, s58
	s_add_u32 s44, s34, 0x18000
	s_addc_u32 s45, s35, 0
	global_load_lds_dwordx4 v192, s[44:45] sc1
	v_rcp_f32_e32 v215, v215
	v_mfma_f32_32x32x16_f16 v[32:47], a[64:67], v[160:163], v[32:47]
	ds_read_b128 v[160:163], v192 offset:40960
	v_exp_f32_e32 v200, v128
	v_mfma_f32_32x32x16_f16 v[48:63], a[64:67], v[164:167], v[48:63]
	ds_read_b128 v[164:167], v192 offset:41984
	v_exp_f32_e32 v201, v129
	v_add_f32_e32 v200, 1.0, v200
	v_mfma_f32_32x32x16_f16 v[32:47], a[68:71], v[168:171], v[32:47]
	ds_read_b128 v[168:171], v192 offset:43008
	v_exp_f32_e32 v202, v130
	v_add_f32_e32 v201, 1.0, v201
	v_mfma_f32_32x32x16_f16 v[48:63], a[68:71], v[172:175], v[48:63]
	ds_read_b128 v[172:175], v192 offset:44032
	global_load_lds_dwordx4 v192, s[44:45] offset:1024 sc1
	v_exp_f32_e32 v203, v131
	v_add_f32_e32 v202, 1.0, v202
	s_waitcnt lgkmcnt(2)
	v_mfma_f32_32x32x16_f16 v[32:47], a[72:75], v[176:179], v[32:47]
	ds_read_b128 v[176:179], v192 offset:45056
	v_add_f32_e32 v203, 1.0, v203
	v_rcp_f32_e32 v200, v200
	v_mfma_f32_32x32x16_f16 v[48:63], a[72:75], v[180:183], v[48:63]
	ds_read_b128 v[180:183], v192 offset:46080
	v_rcp_f32_e32 v201, v201
	v_fma_f32 v200, v200, 2.0, -1.0
	v_mfma_f32_32x32x16_f16 v[32:47], a[76:79], v[184:187], v[32:47]
	ds_read_b128 v[184:187], v192 offset:47104
	v_rcp_f32_e32 v202, v202
	v_fma_f32 v201, v201, 2.0, -1.0
	v_mul_f32_e32 v216, v212, v200
	v_mfma_f32_32x32x16_f16 v[48:63], a[76:79], v[188:191], v[48:63]
	ds_read_b128 v[188:191], v192 offset:48128
	global_load_lds_dwordx4 v192, s[44:45] offset:2048 sc1
	v_rcp_f32_e32 v203, v203
	v_fma_f32 v202, v202, 2.0, -1.0
	v_mul_f32_e32 v217, v213, v201
	v_mfma_f32_32x32x16_f16 v[32:47], a[80:83], v[160:163], v[32:47]
	ds_read_b128 v[160:163], v192 offset:49152
	v_fma_f32 v203, v203, 2.0, -1.0
	v_mul_f32_e32 v218, v214, v202
	v_exp_f32_e32 v200, v16
	v_mfma_f32_32x32x16_f16 v[48:63], a[80:83], v[164:167], v[48:63]
	ds_read_b128 v[164:167], v192 offset:50176
	v_mul_f32_e32 v219, v215, v203
	v_cvt_pk_f16_f32 v220, v216, v217
	v_exp_f32_e32 v201, v17
	s_waitcnt lgkmcnt(2)
	v_mfma_f32_32x32x16_f16 v[32:47], a[84:87], v[168:171], v[32:47]
	ds_read_b128 v[168:171], v192 offset:51200
	v_cvt_pk_f16_f32 v221, v218, v219
	v_exp_f32_e32 v202, v18
	v_add_f32_e32 v200, 1.0, v200
	v_mfma_f32_32x32x16_f16 v[48:63], a[84:87], v[172:175], v[48:63]
	ds_read_b128 v[172:175], v192 offset:52224
	global_load_lds_dwordx4 v192, s[44:45] offset:3072 sc1
	s_cmp_eq_u32 s33, s60
	s_cbranch_scc1 .LE_ht26
.LE_htb27:
	v_exp_f32_e32 v203, v19
	v_mfma_f32_32x32x16_f16 v[32:47], a[88:91], v[176:179], v[32:47]
	ds_read_b128 v[176:179], v192 offset:53248
	v_exp_f32_e32 v204, v20
	v_add_f32_e32 v201, 1.0, v201
	v_add_f32_e32 v202, 1.0, v202
	v_mfma_f32_32x32x16_f16 v[48:63], a[88:91], v[180:183], v[48:63]
	ds_read_b128 v[180:183], v192 offset:54272
	v_exp_f32_e32 v205, v21
	v_add_f32_e32 v203, 1.0, v203
	v_add_f32_e32 v204, 1.0, v204
	v_mfma_f32_32x32x16_f16 v[32:47], a[92:95], v[184:187], v[32:47]
	ds_read_b128 v[184:187], v192 offset:55296
	v_exp_f32_e32 v206, v22
	v_add_f32_e32 v205, 1.0, v205
	v_mfma_f32_32x32x16_f16 v[48:63], a[92:95], v[188:191], v[48:63]
	ds_read_b128 v[188:191], v192 offset:56320
	s_mov_b32 m0, s59
	s_add_u32 s44, s34, 0x19000
	s_addc_u32 s45, s35, 0
	global_load_lds_dwordx4 v192, s[44:45] sc1
	v_exp_f32_e32 v207, v23
	v_add_f32_e32 v206, 1.0, v206
	s_waitcnt lgkmcnt(2)
	v_mfma_f32_32x32x16_f16 v[32:47], a[96:99], v[160:163], v[32:47]
	ds_read_b128 v[160:163], v192 offset:57344
	v_exp_f32_e32 v208, v24
	v_add_f32_e32 v207, 1.0, v207
	v_mfma_f32_32x32x16_f16 v[48:63], a[96:99], v[164:167], v[48:63]
	ds_read_b128 v[164:167], v192 offset:58368
	v_exp_f32_e32 v209, v25
	v_add_f32_e32 v208, 1.0, v208
	v_mfma_f32_32x32x16_f16 v[32:47], a[100:103], v[168:171], v[32:47]
	ds_read_b128 v[168:171], v192 offset:59392
	v_exp_f32_e32 v210, v26
	v_add_f32_e32 v209, 1.0, v209
	v_mfma_f32_32x32x16_f16 v[48:63], a[100:103], v[172:175], v[48:63]
	ds_read_b128 v[172:175], v192 offset:60416
	global_load_lds_dwordx4 v192, s[44:45] offset:1024 sc1
	v_exp_f32_e32 v211, v27
	v_add_f32_e32 v210, 1.0, v210
	v_mfma_f32_32x32x16_f16 v[32:47], a[104:107], v[176:179], v[32:47]
	ds_read_b128 v[176:179], v192 offset:61440
	v_exp_f32_e32 v212, v28
	v_add_f32_e32 v211, 1.0, v211
	v_mfma_f32_32x32x16_f16 v[48:63], a[104:107], v[180:183], v[48:63]
	ds_read_b128 v[180:183], v192 offset:62464
	v_exp_f32_e32 v213, v29
	v_add_f32_e32 v212, 1.0, v212
	s_waitcnt lgkmcnt(2)
	v_mfma_f32_32x32x16_f16 v[32:47], a[108:111], v[184:187], v[32:47]
	ds_read_b128 v[184:187], v192 offset:63488
	v_exp_f32_e32 v214, v30
	v_add_f32_e32 v213, 1.0, v213
	v_mfma_f32_32x32x16_f16 v[48:63], a[108:111], v[188:191], v[48:63]
	ds_read_b128 v[188:191], v192 offset:64512
	global_load_lds_dwordx4 v192, s[44:45] offset:2048 sc1
	v_exp_f32_e32 v215, v31
	v_add_f32_e32 v214, 1.0, v214
	s_waitcnt vmcnt(7)
	s_barrier
	v_mfma_f32_32x32x16_f16 v[32:47], a[112:115], v[160:163], v[32:47]
	ds_read_b128 v[160:163], v193 offset:0
	v_add_f32_e32 v215, 1.0, v215
	v_rcp_f32_e32 v200, v200
	v_mfma_f32_32x32x16_f16 v[48:63], a[112:115], v[164:167], v[48:63]
	ds_read_b128 v[164:167], v193 offset:1024
	v_rcp_f32_e32 v201, v201
	v_mfma_f32_32x32x16_f16 v[32:47], a[116:119], v[168:171], v[32:47]
	ds_read_b128 v[168:171], v193 offset:2048
	v_rcp_f32_e32 v202, v202
	v_mfma_f32_32x32x16_f16 v[48:63], a[116:119], v[172:175], v[48:63]
	ds_read_b128 v[172:175], v193 offset:3072
	global_load_lds_dwordx4 v192, s[44:45] offset:3072 sc1
	v_rcp_f32_e32 v203, v203
	s_waitcnt lgkmcnt(2)
	v_mfma_f32_32x32x16_f16 v[32:47], a[120:123], v[176:179], v[32:47]
	ds_read_b128 v[176:179], v193 offset:4096
	v_rcp_f32_e32 v204, v204
	v_mfma_f32_32x32x16_f16 v[48:63], a[120:123], v[180:183], v[48:63]
	ds_read_b128 v[180:183], v193 offset:5120
	v_rcp_f32_e32 v205, v205
	v_mul_f32_e32 v204, v204, v132
	v_mfma_f32_32x32x2_f32 v[96:111], v248, v228, v[232:247]
	v_mfma_f32_32x32x16_f16 v[32:47], a[124:127], v[184:187], v[32:47]
	ds_read_b128 v[184:187], v193 offset:6144
	v_rcp_f32_e32 v206, v206
	v_mul_f32_e32 v205, v205, v133
	v_mfma_f32_32x32x2_f32 v[112:127], v248, v229, v[232:247]
	v_mfma_f32_32x32x16_f16 v[48:63], a[124:127], v[188:191], v[48:63]
	ds_read_b128 v[188:191], v193 offset:7168
	v_cmp_gt_u32_e32 vcc, 3, v251
	s_cbranch_vccnz .LE_tpoll29
.LE_tok28:
	s_and_b32 s64, s71, 1
	s_lshl_b32 s64, s64, 22
	s_add_u32 s64, s64, s49
	s_add_u32 s64, s64, 0x40000
	s_add_u32 s34, s6, s64
	s_addc_u32 s35, s7, 0
	s_mov_b32 m0, s52
	s_add_u32 s44, s34, 0x0
	s_addc_u32 s45, s35, 0
	global_load_lds_dwordx4 v192, s[44:45] sc1
	v_rcp_f32_e32 v207, v207
	v_mul_f32_e32 v206, v206, v134
	v_mfma_f32_32x32x16_f16 v[32:47], a[128:131], v[160:163], v[32:47]
	ds_read_b128 v[160:163], v193 offset:8192
	v_rcp_f32_e32 v208, v208
	v_mul_f32_e32 v207, v207, v135
	v_mfma_f32_32x32x16_f16 v[48:63], a[128:131], v[164:167], v[48:63]
	ds_read_b128 v[164:167], v193 offset:9216
	v_rcp_f32_e32 v209, v209
	v_fmamk_f32 v208, v208, 0xc0b8aa3b, v198
	s_waitcnt lgkmcnt(2)
	v_mfma_f32_32x32x16_f16 v[32:47], a[132:135], v[168:171], v[32:47]
	ds_read_b128 v[168:171], v193 offset:10240
	v_rcp_f32_e32 v210, v210
	v_fmamk_f32 v209, v209, 0xc0b8aa3b, v198
	v_fma_f32 v132, v200, v208, v204
	v_mfma_f32_32x32x16_f16 v[48:63], a[132:135], v[172:175], v[48:63]
	ds_read_b128 v[172:175], v193 offset:11264
	global_load_lds_dwordx4 v192, s[44:45] offset:1024 sc1
	v_rcp_f32_e32 v211, v211
	v_fmamk_f32 v210, v210, 0xc0b8aa3b, v198
	v_fma_f32 v133, v201, v209, v205
	v_mfma_f32_32x32x16_f16 v[32:47], a[136:139], v[176:179], v[32:47]
	ds_read_b128 v[176:179], v193 offset:12288
	v_rcp_f32_e32 v212, v212
	v_fmamk_f32 v211, v211, 0xc0b8aa3b, v198
	v_fma_f32 v134, v202, v210, v206
	v_mfma_f32_32x32x16_f16 v[48:63], a[136:139], v[180:183], v[48:63]
	ds_read_b128 v[180:183], v193 offset:13312
	v_rcp_f32_e32 v213, v213
	v_fma_f32 v135, v203, v211, v207
	v_mfma_f32_32x32x16_f16 v[32:47], a[140:143], v[184:187], v[32:47]
	ds_read_b128 v[184:187], v193 offset:14336
	v_rcp_f32_e32 v214, v214
	v_mfma_f32_32x32x16_f16 v[48:63], a[140:143], v[188:191], v[48:63]
	ds_read_b128 v[188:191], v193 offset:15360
	global_load_lds_dwordx4 v192, s[44:45] offset:2048 sc1
	v_rcp_f32_e32 v215, v215
	s_waitcnt lgkmcnt(2)
	v_mfma_f32_32x32x16_f16 v[32:47], a[144:147], v[160:163], v[32:47]
	ds_read_b128 v[160:163], v193 offset:16384
	v_exp_f32_e32 v200, v132
	v_mfma_f32_32x32x16_f16 v[48:63], a[144:147], v[164:167], v[48:63]
	ds_read_b128 v[164:167], v193 offset:17408
	v_exp_f32_e32 v201, v133
	v_add_f32_e32 v200, 1.0, v200
	v_mfma_f32_32x32x16_f16 v[32:47], a[148:151], v[168:171], v[32:47]
	ds_read_b128 v[168:171], v193 offset:18432
	v_exp_f32_e32 v202, v134
	v_add_f32_e32 v201, 1.0, v201
	v_mfma_f32_32x32x16_f16 v[48:63], a[148:151], v[172:175], v[48:63]
	ds_read_b128 v[172:175], v193 offset:19456
	global_load_lds_dwordx4 v192, s[44:45] offset:3072 sc1
	v_exp_f32_e32 v203, v135
	v_add_f32_e32 v202, 1.0, v202
	v_mfma_f32_32x32x16_f16 v[32:47], a[152:155], v[176:179], v[32:47]
	ds_read_b128 v[176:179], v193 offset:20480
	v_add_f32_e32 v203, 1.0, v203
	v_rcp_f32_e32 v200, v200
	v_mfma_f32_32x32x16_f16 v[48:63], a[152:155], v[180:183], v[48:63]
	ds_read_b128 v[180:183], v193 offset:21504
	v_rcp_f32_e32 v201, v201
	v_fma_f32 v200, v200, 2.0, -1.0
	s_waitcnt lgkmcnt(2)
	v_mfma_f32_32x32x16_f16 v[32:47], a[156:159], v[184:187], v[32:47]
	ds_read_b128 v[184:187], v193 offset:22528
	v_rcp_f32_e32 v202, v202
	v_fma_f32 v201, v201, 2.0, -1.0
	v_mul_f32_e32 v216, v212, v200
	v_mfma_f32_32x32x16_f16 v[48:63], a[156:159], v[188:191], v[48:63]
	ds_read_b128 v[188:191], v193 offset:23552
	s_mov_b32 m0, s53
	s_add_u32 s44, s34, 0x1000
	s_addc_u32 s45, s35, 0
	global_load_lds_dwordx4 v192, s[44:45] sc1
	v_rcp_f32_e32 v203, v203
	v_fma_f32 v202, v202, 2.0, -1.0
	v_mul_f32_e32 v217, v213, v201
	v_mfma_f32_32x32x16_f16 v[32:47], a[160:163], v[160:163], v[32:47]
	ds_read_b128 v[160:163], v193 offset:24576
	v_fma_f32 v203, v203, 2.0, -1.0
	v_mul_f32_e32 v218, v214, v202
	v_mfma_f32_32x32x16_f16 v[48:63], a[160:163], v[164:167], v[48:63]
	ds_read_b128 v[164:167], v193 offset:25600
	v_mul_f32_e32 v219, v215, v203
	v_cvt_pk_f16_f32 v222, v216, v217
	v_mfma_f32_32x32x16_f16 v[32:47], a[164:167], v[168:171], v[32:47]
	ds_read_b128 v[168:171], v193 offset:26624
	v_cvt_pk_f16_f32 v223, v218, v219
	v_mfma_f32_32x32x16_f16 v[48:63], a[164:167], v[172:175], v[48:63]
	ds_read_b128 v[172:175], v193 offset:27648
	global_load_lds_dwordx4 v192, s[44:45] offset:1024 sc1
	s_cmp_eq_u32 s33, s60
	s_cbranch_scc1 .LE_ht30
.LE_htb31:
	s_waitcnt lgkmcnt(2)
	v_mfma_f32_32x32x16_f16 v[32:47], a[168:171], v[176:179], v[32:47]
	ds_read_b128 v[176:179], v193 offset:28672
	s_nop 1
	v_permlane32_swap_b32_e32 v220, v222
	v_permlane32_swap_b32_e32 v221, v223
	s_cmp_eq_u32 s31, 0
	s_cbranch_scc1 .LE_slow32
	global_store_dwordx4 v195, v[220:223], s[36:37] offset:0
.LE_join33:
	v_mfma_f32_32x32x16_f16 v[48:63], a[168:171], v[180:183], v[48:63]
	ds_read_b128 v[180:183], v193 offset:29696
	v_mfma_f32_32x32x16_f16 v[32:47], a[172:175], v[184:187], v[32:47]
	ds_read_b128 v[184:187], v193 offset:30720
	v_mfma_f32_32x32x16_f16 v[48:63], a[172:175], v[188:191], v[48:63]
	ds_read_b128 v[188:191], v193 offset:31744
	global_load_lds_dwordx4 v192, s[44:45] offset:2048 sc1
	s_waitcnt vmcnt(8)
	s_barrier
	v_mfma_f32_32x32x16_f16 v[32:47], a[176:179], v[160:163], v[32:47]
	ds_read_b128 v[160:163], v193 offset:32768
	v_mfma_f32_32x32x16_f16 v[48:63], a[176:179], v[164:167], v[48:63]
	ds_read_b128 v[164:167], v193 offset:33792
	s_waitcnt lgkmcnt(2)
	v_mfma_f32_32x32x16_f16 v[32:47], a[180:183], v[168:171], v[32:47]
	ds_read_b128 v[168:171], v193 offset:34816
	v_mfma_f32_32x32x16_f16 v[48:63], a[180:183], v[172:175], v[48:63]
	ds_read_b128 v[172:175], v193 offset:35840
	global_load_lds_dwordx4 v192, s[44:45] offset:3072 sc1
	v_mfma_f32_32x32x16_f16 v[32:47], a[184:187], v[176:179], v[32:47]
	ds_read_b128 v[176:179], v193 offset:36864
	v_mfma_f32_32x32x16_f16 v[48:63], a[184:187], v[180:183], v[48:63]
	ds_read_b128 v[180:183], v193 offset:37888
	v_mfma_f32_32x32x16_f16 v[32:47], a[188:191], v[184:187], v[32:47]
	ds_read_b128 v[184:187], v193 offset:38912
	v_mfma_f32_32x32x16_f16 v[48:63], a[188:191], v[188:191], v[48:63]
	ds_read_b128 v[188:191], v193 offset:39936
	s_mov_b32 m0, s54
	s_add_u32 s44, s34, 0x8000
	s_addc_u32 s45, s35, 0
	global_load_lds_dwordx4 v192, s[44:45] sc1
	s_waitcnt lgkmcnt(2)
	v_mfma_f32_32x32x16_f16 v[32:47], a[192:195], v[160:163], v[32:47]
	ds_read_b128 v[160:163], v193 offset:40960
	v_mfma_f32_32x32x16_f16 v[48:63], a[192:195], v[164:167], v[48:63]
	ds_read_b128 v[164:167], v193 offset:41984
	s_waitcnt vmcnt(3)
	s_barrier
	v_mov_b32_e32 v199, 1
	s_cmp_eq_u32 s31, 0
	s_cbranch_scc1 .LE_slow34
	global_store_dword v197, v199, s[40:41]
.LE_join35:
	v_mfma_f32_32x32x16_f16 v[32:47], a[196:199], v[168:171], v[32:47]
	ds_read_b128 v[168:171], v193 offset:43008
	v_mfma_f32_32x32x16_f16 v[48:63], a[196:199], v[172:175], v[48:63]
	ds_read_b128 v[172:175], v193 offset:44032
	global_load_lds_dwordx4 v192, s[44:45] offset:1024 sc1
	v_mfma_f32_32x32x16_f16 v[32:47], a[200:203], v[176:179], v[32:47]
	ds_read_b128 v[176:179], v193 offset:45056
	v_mfma_f32_32x32x16_f16 v[48:63], a[200:203], v[180:183], v[48:63]
	ds_read_b128 v[180:183], v193 offset:46080
	s_and_b32 s64, s33, 1
	s_lshl_b32 s64, s64, 22
	s_add_u32 s64, s64, s50
	s_add_u32 s64, s64, 0x20000
	s_add_u32 s36, s6, s64
	s_addc_u32 s37, s7, 0
	s_lshl_b32 s64, s33, 3
	s_add_u32 s64, s64, s29
	s_lshl_b32 s64, s64, 5
	s_add_u32 s64, s64, s30
	s_lshl_b32 s64, s64, 2
	s_add_u32 s40, s8, s64
	s_addc_u32 s41, s9, 0
	s_lshl_b32 s64, s61, 11
	s_lshl_b32 s65, s29, 8
	s_add_u32 s64, s64, s65
	s_lshl_b32 s64, s64, 3
	s_add_u32 s42, s12, s64
	s_addc_u32 s43, s13, 0
	s_waitcnt lgkmcnt(2)
	v_mfma_f32_32x32x16_f16 v[32:47], a[204:207], v[184:187], v[32:47]
	ds_read_b128 v[184:187], v193 offset:47104
	v_mfma_f32_32x32x16_f16 v[48:63], a[204:207], v[188:191], v[48:63]
	ds_read_b128 v[188:191], v193 offset:48128
	global_load_lds_dwordx4 v192, s[44:45] offset:2048 sc1
	v_mfma_f32_32x32x16_f16 v[32:47], a[208:211], v[160:163], v[32:47]
	ds_read_b128 v[160:163], v193 offset:49152
	v_mfma_f32_32x32x16_f16 v[48:63], a[208:211], v[164:167], v[48:63]
	ds_read_b128 v[164:167], v193 offset:50176
	v_mfma_f32_32x32x16_f16 v[32:47], a[212:215], v[168:171], v[32:47]
	ds_read_b128 v[168:171], v193 offset:51200
	v_mfma_f32_32x32x16_f16 v[48:63], a[212:215], v[172:175], v[48:63]
	ds_read_b128 v[172:175], v193 offset:52224
	global_load_lds_dwordx4 v192, s[44:45] offset:3072 sc1
	s_waitcnt lgkmcnt(2)
	v_mfma_f32_32x32x16_f16 v[32:47], a[216:219], v[176:179], v[32:47]
	ds_read_b128 v[176:179], v193 offset:53248
	v_mfma_f32_32x32x16_f16 v[48:63], a[216:219], v[180:183], v[48:63]
	ds_read_b128 v[180:183], v193 offset:54272
	v_mfma_f32_32x32x16_f16 v[32:47], a[220:223], v[184:187], v[32:47]
	ds_read_b128 v[184:187], v193 offset:55296
	v_mfma_f32_32x32x16_f16 v[48:63], a[220:223], v[188:191], v[48:63]
	ds_read_b128 v[188:191], v193 offset:56320
	s_mov_b32 m0, s55
	s_add_u32 s44, s34, 0x9000
	s_addc_u32 s45, s35, 0
	global_load_lds_dwordx4 v192, s[44:45] sc1
	v_mfma_f32_32x32x16_f16 v[32:47], a[224:227], v[160:163], v[32:47]
	ds_read_b128 v[160:163], v193 offset:57344
	v_mfma_f32_32x32x16_f16 v[48:63], a[224:227], v[164:167], v[48:63]
	ds_read_b128 v[164:167], v193 offset:58368
	s_waitcnt lgkmcnt(2)
	v_mfma_f32_32x32x16_f16 v[32:47], a[228:231], v[168:171], v[32:47]
	ds_read_b128 v[168:171], v193 offset:59392
	v_mfma_f32_32x32x16_f16 v[48:63], a[228:231], v[172:175], v[48:63]
	ds_read_b128 v[172:175], v193 offset:60416
	global_load_lds_dwordx4 v192, s[44:45] offset:1024 sc1
	v_mfma_f32_32x32x16_f16 v[32:47], a[232:235], v[176:179], v[32:47]
	ds_read_b128 v[176:179], v193 offset:61440
	v_mfma_f32_32x32x16_f16 v[48:63], a[232:235], v[180:183], v[48:63]
	ds_read_b128 v[180:183], v193 offset:62464
	v_mfma_f32_32x32x16_f16 v[32:47], a[236:239], v[184:187], v[32:47]
	ds_read_b128 v[184:187], v193 offset:63488
	v_mfma_f32_32x32x16_f16 v[48:63], a[236:239], v[188:191], v[48:63]
	ds_read_b128 v[188:191], v193 offset:64512
	global_load_lds_dwordx4 v192, s[44:45] offset:2048 sc1
	s_waitcnt vmcnt(8)
	s_barrier
	s_waitcnt lgkmcnt(2)
	v_mfma_f32_32x32x16_f16 v[32:47], a[240:243], v[160:163], v[32:47]
	ds_read_b128 v[160:163], v192 offset:0
	v_mfma_f32_32x32x16_f16 v[48:63], a[240:243], v[164:167], v[48:63]
	ds_read_b128 v[164:167], v192 offset:1024
	v_mfma_f32_32x32x16_f16 v[32:47], a[244:247], v[168:171], v[32:47]
	ds_read_b128 v[168:171], v192 offset:2048
	v_mfma_f32_32x32x16_f16 v[48:63], a[244:247], v[172:175], v[48:63]
	ds_read_b128 v[172:175], v192 offset:3072
	global_load_lds_dwordx4 v192, s[44:45] offset:3072 sc1
	v_mfma_f32_32x32x16_f16 v[32:47], a[248:251], v[176:179], v[32:47]
	ds_read_b128 v[176:179], v192 offset:4096
	v_mfma_f32_32x32x16_f16 v[48:63], a[248:251], v[180:183], v[48:63]
	ds_read_b128 v[180:183], v192 offset:5120
	s_waitcnt lgkmcnt(2)
	v_mfma_f32_32x32x16_f16 v[32:47], a[252:255], v[184:187], v[32:47]
	ds_read_b128 v[184:187], v192 offset:6144
	v_mfma_f32_32x32x16_f16 v[48:63], a[252:255], v[188:191], v[48:63]
	ds_read_b128 v[188:191], v192 offset:7168
	s_mov_b32 m0, s56
	s_add_u32 s44, s34, 0x10000
	s_addc_u32 s45, s35, 0
	global_load_lds_dwordx4 v192, s[44:45] sc1
	s_nop 3
	global_load_dword v228, v249, s[42:43] offset:0
	global_load_dword v229, v249, s[42:43] offset:256
	s_waitcnt lgkmcnt(2)
	v_mfma_f32_32x32x16_f16 v[64:79], a[0:3], v[160:163], v[64:79]
	ds_read_b128 v[160:163], v192 offset:8192
	v_exp_f32_e32 v200, v32
	v_mfma_f32_32x32x16_f16 v[80:95], a[0:3], v[164:167], v[80:95]
	ds_read_b128 v[164:167], v192 offset:9216
	s_lshl_b32 s64, s71, 3
	s_add_u32 s64, s64, s29
	s_lshl_b32 s64, s64, 7
	s_add_u32 s38, s8, s64
	s_addc_u32 s39, s9, 0
	global_load_dword v251, v196, s[38:39] sc1
	v_exp_f32_e32 v201, v33
	v_add_f32_e32 v200, 1.0, v200
	v_mfma_f32_32x32x16_f16 v[64:79], a[4:7], v[168:171], v[64:79]
	ds_read_b128 v[168:171], v192 offset:10240
	v_exp_f32_e32 v202, v34
	v_add_f32_e32 v201, 1.0, v201
	v_mfma_f32_32x32x16_f16 v[80:95], a[4:7], v[172:175], v[80:95]
	ds_read_b128 v[172:175], v192 offset:11264
	global_load_lds_dwordx4 v192, s[44:45] offset:1024 sc1
	v_exp_f32_e32 v203, v35
	v_add_f32_e32 v202, 1.0, v202
	v_mfma_f32_32x32x16_f16 v[64:79], a[8:11], v[176:179], v[64:79]
	ds_read_b128 v[176:179], v192 offset:12288
	v_exp_f32_e32 v204, v36
	v_add_f32_e32 v203, 1.0, v203
	v_mfma_f32_32x32x16_f16 v[80:95], a[8:11], v[180:183], v[80:95]
	ds_read_b128 v[180:183], v192 offset:13312
	v_exp_f32_e32 v205, v37
	v_add_f32_e32 v204, 1.0, v204
	s_waitcnt lgkmcnt(2)
	v_mfma_f32_32x32x16_f16 v[64:79], a[12:15], v[184:187], v[64:79]
	ds_read_b128 v[184:187], v192 offset:14336
	v_exp_f32_e32 v206, v38
	v_add_f32_e32 v205, 1.0, v205
	v_mfma_f32_32x32x16_f16 v[80:95], a[12:15], v[188:191], v[80:95]
	ds_read_b128 v[188:191], v192 offset:15360
	global_load_lds_dwordx4 v192, s[44:45] offset:2048 sc1
	v_exp_f32_e32 v207, v39
	v_add_f32_e32 v206, 1.0, v206
	v_mfma_f32_32x32x16_f16 v[64:79], a[16:19], v[160:163], v[64:79]
	ds_read_b128 v[160:163], v192 offset:16384
	v_exp_f32_e32 v208, v40
	v_add_f32_e32 v207, 1.0, v207
	v_mfma_f32_32x32x16_f16 v[80:95], a[16:19], v[164:167], v[80:95]
	ds_read_b128 v[164:167], v192 offset:17408
	v_exp_f32_e32 v209, v41
	v_add_f32_e32 v208, 1.0, v208
	v_mfma_f32_32x32x16_f16 v[64:79], a[20:23], v[168:171], v[64:79]
	ds_read_b128 v[168:171], v192 offset:18432
	v_exp_f32_e32 v210, v42
	v_add_f32_e32 v209, 1.0, v209
	v_mfma_f32_32x32x16_f16 v[80:95], a[20:23], v[172:175], v[80:95]
	ds_read_b128 v[172:175], v192 offset:19456
	global_load_lds_dwordx4 v192, s[44:45] offset:3072 sc1
	v_exp_f32_e32 v211, v43
	v_add_f32_e32 v210, 1.0, v210
	s_waitcnt lgkmcnt(2)
	v_mfma_f32_32x32x16_f16 v[64:79], a[24:27], v[176:179], v[64:79]
	ds_read_b128 v[176:179], v192 offset:20480
	v_exp_f32_e32 v212, v44
	v_add_f32_e32 v211, 1.0, v211
	v_mfma_f32_32x32x16_f16 v[80:95], a[24:27], v[180:183], v[80:95]
	ds_read_b128 v[180:183], v192 offset:21504
	v_exp_f32_e32 v213, v45
	v_add_f32_e32 v212, 1.0, v212
	v_mfma_f32_32x32x16_f16 v[64:79], a[28:31], v[184:187], v[64:79]
	ds_read_b128 v[184:187], v192 offset:22528
	v_exp_f32_e32 v214, v46
	v_add_f32_e32 v213, 1.0, v213
	v_mfma_f32_32x32x16_f16 v[80:95], a[28:31], v[188:191], v[80:95]
	ds_read_b128 v[188:191], v192 offset:23552
	s_mov_b32 m0, s57
	s_add_u32 s44, s34, 0x11000
	s_addc_u32 s45, s35, 0
	global_load_lds_dwordx4 v192, s[44:45] sc1
	v_exp_f32_e32 v215, v47
	v_add_f32_e32 v214, 1.0, v214
	v_mfma_f32_32x32x16_f16 v[64:79], a[32:35], v[160:163], v[64:79]
	ds_read_b128 v[160:163], v192 offset:24576
	v_add_f32_e32 v215, 1.0, v215
	v_rcp_f32_e32 v200, v200
	v_mfma_f32_32x32x16_f16 v[80:95], a[32:35], v[164:167], v[80:95]
	ds_read_b128 v[164:167], v192 offset:25600
	v_rcp_f32_e32 v201, v201
	s_waitcnt lgkmcnt(2)
	v_mfma_f32_32x32x16_f16 v[64:79], a[36:39], v[168:171], v[64:79]
	ds_read_b128 v[168:171], v192 offset:26624
	v_rcp_f32_e32 v202, v202
	v_mfma_f32_32x32x16_f16 v[80:95], a[36:39], v[172:175], v[80:95]
	ds_read_b128 v[172:175], v192 offset:27648
	global_load_lds_dwordx4 v192, s[44:45] offset:1024 sc1
	v_rcp_f32_e32 v203, v203
	v_mfma_f32_32x32x16_f16 v[64:79], a[40:43], v[176:179], v[64:79]
	ds_read_b128 v[176:179], v192 offset:28672
	v_rcp_f32_e32 v204, v204
	v_mfma_f32_32x32x16_f16 v[80:95], a[40:43], v[180:183], v[80:95]
	ds_read_b128 v[180:183], v192 offset:29696
	v_rcp_f32_e32 v205, v205
	v_mul_f32_e32 v204, v204, v136
	v_mfma_f32_32x32x16_f16 v[64:79], a[44:47], v[184:187], v[64:79]
	ds_read_b128 v[184:187], v192 offset:30720
	v_rcp_f32_e32 v206, v206
	v_mul_f32_e32 v205, v205, v137
	v_mfma_f32_32x32x16_f16 v[80:95], a[44:47], v[188:191], v[80:95]
	ds_read_b128 v[188:191], v192 offset:31744
	global_load_lds_dwordx4 v192, s[44:45] offset:2048 sc1
	v_rcp_f32_e32 v207, v207
	v_mul_f32_e32 v206, v206, v138
	s_waitcnt vmcnt(10)
	s_barrier
	s_waitcnt lgkmcnt(2)
	v_mfma_f32_32x32x16_f16 v[64:79], a[48:51], v[160:163], v[64:79]
	ds_read_b128 v[160:163], v192 offset:32768
	v_rcp_f32_e32 v208, v208
	v_mul_f32_e32 v207, v207, v139
	v_mfma_f32_32x32x16_f16 v[80:95], a[48:51], v[164:167], v[80:95]
	ds_read_b128 v[164:167], v192 offset:33792
	v_rcp_f32_e32 v209, v209
	v_fmamk_f32 v208, v208, 0xc0b8aa3b, v198
	v_mfma_f32_32x32x16_f16 v[64:79], a[52:55], v[168:171], v[64:79]
	ds_read_b128 v[168:171], v192 offset:34816
	v_rcp_f32_e32 v210, v210
	v_fmamk_f32 v209, v209, 0xc0b8aa3b, v198
	v_fma_f32 v136, v200, v208, v204
	v_mfma_f32_32x32x16_f16 v[80:95], a[52:55], v[172:175], v[80:95]
	ds_read_b128 v[172:175], v192 offset:35840
	global_load_lds_dwordx4 v192, s[44:45] offset:3072 sc1
	v_rcp_f32_e32 v211, v211
	v_fmamk_f32 v210, v210, 0xc0b8aa3b, v198
	v_fma_f32 v137, v201, v209, v205
	v_mfma_f32_32x32x16_f16 v[64:79], a[56:59], v[176:179], v[64:79]
	ds_read_b128 v[176:179], v192 offset:36864
	v_rcp_f32_e32 v212, v212
	v_fmamk_f32 v211, v211, 0xc0b8aa3b, v198
	v_fma_f32 v138, v202, v210, v206
	v_mfma_f32_32x32x16_f16 v[80:95], a[56:59], v[180:183], v[80:95]
	ds_read_b128 v[180:183], v192 offset:37888
	v_rcp_f32_e32 v213, v213
	v_fma_f32 v139, v203, v211, v207
	s_waitcnt lgkmcnt(2)
	v_mfma_f32_32x32x16_f16 v[64:79], a[60:63], v[184:187], v[64:79]
	ds_read_b128 v[184:187], v192 offset:38912
	v_rcp_f32_e32 v214, v214
	v_mfma_f32_32x32x16_f16 v[80:95], a[60:63], v[188:191], v[80:95]
	ds_read_b128 v[188:191], v192 offset:39936
	s_mov_b32 m0, s58
	s_add_u32 s44, s34, 0x18000
	s_addc_u32 s45, s35, 0
	global_load_lds_dwordx4 v192, s[44:45] sc1
	v_rcp_f32_e32 v215, v215
	v_mfma_f32_32x32x16_f16 v[64:79], a[64:67], v[160:163], v[64:79]
	ds_read_b128 v[160:163], v192 offset:40960
	v_exp_f32_e32 v200, v136
	v_mfma_f32_32x32x16_f16 v[80:95], a[64:67], v[164:167], v[80:95]
	ds_read_b128 v[164:167], v192 offset:41984
	v_exp_f32_e32 v201, v137
	v_add_f32_e32 v200, 1.0, v200
	v_mfma_f32_32x32x16_f16 v[64:79], a[68:71], v[168:171], v[64:79]
	ds_read_b128 v[168:171], v192 offset:43008
	v_exp_f32_e32 v202, v138
	v_add_f32_e32 v201, 1.0, v201
	v_mfma_f32_32x32x16_f16 v[80:95], a[68:71], v[172:175], v[80:95]
	ds_read_b128 v[172:175], v192 offset:44032
	global_load_lds_dwordx4 v192, s[44:45] offset:1024 sc1
	v_exp_f32_e32 v203, v139
	v_add_f32_e32 v202, 1.0, v202
	s_waitcnt lgkmcnt(2)
	v_mfma_f32_32x32x16_f16 v[64:79], a[72:75], v[176:179], v[64:79]
	ds_read_b128 v[176:179], v192 offset:45056
	v_add_f32_e32 v203, 1.0, v203
	v_rcp_f32_e32 v200, v200
	v_mfma_f32_32x32x16_f16 v[80:95], a[72:75], v[180:183], v[80:95]
	ds_read_b128 v[180:183], v192 offset:46080
	v_rcp_f32_e32 v201, v201
	v_fma_f32 v200, v200, 2.0, -1.0
	v_mfma_f32_32x32x16_f16 v[64:79], a[76:79], v[184:187], v[64:79]
	ds_read_b128 v[184:187], v192 offset:47104
	v_rcp_f32_e32 v202, v202
	v_fma_f32 v201, v201, 2.0, -1.0
	v_mul_f32_e32 v216, v212, v200
	v_mfma_f32_32x32x16_f16 v[80:95], a[76:79], v[188:191], v[80:95]
	ds_read_b128 v[188:191], v192 offset:48128
	global_load_lds_dwordx4 v192, s[44:45] offset:2048 sc1
	v_rcp_f32_e32 v203, v203
	v_fma_f32 v202, v202, 2.0, -1.0
	v_mul_f32_e32 v217, v213, v201
	v_mfma_f32_32x32x16_f16 v[64:79], a[80:83], v[160:163], v[64:79]
	ds_read_b128 v[160:163], v192 offset:49152
	v_fma_f32 v203, v203, 2.0, -1.0
	v_mul_f32_e32 v218, v214, v202
	v_exp_f32_e32 v200, v48
	v_mfma_f32_32x32x16_f16 v[80:95], a[80:83], v[164:167], v[80:95]
	ds_read_b128 v[164:167], v192 offset:50176
	v_mul_f32_e32 v219, v215, v203
	v_cvt_pk_f16_f32 v220, v216, v217
	v_exp_f32_e32 v201, v49
	s_waitcnt lgkmcnt(2)
	v_mfma_f32_32x32x16_f16 v[64:79], a[84:87], v[168:171], v[64:79]
	ds_read_b128 v[168:171], v192 offset:51200
	v_cvt_pk_f16_f32 v221, v218, v219
	v_exp_f32_e32 v202, v50
	v_add_f32_e32 v200, 1.0, v200
	v_mfma_f32_32x32x16_f16 v[80:95], a[84:87], v[172:175], v[80:95]
	ds_read_b128 v[172:175], v192 offset:52224
	global_load_lds_dwordx4 v192, s[44:45] offset:3072 sc1
	s_cmp_eq_u32 s33, s60
	s_cbranch_scc1 .LE_ht36
.LE_htb37:
	v_exp_f32_e32 v203, v51
	v_mfma_f32_32x32x16_f16 v[64:79], a[88:91], v[176:179], v[64:79]
	ds_read_b128 v[176:179], v192 offset:53248
	v_exp_f32_e32 v204, v52
	v_add_f32_e32 v201, 1.0, v201
	v_add_f32_e32 v202, 1.0, v202
	v_mfma_f32_32x32x16_f16 v[80:95], a[88:91], v[180:183], v[80:95]
	ds_read_b128 v[180:183], v192 offset:54272
	v_exp_f32_e32 v205, v53
	v_add_f32_e32 v203, 1.0, v203
	v_add_f32_e32 v204, 1.0, v204
	v_mfma_f32_32x32x16_f16 v[64:79], a[92:95], v[184:187], v[64:79]
	ds_read_b128 v[184:187], v192 offset:55296
	v_exp_f32_e32 v206, v54
	v_add_f32_e32 v205, 1.0, v205
	v_mfma_f32_32x32x16_f16 v[80:95], a[92:95], v[188:191], v[80:95]
	ds_read_b128 v[188:191], v192 offset:56320
	s_mov_b32 m0, s59
	s_add_u32 s44, s34, 0x19000
	s_addc_u32 s45, s35, 0
	global_load_lds_dwordx4 v192, s[44:45] sc1
	v_exp_f32_e32 v207, v55
	v_add_f32_e32 v206, 1.0, v206
	s_waitcnt lgkmcnt(2)
	v_mfma_f32_32x32x16_f16 v[64:79], a[96:99], v[160:163], v[64:79]
	ds_read_b128 v[160:163], v192 offset:57344
	v_exp_f32_e32 v208, v56
	v_add_f32_e32 v207, 1.0, v207
	v_mfma_f32_32x32x16_f16 v[80:95], a[96:99], v[164:167], v[80:95]
	ds_read_b128 v[164:167], v192 offset:58368
	v_exp_f32_e32 v209, v57
	v_add_f32_e32 v208, 1.0, v208
	v_mfma_f32_32x32x16_f16 v[64:79], a[100:103], v[168:171], v[64:79]
	ds_read_b128 v[168:171], v192 offset:59392
	v_exp_f32_e32 v210, v58
	v_add_f32_e32 v209, 1.0, v209
	v_mfma_f32_32x32x16_f16 v[80:95], a[100:103], v[172:175], v[80:95]
	ds_read_b128 v[172:175], v192 offset:60416
	global_load_lds_dwordx4 v192, s[44:45] offset:1024 sc1
	v_exp_f32_e32 v211, v59
	v_add_f32_e32 v210, 1.0, v210
	v_mfma_f32_32x32x16_f16 v[64:79], a[104:107], v[176:179], v[64:79]
	ds_read_b128 v[176:179], v192 offset:61440
	v_exp_f32_e32 v212, v60
	v_add_f32_e32 v211, 1.0, v211
	v_mfma_f32_32x32x16_f16 v[80:95], a[104:107], v[180:183], v[80:95]
	ds_read_b128 v[180:183], v192 offset:62464
	v_exp_f32_e32 v213, v61
	v_add_f32_e32 v212, 1.0, v212
	s_waitcnt lgkmcnt(2)
	v_mfma_f32_32x32x16_f16 v[64:79], a[108:111], v[184:187], v[64:79]
	ds_read_b128 v[184:187], v192 offset:63488
	v_exp_f32_e32 v214, v62
	v_add_f32_e32 v213, 1.0, v213
	v_mfma_f32_32x32x16_f16 v[80:95], a[108:111], v[188:191], v[80:95]
	ds_read_b128 v[188:191], v192 offset:64512
	global_load_lds_dwordx4 v192, s[44:45] offset:2048 sc1
	v_exp_f32_e32 v215, v63
	v_add_f32_e32 v214, 1.0, v214
	s_waitcnt vmcnt(7)
	s_barrier
	v_mfma_f32_32x32x16_f16 v[64:79], a[112:115], v[160:163], v[64:79]
	ds_read_b128 v[160:163], v193 offset:0
	v_add_f32_e32 v215, 1.0, v215
	v_rcp_f32_e32 v200, v200
	v_mfma_f32_32x32x16_f16 v[80:95], a[112:115], v[164:167], v[80:95]
	ds_read_b128 v[164:167], v193 offset:1024
	v_rcp_f32_e32 v201, v201
	v_mfma_f32_32x32x16_f16 v[64:79], a[116:119], v[168:171], v[64:79]
	ds_read_b128 v[168:171], v193 offset:2048
	v_rcp_f32_e32 v202, v202
	v_mfma_f32_32x32x16_f16 v[80:95], a[116:119], v[172:175], v[80:95]
	ds_read_b128 v[172:175], v193 offset:3072
	global_load_lds_dwordx4 v192, s[44:45] offset:3072 sc1
	v_rcp_f32_e32 v203, v203
	s_waitcnt lgkmcnt(2)
	v_mfma_f32_32x32x16_f16 v[64:79], a[120:123], v[176:179], v[64:79]
	ds_read_b128 v[176:179], v193 offset:4096
	v_rcp_f32_e32 v204, v204
	v_mfma_f32_32x32x16_f16 v[80:95], a[120:123], v[180:183], v[80:95]
	ds_read_b128 v[180:183], v193 offset:5120
	v_rcp_f32_e32 v205, v205
	v_mul_f32_e32 v204, v204, v140
	v_mfma_f32_32x32x2_f32 v[0:15], v248, v228, v[232:247]
	v_mfma_f32_32x32x16_f16 v[64:79], a[124:127], v[184:187], v[64:79]
	ds_read_b128 v[184:187], v193 offset:6144
	v_rcp_f32_e32 v206, v206
	v_mul_f32_e32 v205, v205, v141
	v_mfma_f32_32x32x2_f32 v[16:31], v248, v229, v[232:247]
	v_mfma_f32_32x32x16_f16 v[80:95], a[124:127], v[188:191], v[80:95]
	ds_read_b128 v[188:191], v193 offset:7168
	v_cmp_gt_u32_e32 vcc, 4, v251
	s_cbranch_vccnz .LE_tpoll39
.LE_tok38:
	s_and_b32 s64, s71, 1
	s_lshl_b32 s64, s64, 22
	s_add_u32 s64, s64, s49
	s_add_u32 s64, s64, 0x60000
	s_add_u32 s34, s6, s64
	s_addc_u32 s35, s7, 0
	s_mov_b32 m0, s52
	s_add_u32 s44, s34, 0x0
	s_addc_u32 s45, s35, 0
	global_load_lds_dwordx4 v192, s[44:45] sc1
	v_rcp_f32_e32 v207, v207
	v_mul_f32_e32 v206, v206, v142
	v_mfma_f32_32x32x16_f16 v[64:79], a[128:131], v[160:163], v[64:79]
	ds_read_b128 v[160:163], v193 offset:8192
	v_rcp_f32_e32 v208, v208
	v_mul_f32_e32 v207, v207, v143
	v_mfma_f32_32x32x16_f16 v[80:95], a[128:131], v[164:167], v[80:95]
	ds_read_b128 v[164:167], v193 offset:9216
	v_rcp_f32_e32 v209, v209
	v_fmamk_f32 v208, v208, 0xc0b8aa3b, v198
	s_waitcnt lgkmcnt(2)
	v_mfma_f32_32x32x16_f16 v[64:79], a[132:135], v[168:171], v[64:79]
	ds_read_b128 v[168:171], v193 offset:10240
	v_rcp_f32_e32 v210, v210
	v_fmamk_f32 v209, v209, 0xc0b8aa3b, v198
	v_fma_f32 v140, v200, v208, v204
	v_mfma_f32_32x32x16_f16 v[80:95], a[132:135], v[172:175], v[80:95]
	ds_read_b128 v[172:175], v193 offset:11264
	global_load_lds_dwordx4 v192, s[44:45] offset:1024 sc1
	v_rcp_f32_e32 v211, v211
	v_fmamk_f32 v210, v210, 0xc0b8aa3b, v198
	v_fma_f32 v141, v201, v209, v205
	v_mfma_f32_32x32x16_f16 v[64:79], a[136:139], v[176:179], v[64:79]
	ds_read_b128 v[176:179], v193 offset:12288
	v_rcp_f32_e32 v212, v212
	v_fmamk_f32 v211, v211, 0xc0b8aa3b, v198
	v_fma_f32 v142, v202, v210, v206
	v_mfma_f32_32x32x16_f16 v[80:95], a[136:139], v[180:183], v[80:95]
	ds_read_b128 v[180:183], v193 offset:13312
	v_rcp_f32_e32 v213, v213
	v_fma_f32 v143, v203, v211, v207
	v_mfma_f32_32x32x16_f16 v[64:79], a[140:143], v[184:187], v[64:79]
	ds_read_b128 v[184:187], v193 offset:14336
	v_rcp_f32_e32 v214, v214
	v_mfma_f32_32x32x16_f16 v[80:95], a[140:143], v[188:191], v[80:95]
	ds_read_b128 v[188:191], v193 offset:15360
	global_load_lds_dwordx4 v192, s[44:45] offset:2048 sc1
	v_rcp_f32_e32 v215, v215
	s_waitcnt lgkmcnt(2)
	v_mfma_f32_32x32x16_f16 v[64:79], a[144:147], v[160:163], v[64:79]
	ds_read_b128 v[160:163], v193 offset:16384
	v_exp_f32_e32 v200, v140
	v_mfma_f32_32x32x16_f16 v[80:95], a[144:147], v[164:167], v[80:95]
	ds_read_b128 v[164:167], v193 offset:17408
	v_exp_f32_e32 v201, v141
	v_add_f32_e32 v200, 1.0, v200
	v_mfma_f32_32x32x16_f16 v[64:79], a[148:151], v[168:171], v[64:79]
	ds_read_b128 v[168:171], v193 offset:18432
	v_exp_f32_e32 v202, v142
	v_add_f32_e32 v201, 1.0, v201
	v_mfma_f32_32x32x16_f16 v[80:95], a[148:151], v[172:175], v[80:95]
	ds_read_b128 v[172:175], v193 offset:19456
	global_load_lds_dwordx4 v192, s[44:45] offset:3072 sc1
	v_exp_f32_e32 v203, v143
	v_add_f32_e32 v202, 1.0, v202
	v_mfma_f32_32x32x16_f16 v[64:79], a[152:155], v[176:179], v[64:79]
	ds_read_b128 v[176:179], v193 offset:20480
	v_add_f32_e32 v203, 1.0, v203
	v_rcp_f32_e32 v200, v200
	v_mfma_f32_32x32x16_f16 v[80:95], a[152:155], v[180:183], v[80:95]
	ds_read_b128 v[180:183], v193 offset:21504
	v_rcp_f32_e32 v201, v201
	v_fma_f32 v200, v200, 2.0, -1.0
	s_waitcnt lgkmcnt(2)
	v_mfma_f32_32x32x16_f16 v[64:79], a[156:159], v[184:187], v[64:79]
	ds_read_b128 v[184:187], v193 offset:22528
	v_rcp_f32_e32 v202, v202
	v_fma_f32 v201, v201, 2.0, -1.0
	v_mul_f32_e32 v216, v212, v200
	v_mfma_f32_32x32x16_f16 v[80:95], a[156:159], v[188:191], v[80:95]
	ds_read_b128 v[188:191], v193 offset:23552
	s_mov_b32 m0, s53
	s_add_u32 s44, s34, 0x1000
	s_addc_u32 s45, s35, 0
	global_load_lds_dwordx4 v192, s[44:45] sc1
	v_rcp_f32_e32 v203, v203
	v_fma_f32 v202, v202, 2.0, -1.0
	v_mul_f32_e32 v217, v213, v201
	v_mfma_f32_32x32x16_f16 v[64:79], a[160:163], v[160:163], v[64:79]
	ds_read_b128 v[160:163], v193 offset:24576
	v_fma_f32 v203, v203, 2.0, -1.0
	v_mul_f32_e32 v218, v214, v202
	v_mfma_f32_32x32x16_f16 v[80:95], a[160:163], v[164:167], v[80:95]
	ds_read_b128 v[164:167], v193 offset:25600
	v_mul_f32_e32 v219, v215, v203
	v_cvt_pk_f16_f32 v222, v216, v217
	v_mfma_f32_32x32x16_f16 v[64:79], a[164:167], v[168:171], v[64:79]
	ds_read_b128 v[168:171], v193 offset:26624
	v_cvt_pk_f16_f32 v223, v218, v219
	v_mfma_f32_32x32x16_f16 v[80:95], a[164:167], v[172:175], v[80:95]
	ds_read_b128 v[172:175], v193 offset:27648
	global_load_lds_dwordx4 v192, s[44:45] offset:1024 sc1
	s_cmp_eq_u32 s33, s60
	s_cbranch_scc1 .LE_ht40
.LE_htb41:
	s_waitcnt lgkmcnt(2)
	v_mfma_f32_32x32x16_f16 v[64:79], a[168:171], v[176:179], v[64:79]
	ds_read_b128 v[176:179], v193 offset:28672
	s_nop 1
	v_permlane32_swap_b32_e32 v220, v222
	v_permlane32_swap_b32_e32 v221, v223
	s_cmp_eq_u32 s31, 0
	s_cbranch_scc1 .LE_slow42
	global_store_dwordx4 v195, v[220:223], s[36:37] offset:0
.LE_join43:
	v_mfma_f32_32x32x16_f16 v[80:95], a[168:171], v[180:183], v[80:95]
	ds_read_b128 v[180:183], v193 offset:29696
	v_mfma_f32_32x32x16_f16 v[64:79], a[172:175], v[184:187], v[64:79]
	ds_read_b128 v[184:187], v193 offset:30720
	v_mfma_f32_32x32x16_f16 v[80:95], a[172:175], v[188:191], v[80:95]
	ds_read_b128 v[188:191], v193 offset:31744
	global_load_lds_dwordx4 v192, s[44:45] offset:2048 sc1
	s_waitcnt vmcnt(8)
	s_barrier
	v_mfma_f32_32x32x16_f16 v[64:79], a[176:179], v[160:163], v[64:79]
	ds_read_b128 v[160:163], v193 offset:32768
	v_mfma_f32_32x32x16_f16 v[80:95], a[176:179], v[164:167], v[80:95]
	ds_read_b128 v[164:167], v193 offset:33792
	s_waitcnt lgkmcnt(2)
	v_mfma_f32_32x32x16_f16 v[64:79], a[180:183], v[168:171], v[64:79]
	ds_read_b128 v[168:171], v193 offset:34816
	v_mfma_f32_32x32x16_f16 v[80:95], a[180:183], v[172:175], v[80:95]
	ds_read_b128 v[172:175], v193 offset:35840
	global_load_lds_dwordx4 v192, s[44:45] offset:3072 sc1
	v_mfma_f32_32x32x16_f16 v[64:79], a[184:187], v[176:179], v[64:79]
	ds_read_b128 v[176:179], v193 offset:36864
	v_mfma_f32_32x32x16_f16 v[80:95], a[184:187], v[180:183], v[80:95]
	ds_read_b128 v[180:183], v193 offset:37888
	v_mfma_f32_32x32x16_f16 v[64:79], a[188:191], v[184:187], v[64:79]
	ds_read_b128 v[184:187], v193 offset:38912
	v_mfma_f32_32x32x16_f16 v[80:95], a[188:191], v[188:191], v[80:95]
	ds_read_b128 v[188:191], v193 offset:39936
	s_mov_b32 m0, s54
	s_add_u32 s44, s34, 0x8000
	s_addc_u32 s45, s35, 0
	global_load_lds_dwordx4 v192, s[44:45] sc1
	s_waitcnt lgkmcnt(2)
	v_mfma_f32_32x32x16_f16 v[64:79], a[192:195], v[160:163], v[64:79]
	ds_read_b128 v[160:163], v193 offset:40960
	v_mfma_f32_32x32x16_f16 v[80:95], a[192:195], v[164:167], v[80:95]
	ds_read_b128 v[164:167], v193 offset:41984
	s_waitcnt vmcnt(3)
	s_barrier
	v_mov_b32_e32 v199, 2
	s_cmp_eq_u32 s31, 0
	s_cbranch_scc1 .LE_slow44
	global_store_dword v197, v199, s[40:41]
.LE_join45:
	v_mfma_f32_32x32x16_f16 v[64:79], a[196:199], v[168:171], v[64:79]
	ds_read_b128 v[168:171], v193 offset:43008
	v_mfma_f32_32x32x16_f16 v[80:95], a[196:199], v[172:175], v[80:95]
	ds_read_b128 v[172:175], v193 offset:44032
	global_load_lds_dwordx4 v192, s[44:45] offset:1024 sc1
	v_mfma_f32_32x32x16_f16 v[64:79], a[200:203], v[176:179], v[64:79]
	ds_read_b128 v[176:179], v193 offset:45056
	v_mfma_f32_32x32x16_f16 v[80:95], a[200:203], v[180:183], v[80:95]
	ds_read_b128 v[180:183], v193 offset:46080
	s_and_b32 s64, s33, 1
	s_lshl_b32 s64, s64, 22
	s_add_u32 s64, s64, s50
	s_add_u32 s64, s64, 0x40000
	s_add_u32 s36, s6, s64
	s_addc_u32 s37, s7, 0
	s_lshl_b32 s64, s33, 3
	s_add_u32 s64, s64, s29
	s_lshl_b32 s64, s64, 5
	s_add_u32 s64, s64, s30
	s_lshl_b32 s64, s64, 2
	s_add_u32 s40, s8, s64
	s_addc_u32 s41, s9, 0
	s_lshl_b32 s64, s61, 11
	s_lshl_b32 s65, s29, 8
	s_add_u32 s64, s64, s65
	s_add_u32 s64, s64, 64
	s_lshl_b32 s64, s64, 3
	s_add_u32 s42, s12, s64
	s_addc_u32 s43, s13, 0
	s_waitcnt lgkmcnt(2)
	v_mfma_f32_32x32x16_f16 v[64:79], a[204:207], v[184:187], v[64:79]
	ds_read_b128 v[184:187], v193 offset:47104
	v_mfma_f32_32x32x16_f16 v[80:95], a[204:207], v[188:191], v[80:95]
	ds_read_b128 v[188:191], v193 offset:48128
	global_load_lds_dwordx4 v192, s[44:45] offset:2048 sc1
	v_mfma_f32_32x32x16_f16 v[64:79], a[208:211], v[160:163], v[64:79]
	ds_read_b128 v[160:163], v193 offset:49152
	v_mfma_f32_32x32x16_f16 v[80:95], a[208:211], v[164:167], v[80:95]
	ds_read_b128 v[164:167], v193 offset:50176
	v_mfma_f32_32x32x16_f16 v[64:79], a[212:215], v[168:171], v[64:79]
	ds_read_b128 v[168:171], v193 offset:51200
	v_mfma_f32_32x32x16_f16 v[80:95], a[212:215], v[172:175], v[80:95]
	ds_read_b128 v[172:175], v193 offset:52224
	global_load_lds_dwordx4 v192, s[44:45] offset:3072 sc1
	s_waitcnt lgkmcnt(2)
	v_mfma_f32_32x32x16_f16 v[64:79], a[216:219], v[176:179], v[64:79]
	ds_read_b128 v[176:179], v193 offset:53248
	v_mfma_f32_32x32x16_f16 v[80:95], a[216:219], v[180:183], v[80:95]
	ds_read_b128 v[180:183], v193 offset:54272
	v_mfma_f32_32x32x16_f16 v[64:79], a[220:223], v[184:187], v[64:79]
	ds_read_b128 v[184:187], v193 offset:55296
	v_mfma_f32_32x32x16_f16 v[80:95], a[220:223], v[188:191], v[80:95]
	ds_read_b128 v[188:191], v193 offset:56320
	s_mov_b32 m0, s55
	s_add_u32 s44, s34, 0x9000
	s_addc_u32 s45, s35, 0
	global_load_lds_dwordx4 v192, s[44:45] sc1
	v_mfma_f32_32x32x16_f16 v[64:79], a[224:227], v[160:163], v[64:79]
	ds_read_b128 v[160:163], v193 offset:57344
	v_mfma_f32_32x32x16_f16 v[80:95], a[224:227], v[164:167], v[80:95]
	ds_read_b128 v[164:167], v193 offset:58368
	s_waitcnt lgkmcnt(2)
	v_mfma_f32_32x32x16_f16 v[64:79], a[228:231], v[168:171], v[64:79]
	ds_read_b128 v[168:171], v193 offset:59392
	v_mfma_f32_32x32x16_f16 v[80:95], a[228:231], v[172:175], v[80:95]
	ds_read_b128 v[172:175], v193 offset:60416
	global_load_lds_dwordx4 v192, s[44:45] offset:1024 sc1
	v_mfma_f32_32x32x16_f16 v[64:79], a[232:235], v[176:179], v[64:79]
	ds_read_b128 v[176:179], v193 offset:61440
	v_mfma_f32_32x32x16_f16 v[80:95], a[232:235], v[180:183], v[80:95]
	ds_read_b128 v[180:183], v193 offset:62464
	v_mfma_f32_32x32x16_f16 v[64:79], a[236:239], v[184:187], v[64:79]
	ds_read_b128 v[184:187], v193 offset:63488
	v_mfma_f32_32x32x16_f16 v[80:95], a[236:239], v[188:191], v[80:95]
	ds_read_b128 v[188:191], v193 offset:64512
	global_load_lds_dwordx4 v192, s[44:45] offset:2048 sc1
	s_waitcnt vmcnt(8)
	s_barrier
	s_waitcnt lgkmcnt(2)
	v_mfma_f32_32x32x16_f16 v[64:79], a[240:243], v[160:163], v[64:79]
	ds_read_b128 v[160:163], v192 offset:0
	v_mfma_f32_32x32x16_f16 v[80:95], a[240:243], v[164:167], v[80:95]
	ds_read_b128 v[164:167], v192 offset:1024
	v_mfma_f32_32x32x16_f16 v[64:79], a[244:247], v[168:171], v[64:79]
	ds_read_b128 v[168:171], v192 offset:2048
	v_mfma_f32_32x32x16_f16 v[80:95], a[244:247], v[172:175], v[80:95]
	ds_read_b128 v[172:175], v192 offset:3072
	global_load_lds_dwordx4 v192, s[44:45] offset:3072 sc1
	v_mfma_f32_32x32x16_f16 v[64:79], a[248:251], v[176:179], v[64:79]
	ds_read_b128 v[176:179], v192 offset:4096
	v_mfma_f32_32x32x16_f16 v[80:95], a[248:251], v[180:183], v[80:95]
	ds_read_b128 v[180:183], v192 offset:5120
	s_waitcnt lgkmcnt(2)
	v_mfma_f32_32x32x16_f16 v[64:79], a[252:255], v[184:187], v[64:79]
	ds_read_b128 v[184:187], v192 offset:6144
	v_mfma_f32_32x32x16_f16 v[80:95], a[252:255], v[188:191], v[80:95]
	ds_read_b128 v[188:191], v192 offset:7168
	s_mov_b32 m0, s56
	s_add_u32 s44, s34, 0x10000
	s_addc_u32 s45, s35, 0
	global_load_lds_dwordx4 v192, s[44:45] sc1
	s_nop 3
	global_load_dword v228, v249, s[42:43] offset:0
	global_load_dword v229, v249, s[42:43] offset:256
	s_waitcnt lgkmcnt(2)
	v_mfma_f32_32x32x16_f16 v[96:111], a[0:3], v[160:163], v[96:111]
	ds_read_b128 v[160:163], v192 offset:8192
	v_exp_f32_e32 v200, v64
	v_mfma_f32_32x32x16_f16 v[112:127], a[0:3], v[164:167], v[112:127]
	ds_read_b128 v[164:167], v192 offset:9216
	s_lshl_b32 s64, s33, 3
	s_add_u32 s64, s64, s29
	s_lshl_b32 s64, s64, 7
	s_add_u32 s38, s8, s64
	s_addc_u32 s39, s9, 0
	global_load_dword v251, v196, s[38:39] sc1
	v_exp_f32_e32 v201, v65
	v_add_f32_e32 v200, 1.0, v200
	v_mfma_f32_32x32x16_f16 v[96:111], a[4:7], v[168:171], v[96:111]
	ds_read_b128 v[168:171], v192 offset:10240
	v_exp_f32_e32 v202, v66
	v_add_f32_e32 v201, 1.0, v201
	v_mfma_f32_32x32x16_f16 v[112:127], a[4:7], v[172:175], v[112:127]
	ds_read_b128 v[172:175], v192 offset:11264
	global_load_lds_dwordx4 v192, s[44:45] offset:1024 sc1
	v_exp_f32_e32 v203, v67
	v_add_f32_e32 v202, 1.0, v202
	v_mfma_f32_32x32x16_f16 v[96:111], a[8:11], v[176:179], v[96:111]
	ds_read_b128 v[176:179], v192 offset:12288
	v_exp_f32_e32 v204, v68
	v_add_f32_e32 v203, 1.0, v203
	v_mfma_f32_32x32x16_f16 v[112:127], a[8:11], v[180:183], v[112:127]
	ds_read_b128 v[180:183], v192 offset:13312
	v_exp_f32_e32 v205, v69
	v_add_f32_e32 v204, 1.0, v204
	s_waitcnt lgkmcnt(2)
	v_mfma_f32_32x32x16_f16 v[96:111], a[12:15], v[184:187], v[96:111]
	ds_read_b128 v[184:187], v192 offset:14336
	v_exp_f32_e32 v206, v70
	v_add_f32_e32 v205, 1.0, v205
	v_mfma_f32_32x32x16_f16 v[112:127], a[12:15], v[188:191], v[112:127]
	ds_read_b128 v[188:191], v192 offset:15360
	global_load_lds_dwordx4 v192, s[44:45] offset:2048 sc1
	v_exp_f32_e32 v207, v71
	v_add_f32_e32 v206, 1.0, v206
	v_mfma_f32_32x32x16_f16 v[96:111], a[16:19], v[160:163], v[96:111]
	ds_read_b128 v[160:163], v192 offset:16384
	v_exp_f32_e32 v208, v72
	v_add_f32_e32 v207, 1.0, v207
	v_mfma_f32_32x32x16_f16 v[112:127], a[16:19], v[164:167], v[112:127]
	ds_read_b128 v[164:167], v192 offset:17408
	v_exp_f32_e32 v209, v73
	v_add_f32_e32 v208, 1.0, v208
	v_mfma_f32_32x32x16_f16 v[96:111], a[20:23], v[168:171], v[96:111]
	ds_read_b128 v[168:171], v192 offset:18432
	v_exp_f32_e32 v210, v74
	v_add_f32_e32 v209, 1.0, v209
	v_mfma_f32_32x32x16_f16 v[112:127], a[20:23], v[172:175], v[112:127]
	ds_read_b128 v[172:175], v192 offset:19456
	global_load_lds_dwordx4 v192, s[44:45] offset:3072 sc1
	v_exp_f32_e32 v211, v75
	v_add_f32_e32 v210, 1.0, v210
	s_waitcnt lgkmcnt(2)
	v_mfma_f32_32x32x16_f16 v[96:111], a[24:27], v[176:179], v[96:111]
	ds_read_b128 v[176:179], v192 offset:20480
	v_exp_f32_e32 v212, v76
	v_add_f32_e32 v211, 1.0, v211
	v_mfma_f32_32x32x16_f16 v[112:127], a[24:27], v[180:183], v[112:127]
	ds_read_b128 v[180:183], v192 offset:21504
	v_exp_f32_e32 v213, v77
	v_add_f32_e32 v212, 1.0, v212
	v_mfma_f32_32x32x16_f16 v[96:111], a[28:31], v[184:187], v[96:111]
	ds_read_b128 v[184:187], v192 offset:22528
	v_exp_f32_e32 v214, v78
	v_add_f32_e32 v213, 1.0, v213
	v_mfma_f32_32x32x16_f16 v[112:127], a[28:31], v[188:191], v[112:127]
	ds_read_b128 v[188:191], v192 offset:23552
	s_mov_b32 m0, s57
	s_add_u32 s44, s34, 0x11000
	s_addc_u32 s45, s35, 0
	global_load_lds_dwordx4 v192, s[44:45] sc1
	v_exp_f32_e32 v215, v79
	v_add_f32_e32 v214, 1.0, v214
	v_mfma_f32_32x32x16_f16 v[96:111], a[32:35], v[160:163], v[96:111]
	ds_read_b128 v[160:163], v192 offset:24576
	v_add_f32_e32 v215, 1.0, v215
	v_rcp_f32_e32 v200, v200
	v_mfma_f32_32x32x16_f16 v[112:127], a[32:35], v[164:167], v[112:127]
	ds_read_b128 v[164:167], v192 offset:25600
	v_rcp_f32_e32 v201, v201
	s_waitcnt lgkmcnt(2)
	v_mfma_f32_32x32x16_f16 v[96:111], a[36:39], v[168:171], v[96:111]
	ds_read_b128 v[168:171], v192 offset:26624
	v_rcp_f32_e32 v202, v202
	v_mfma_f32_32x32x16_f16 v[112:127], a[36:39], v[172:175], v[112:127]
	ds_read_b128 v[172:175], v192 offset:27648
	global_load_lds_dwordx4 v192, s[44:45] offset:1024 sc1
	v_rcp_f32_e32 v203, v203
	v_mfma_f32_32x32x16_f16 v[96:111], a[40:43], v[176:179], v[96:111]
	ds_read_b128 v[176:179], v192 offset:28672
	v_rcp_f32_e32 v204, v204
	v_mfma_f32_32x32x16_f16 v[112:127], a[40:43], v[180:183], v[112:127]
	ds_read_b128 v[180:183], v192 offset:29696
	v_rcp_f32_e32 v205, v205
	v_mul_f32_e32 v204, v204, v144
	v_mfma_f32_32x32x16_f16 v[96:111], a[44:47], v[184:187], v[96:111]
	ds_read_b128 v[184:187], v192 offset:30720
	v_rcp_f32_e32 v206, v206
	v_mul_f32_e32 v205, v205, v145
	v_mfma_f32_32x32x16_f16 v[112:127], a[44:47], v[188:191], v[112:127]
	ds_read_b128 v[188:191], v192 offset:31744
	global_load_lds_dwordx4 v192, s[44:45] offset:2048 sc1
	v_rcp_f32_e32 v207, v207
	v_mul_f32_e32 v206, v206, v146
	s_waitcnt vmcnt(10)
	s_barrier
	s_waitcnt lgkmcnt(2)
	v_mfma_f32_32x32x16_f16 v[96:111], a[48:51], v[160:163], v[96:111]
	ds_read_b128 v[160:163], v192 offset:32768
	v_rcp_f32_e32 v208, v208
	v_mul_f32_e32 v207, v207, v147
	v_mfma_f32_32x32x16_f16 v[112:127], a[48:51], v[164:167], v[112:127]
	ds_read_b128 v[164:167], v192 offset:33792
	v_rcp_f32_e32 v209, v209
	v_fmamk_f32 v208, v208, 0xc0b8aa3b, v198
	v_mfma_f32_32x32x16_f16 v[96:111], a[52:55], v[168:171], v[96:111]
	ds_read_b128 v[168:171], v192 offset:34816
	v_rcp_f32_e32 v210, v210
	v_fmamk_f32 v209, v209, 0xc0b8aa3b, v198
	v_fma_f32 v144, v200, v208, v204
	v_mfma_f32_32x32x16_f16 v[112:127], a[52:55], v[172:175], v[112:127]
	ds_read_b128 v[172:175], v192 offset:35840
	global_load_lds_dwordx4 v192, s[44:45] offset:3072 sc1
	v_rcp_f32_e32 v211, v211
	v_fmamk_f32 v210, v210, 0xc0b8aa3b, v198
	v_fma_f32 v145, v201, v209, v205
	v_mfma_f32_32x32x16_f16 v[96:111], a[56:59], v[176:179], v[96:111]
	ds_read_b128 v[176:179], v192 offset:36864
	v_rcp_f32_e32 v212, v212
	v_fmamk_f32 v211, v211, 0xc0b8aa3b, v198
	v_fma_f32 v146, v202, v210, v206
	v_mfma_f32_32x32x16_f16 v[112:127], a[56:59], v[180:183], v[112:127]
	ds_read_b128 v[180:183], v192 offset:37888
	v_rcp_f32_e32 v213, v213
	v_fma_f32 v147, v203, v211, v207
	s_waitcnt lgkmcnt(2)
	v_mfma_f32_32x32x16_f16 v[96:111], a[60:63], v[184:187], v[96:111]
	ds_read_b128 v[184:187], v192 offset:38912
	v_rcp_f32_e32 v214, v214
	v_mfma_f32_32x32x16_f16 v[112:127], a[60:63], v[188:191], v[112:127]
	ds_read_b128 v[188:191], v192 offset:39936
	s_mov_b32 m0, s58
	s_add_u32 s44, s34, 0x18000
	s_addc_u32 s45, s35, 0
	global_load_lds_dwordx4 v192, s[44:45] sc1
	v_rcp_f32_e32 v215, v215
	v_mfma_f32_32x32x16_f16 v[96:111], a[64:67], v[160:163], v[96:111]
	ds_read_b128 v[160:163], v192 offset:40960
	v_exp_f32_e32 v200, v144
	v_mfma_f32_32x32x16_f16 v[112:127], a[64:67], v[164:167], v[112:127]
	ds_read_b128 v[164:167], v192 offset:41984
	v_exp_f32_e32 v201, v145
	v_add_f32_e32 v200, 1.0, v200
	v_mfma_f32_32x32x16_f16 v[96:111], a[68:71], v[168:171], v[96:111]
	ds_read_b128 v[168:171], v192 offset:43008
	v_exp_f32_e32 v202, v146
	v_add_f32_e32 v201, 1.0, v201
	v_mfma_f32_32x32x16_f16 v[112:127], a[68:71], v[172:175], v[112:127]
	ds_read_b128 v[172:175], v192 offset:44032
	global_load_lds_dwordx4 v192, s[44:45] offset:1024 sc1
	v_exp_f32_e32 v203, v147
	v_add_f32_e32 v202, 1.0, v202
	s_waitcnt lgkmcnt(2)
	v_mfma_f32_32x32x16_f16 v[96:111], a[72:75], v[176:179], v[96:111]
	ds_read_b128 v[176:179], v192 offset:45056
	v_add_f32_e32 v203, 1.0, v203
	v_rcp_f32_e32 v200, v200
	v_mfma_f32_32x32x16_f16 v[112:127], a[72:75], v[180:183], v[112:127]
	ds_read_b128 v[180:183], v192 offset:46080
	v_rcp_f32_e32 v201, v201
	v_fma_f32 v200, v200, 2.0, -1.0
	v_mfma_f32_32x32x16_f16 v[96:111], a[76:79], v[184:187], v[96:111]
	ds_read_b128 v[184:187], v192 offset:47104
	v_rcp_f32_e32 v202, v202
	v_fma_f32 v201, v201, 2.0, -1.0
	v_mul_f32_e32 v216, v212, v200
	v_mfma_f32_32x32x16_f16 v[112:127], a[76:79], v[188:191], v[112:127]
	ds_read_b128 v[188:191], v192 offset:48128
	global_load_lds_dwordx4 v192, s[44:45] offset:2048 sc1
	v_rcp_f32_e32 v203, v203
	v_fma_f32 v202, v202, 2.0, -1.0
	v_mul_f32_e32 v217, v213, v201
	v_mfma_f32_32x32x16_f16 v[96:111], a[80:83], v[160:163], v[96:111]
	ds_read_b128 v[160:163], v192 offset:49152
	v_fma_f32 v203, v203, 2.0, -1.0
	v_mul_f32_e32 v218, v214, v202
	v_exp_f32_e32 v200, v80
	v_mfma_f32_32x32x16_f16 v[112:127], a[80:83], v[164:167], v[112:127]
	ds_read_b128 v[164:167], v192 offset:50176
	v_mul_f32_e32 v219, v215, v203
	v_cvt_pk_f16_f32 v220, v216, v217
	v_exp_f32_e32 v201, v81
	s_waitcnt lgkmcnt(2)
	v_mfma_f32_32x32x16_f16 v[96:111], a[84:87], v[168:171], v[96:111]
	ds_read_b128 v[168:171], v192 offset:51200
	v_cvt_pk_f16_f32 v221, v218, v219
	v_exp_f32_e32 v202, v82
	v_add_f32_e32 v200, 1.0, v200
	v_mfma_f32_32x32x16_f16 v[112:127], a[84:87], v[172:175], v[112:127]
	ds_read_b128 v[172:175], v192 offset:52224
	global_load_lds_dwordx4 v192, s[44:45] offset:3072 sc1
	s_cmp_eq_u32 s33, s60
	s_cbranch_scc1 .LE_ht46
.LE_htb47:
	v_exp_f32_e32 v203, v83
	v_mfma_f32_32x32x16_f16 v[96:111], a[88:91], v[176:179], v[96:111]
	ds_read_b128 v[176:179], v192 offset:53248
	v_exp_f32_e32 v204, v84
	v_add_f32_e32 v201, 1.0, v201
	v_add_f32_e32 v202, 1.0, v202
	v_mfma_f32_32x32x16_f16 v[112:127], a[88:91], v[180:183], v[112:127]
	ds_read_b128 v[180:183], v192 offset:54272
	v_exp_f32_e32 v205, v85
	v_add_f32_e32 v203, 1.0, v203
	v_add_f32_e32 v204, 1.0, v204
	v_mfma_f32_32x32x16_f16 v[96:111], a[92:95], v[184:187], v[96:111]
	ds_read_b128 v[184:187], v192 offset:55296
	v_exp_f32_e32 v206, v86
	v_add_f32_e32 v205, 1.0, v205
	v_mfma_f32_32x32x16_f16 v[112:127], a[92:95], v[188:191], v[112:127]
	ds_read_b128 v[188:191], v192 offset:56320
	s_mov_b32 m0, s59
	s_add_u32 s44, s34, 0x19000
	s_addc_u32 s45, s35, 0
	global_load_lds_dwordx4 v192, s[44:45] sc1
	v_exp_f32_e32 v207, v87
	v_add_f32_e32 v206, 1.0, v206
	s_waitcnt lgkmcnt(2)
	v_mfma_f32_32x32x16_f16 v[96:111], a[96:99], v[160:163], v[96:111]
	ds_read_b128 v[160:163], v192 offset:57344
	v_exp_f32_e32 v208, v88
	v_add_f32_e32 v207, 1.0, v207
	v_mfma_f32_32x32x16_f16 v[112:127], a[96:99], v[164:167], v[112:127]
	ds_read_b128 v[164:167], v192 offset:58368
	v_exp_f32_e32 v209, v89
	v_add_f32_e32 v208, 1.0, v208
	v_mfma_f32_32x32x16_f16 v[96:111], a[100:103], v[168:171], v[96:111]
	ds_read_b128 v[168:171], v192 offset:59392
	v_exp_f32_e32 v210, v90
	v_add_f32_e32 v209, 1.0, v209
	v_mfma_f32_32x32x16_f16 v[112:127], a[100:103], v[172:175], v[112:127]
	ds_read_b128 v[172:175], v192 offset:60416
	global_load_lds_dwordx4 v192, s[44:45] offset:1024 sc1
	v_exp_f32_e32 v211, v91
	v_add_f32_e32 v210, 1.0, v210
	v_mfma_f32_32x32x16_f16 v[96:111], a[104:107], v[176:179], v[96:111]
	ds_read_b128 v[176:179], v192 offset:61440
	v_exp_f32_e32 v212, v92
	v_add_f32_e32 v211, 1.0, v211
	v_mfma_f32_32x32x16_f16 v[112:127], a[104:107], v[180:183], v[112:127]
	ds_read_b128 v[180:183], v192 offset:62464
	v_exp_f32_e32 v213, v93
	v_add_f32_e32 v212, 1.0, v212
	s_waitcnt lgkmcnt(2)
	v_mfma_f32_32x32x16_f16 v[96:111], a[108:111], v[184:187], v[96:111]
	ds_read_b128 v[184:187], v192 offset:63488
	v_exp_f32_e32 v214, v94
	v_add_f32_e32 v213, 1.0, v213
	v_mfma_f32_32x32x16_f16 v[112:127], a[108:111], v[188:191], v[112:127]
	ds_read_b128 v[188:191], v192 offset:64512
	global_load_lds_dwordx4 v192, s[44:45] offset:2048 sc1
	v_exp_f32_e32 v215, v95
	v_add_f32_e32 v214, 1.0, v214
	s_waitcnt vmcnt(7)
	s_barrier
	v_mfma_f32_32x32x16_f16 v[96:111], a[112:115], v[160:163], v[96:111]
	ds_read_b128 v[160:163], v193 offset:0
	v_add_f32_e32 v215, 1.0, v215
	v_rcp_f32_e32 v200, v200
	v_mfma_f32_32x32x16_f16 v[112:127], a[112:115], v[164:167], v[112:127]
	ds_read_b128 v[164:167], v193 offset:1024
	v_rcp_f32_e32 v201, v201
	v_mfma_f32_32x32x16_f16 v[96:111], a[116:119], v[168:171], v[96:111]
	ds_read_b128 v[168:171], v193 offset:2048
	v_rcp_f32_e32 v202, v202
	v_mfma_f32_32x32x16_f16 v[112:127], a[116:119], v[172:175], v[112:127]
	ds_read_b128 v[172:175], v193 offset:3072
	global_load_lds_dwordx4 v192, s[44:45] offset:3072 sc1
	v_rcp_f32_e32 v203, v203
	s_waitcnt lgkmcnt(2)
	v_mfma_f32_32x32x16_f16 v[96:111], a[120:123], v[176:179], v[96:111]
	ds_read_b128 v[176:179], v193 offset:4096
	v_rcp_f32_e32 v204, v204
	v_mfma_f32_32x32x16_f16 v[112:127], a[120:123], v[180:183], v[112:127]
	ds_read_b128 v[180:183], v193 offset:5120
	v_rcp_f32_e32 v205, v205
	v_mul_f32_e32 v204, v204, v148
	v_mfma_f32_32x32x2_f32 v[32:47], v248, v228, v[232:247]
	v_mfma_f32_32x32x16_f16 v[96:111], a[124:127], v[184:187], v[96:111]
	ds_read_b128 v[184:187], v193 offset:6144
	v_rcp_f32_e32 v206, v206
	v_mul_f32_e32 v205, v205, v149
	v_mfma_f32_32x32x2_f32 v[48:63], v248, v229, v[232:247]
	v_mfma_f32_32x32x16_f16 v[112:127], a[124:127], v[188:191], v[112:127]
	ds_read_b128 v[188:191], v193 offset:7168
	v_cmp_gt_u32_e32 vcc, 1, v251
	s_cbranch_vccnz .LE_tpoll49
.LE_tok48:
	s_and_b32 s64, s33, 1
	s_lshl_b32 s64, s64, 22
	s_add_u32 s64, s64, s49
	s_add_u32 s34, s6, s64
	s_addc_u32 s35, s7, 0
	s_mov_b32 m0, s52
	s_add_u32 s44, s34, 0x0
	s_addc_u32 s45, s35, 0
	global_load_lds_dwordx4 v192, s[44:45] sc1
	v_rcp_f32_e32 v207, v207
	v_mul_f32_e32 v206, v206, v150
	v_mfma_f32_32x32x16_f16 v[96:111], a[128:131], v[160:163], v[96:111]
	ds_read_b128 v[160:163], v193 offset:8192
	v_rcp_f32_e32 v208, v208
	v_mul_f32_e32 v207, v207, v151
	v_mfma_f32_32x32x16_f16 v[112:127], a[128:131], v[164:167], v[112:127]
	ds_read_b128 v[164:167], v193 offset:9216
	v_rcp_f32_e32 v209, v209
	v_fmamk_f32 v208, v208, 0xc0b8aa3b, v198
	s_waitcnt lgkmcnt(2)
	v_mfma_f32_32x32x16_f16 v[96:111], a[132:135], v[168:171], v[96:111]
	ds_read_b128 v[168:171], v193 offset:10240
	v_rcp_f32_e32 v210, v210
	v_fmamk_f32 v209, v209, 0xc0b8aa3b, v198
	v_fma_f32 v148, v200, v208, v204
	v_mfma_f32_32x32x16_f16 v[112:127], a[132:135], v[172:175], v[112:127]
	ds_read_b128 v[172:175], v193 offset:11264
	global_load_lds_dwordx4 v192, s[44:45] offset:1024 sc1
	v_rcp_f32_e32 v211, v211
	v_fmamk_f32 v210, v210, 0xc0b8aa3b, v198
	v_fma_f32 v149, v201, v209, v205
	v_mfma_f32_32x32x16_f16 v[96:111], a[136:139], v[176:179], v[96:111]
	ds_read_b128 v[176:179], v193 offset:12288
	v_rcp_f32_e32 v212, v212
	v_fmamk_f32 v211, v211, 0xc0b8aa3b, v198
	v_fma_f32 v150, v202, v210, v206
	v_mfma_f32_32x32x16_f16 v[112:127], a[136:139], v[180:183], v[112:127]
	ds_read_b128 v[180:183], v193 offset:13312
	v_rcp_f32_e32 v213, v213
	v_fma_f32 v151, v203, v211, v207
	v_mfma_f32_32x32x16_f16 v[96:111], a[140:143], v[184:187], v[96:111]
	ds_read_b128 v[184:187], v193 offset:14336
	v_rcp_f32_e32 v214, v214
	v_mfma_f32_32x32x16_f16 v[112:127], a[140:143], v[188:191], v[112:127]
	ds_read_b128 v[188:191], v193 offset:15360
	global_load_lds_dwordx4 v192, s[44:45] offset:2048 sc1
	v_rcp_f32_e32 v215, v215
	s_waitcnt lgkmcnt(2)
	v_mfma_f32_32x32x16_f16 v[96:111], a[144:147], v[160:163], v[96:111]
	ds_read_b128 v[160:163], v193 offset:16384
	v_exp_f32_e32 v200, v148
	v_mfma_f32_32x32x16_f16 v[112:127], a[144:147], v[164:167], v[112:127]
	ds_read_b128 v[164:167], v193 offset:17408
	v_exp_f32_e32 v201, v149
	v_add_f32_e32 v200, 1.0, v200
	v_mfma_f32_32x32x16_f16 v[96:111], a[148:151], v[168:171], v[96:111]
	ds_read_b128 v[168:171], v193 offset:18432
	v_exp_f32_e32 v202, v150
	v_add_f32_e32 v201, 1.0, v201
	v_mfma_f32_32x32x16_f16 v[112:127], a[148:151], v[172:175], v[112:127]
	ds_read_b128 v[172:175], v193 offset:19456
	global_load_lds_dwordx4 v192, s[44:45] offset:3072 sc1
	v_exp_f32_e32 v203, v151
	v_add_f32_e32 v202, 1.0, v202
	v_mfma_f32_32x32x16_f16 v[96:111], a[152:155], v[176:179], v[96:111]
	ds_read_b128 v[176:179], v193 offset:20480
	v_add_f32_e32 v203, 1.0, v203
	v_rcp_f32_e32 v200, v200
	v_mfma_f32_32x32x16_f16 v[112:127], a[152:155], v[180:183], v[112:127]
	ds_read_b128 v[180:183], v193 offset:21504
	v_rcp_f32_e32 v201, v201
	v_fma_f32 v200, v200, 2.0, -1.0
	s_waitcnt lgkmcnt(2)
	v_mfma_f32_32x32x16_f16 v[96:111], a[156:159], v[184:187], v[96:111]
	ds_read_b128 v[184:187], v193 offset:22528
	v_rcp_f32_e32 v202, v202
	v_fma_f32 v201, v201, 2.0, -1.0
	v_mul_f32_e32 v216, v212, v200
	v_mfma_f32_32x32x16_f16 v[112:127], a[156:159], v[188:191], v[112:127]
	ds_read_b128 v[188:191], v193 offset:23552
	s_mov_b32 m0, s53
	s_add_u32 s44, s34, 0x1000
	s_addc_u32 s45, s35, 0
	global_load_lds_dwordx4 v192, s[44:45] sc1
	v_rcp_f32_e32 v203, v203
	v_fma_f32 v202, v202, 2.0, -1.0
	v_mul_f32_e32 v217, v213, v201
	v_mfma_f32_32x32x16_f16 v[96:111], a[160:163], v[160:163], v[96:111]
	ds_read_b128 v[160:163], v193 offset:24576
	v_fma_f32 v203, v203, 2.0, -1.0
	v_mul_f32_e32 v218, v214, v202
	v_mfma_f32_32x32x16_f16 v[112:127], a[160:163], v[164:167], v[112:127]
	ds_read_b128 v[164:167], v193 offset:25600
	v_mul_f32_e32 v219, v215, v203
	v_cvt_pk_f16_f32 v222, v216, v217
	v_mfma_f32_32x32x16_f16 v[96:111], a[164:167], v[168:171], v[96:111]
	ds_read_b128 v[168:171], v193 offset:26624
	v_cvt_pk_f16_f32 v223, v218, v219
	v_mfma_f32_32x32x16_f16 v[112:127], a[164:167], v[172:175], v[112:127]
	ds_read_b128 v[172:175], v193 offset:27648
	global_load_lds_dwordx4 v192, s[44:45] offset:1024 sc1
	s_cmp_eq_u32 s33, s60
	s_cbranch_scc1 .LE_ht50
.LE_htb51:
	s_waitcnt lgkmcnt(2)
	v_mfma_f32_32x32x16_f16 v[96:111], a[168:171], v[176:179], v[96:111]
	ds_read_b128 v[176:179], v193 offset:28672
	s_nop 1
	v_permlane32_swap_b32_e32 v220, v222
	v_permlane32_swap_b32_e32 v221, v223
	s_cmp_eq_u32 s31, 0
	s_cbranch_scc1 .LE_slow52
	global_store_dwordx4 v195, v[220:223], s[36:37] offset:0
.LE_join53:
	v_mfma_f32_32x32x16_f16 v[112:127], a[168:171], v[180:183], v[112:127]
	ds_read_b128 v[180:183], v193 offset:29696
	v_mfma_f32_32x32x16_f16 v[96:111], a[172:175], v[184:187], v[96:111]
	ds_read_b128 v[184:187], v193 offset:30720
	v_mfma_f32_32x32x16_f16 v[112:127], a[172:175], v[188:191], v[112:127]
	ds_read_b128 v[188:191], v193 offset:31744
	global_load_lds_dwordx4 v192, s[44:45] offset:2048 sc1
	s_waitcnt vmcnt(8)
	s_barrier
	v_mfma_f32_32x32x16_f16 v[96:111], a[176:179], v[160:163], v[96:111]
	ds_read_b128 v[160:163], v193 offset:32768
	v_mfma_f32_32x32x16_f16 v[112:127], a[176:179], v[164:167], v[112:127]
	ds_read_b128 v[164:167], v193 offset:33792
	s_waitcnt lgkmcnt(2)
	v_mfma_f32_32x32x16_f16 v[96:111], a[180:183], v[168:171], v[96:111]
	ds_read_b128 v[168:171], v193 offset:34816
	v_mfma_f32_32x32x16_f16 v[112:127], a[180:183], v[172:175], v[112:127]
	ds_read_b128 v[172:175], v193 offset:35840
	global_load_lds_dwordx4 v192, s[44:45] offset:3072 sc1
	v_mfma_f32_32x32x16_f16 v[96:111], a[184:187], v[176:179], v[96:111]
	ds_read_b128 v[176:179], v193 offset:36864
	v_mfma_f32_32x32x16_f16 v[112:127], a[184:187], v[180:183], v[112:127]
	ds_read_b128 v[180:183], v193 offset:37888
	v_mfma_f32_32x32x16_f16 v[96:111], a[188:191], v[184:187], v[96:111]
	ds_read_b128 v[184:187], v193 offset:38912
	v_mfma_f32_32x32x16_f16 v[112:127], a[188:191], v[188:191], v[112:127]
	ds_read_b128 v[188:191], v193 offset:39936
	s_mov_b32 m0, s54
	s_add_u32 s44, s34, 0x8000
	s_addc_u32 s45, s35, 0
	global_load_lds_dwordx4 v192, s[44:45] sc1
	s_waitcnt lgkmcnt(2)
	v_mfma_f32_32x32x16_f16 v[96:111], a[192:195], v[160:163], v[96:111]
	ds_read_b128 v[160:163], v193 offset:40960
	v_mfma_f32_32x32x16_f16 v[112:127], a[192:195], v[164:167], v[112:127]
	ds_read_b128 v[164:167], v193 offset:41984
	s_waitcnt vmcnt(3)
	s_barrier
	v_mov_b32_e32 v199, 3
	s_cmp_eq_u32 s31, 0
	s_cbranch_scc1 .LE_slow54
	global_store_dword v197, v199, s[40:41]
.LE_join55:
	v_mfma_f32_32x32x16_f16 v[96:111], a[196:199], v[168:171], v[96:111]
	ds_read_b128 v[168:171], v193 offset:43008
	v_mfma_f32_32x32x16_f16 v[112:127], a[196:199], v[172:175], v[112:127]
	ds_read_b128 v[172:175], v193 offset:44032
	global_load_lds_dwordx4 v192, s[44:45] offset:1024 sc1
	v_mfma_f32_32x32x16_f16 v[96:111], a[200:203], v[176:179], v[96:111]
	ds_read_b128 v[176:179], v193 offset:45056
	v_mfma_f32_32x32x16_f16 v[112:127], a[200:203], v[180:183], v[112:127]
	ds_read_b128 v[180:183], v193 offset:46080
	s_waitcnt lgkmcnt(2)
	v_mfma_f32_32x32x16_f16 v[96:111], a[204:207], v[184:187], v[96:111]
	ds_read_b128 v[184:187], v193 offset:47104
	v_mfma_f32_32x32x16_f16 v[112:127], a[204:207], v[188:191], v[112:127]
	ds_read_b128 v[188:191], v193 offset:48128
	global_load_lds_dwordx4 v192, s[44:45] offset:2048 sc1
	v_mfma_f32_32x32x16_f16 v[96:111], a[208:211], v[160:163], v[96:111]
	ds_read_b128 v[160:163], v193 offset:49152
	v_mfma_f32_32x32x16_f16 v[112:127], a[208:211], v[164:167], v[112:127]
	ds_read_b128 v[164:167], v193 offset:50176
	v_mfma_f32_32x32x16_f16 v[96:111], a[212:215], v[168:171], v[96:111]
	ds_read_b128 v[168:171], v193 offset:51200
	v_mfma_f32_32x32x16_f16 v[112:127], a[212:215], v[172:175], v[112:127]
	ds_read_b128 v[172:175], v193 offset:52224
	global_load_lds_dwordx4 v192, s[44:45] offset:3072 sc1
	s_waitcnt lgkmcnt(2)
	v_mfma_f32_32x32x16_f16 v[96:111], a[216:219], v[176:179], v[96:111]
	ds_read_b128 v[176:179], v193 offset:53248
	v_mfma_f32_32x32x16_f16 v[112:127], a[216:219], v[180:183], v[112:127]
	ds_read_b128 v[180:183], v193 offset:54272
	v_mfma_f32_32x32x16_f16 v[96:111], a[220:223], v[184:187], v[96:111]
	ds_read_b128 v[184:187], v193 offset:55296
	v_mfma_f32_32x32x16_f16 v[112:127], a[220:223], v[188:191], v[112:127]
	ds_read_b128 v[188:191], v193 offset:56320
	s_mov_b32 m0, s55
	s_add_u32 s44, s34, 0x9000
	s_addc_u32 s45, s35, 0
	global_load_lds_dwordx4 v192, s[44:45] sc1
	v_mfma_f32_32x32x16_f16 v[96:111], a[224:227], v[160:163], v[96:111]
	ds_read_b128 v[160:163], v193 offset:57344
	v_mfma_f32_32x32x16_f16 v[112:127], a[224:227], v[164:167], v[112:127]
	ds_read_b128 v[164:167], v193 offset:58368
	s_waitcnt lgkmcnt(2)
	v_mfma_f32_32x32x16_f16 v[96:111], a[228:231], v[168:171], v[96:111]
	ds_read_b128 v[168:171], v193 offset:59392
	v_mfma_f32_32x32x16_f16 v[112:127], a[228:231], v[172:175], v[112:127]
	ds_read_b128 v[172:175], v193 offset:60416
	global_load_lds_dwordx4 v192, s[44:45] offset:1024 sc1
	v_mfma_f32_32x32x16_f16 v[96:111], a[232:235], v[176:179], v[96:111]
	ds_read_b128 v[176:179], v193 offset:61440
	v_mfma_f32_32x32x16_f16 v[112:127], a[232:235], v[180:183], v[112:127]
	ds_read_b128 v[180:183], v193 offset:62464
	v_mfma_f32_32x32x16_f16 v[96:111], a[236:239], v[184:187], v[96:111]
	ds_read_b128 v[184:187], v193 offset:63488
	v_mfma_f32_32x32x16_f16 v[112:127], a[236:239], v[188:191], v[112:127]
	ds_read_b128 v[188:191], v193 offset:64512
	global_load_lds_dwordx4 v192, s[44:45] offset:2048 sc1
	s_waitcnt vmcnt(8)
	s_barrier
	s_waitcnt lgkmcnt(2)
	v_mfma_f32_32x32x16_f16 v[96:111], a[240:243], v[160:163], v[96:111]
	ds_read_b128 v[160:163], v192 offset:0
	v_mfma_f32_32x32x16_f16 v[112:127], a[240:243], v[164:167], v[112:127]
	ds_read_b128 v[164:167], v192 offset:1024
	v_mfma_f32_32x32x16_f16 v[96:111], a[244:247], v[168:171], v[96:111]
	ds_read_b128 v[168:171], v192 offset:2048
	v_mfma_f32_32x32x16_f16 v[112:127], a[244:247], v[172:175], v[112:127]
	ds_read_b128 v[172:175], v192 offset:3072
	global_load_lds_dwordx4 v192, s[44:45] offset:3072 sc1
	v_mfma_f32_32x32x16_f16 v[96:111], a[248:251], v[176:179], v[96:111]
	ds_read_b128 v[176:179], v192 offset:4096
	v_mfma_f32_32x32x16_f16 v[112:127], a[248:251], v[180:183], v[112:127]
	ds_read_b128 v[180:183], v192 offset:5120
	s_waitcnt lgkmcnt(2)
	v_mfma_f32_32x32x16_f16 v[96:111], a[252:255], v[184:187], v[96:111]
	ds_read_b128 v[184:187], v192 offset:6144
	v_mfma_f32_32x32x16_f16 v[112:127], a[252:255], v[188:191], v[112:127]
	ds_read_b128 v[188:191], v192 offset:7168
	s_mov_b32 m0, s56
	s_add_u32 s44, s34, 0x10000
	s_addc_u32 s45, s35, 0
	global_load_lds_dwordx4 v192, s[44:45] sc1
	s_add_u32 s33, s33, 1
	s_cmp_lt_u32 s33, s28
	s_cbranch_scc1 .LE_loop16

.LD_loop16:
	s_sub_u32 s71, s33, 1
	s_add_u32 s61, s33, 1
	s_min_u32 s61, s61, s60
	s_and_b32 s64, s71, 1
	s_lshl_b32 s64, s64, 22
	s_add_u32 s64, s64, s50
	s_add_u32 s64, s64, 0x60000
	s_add_u32 s36, s6, s64
	s_addc_u32 s37, s7, 0
	s_lshl_b32 s64, s71, 3
	s_add_u32 s64, s64, s29
	s_lshl_b32 s64, s64, 5
	s_add_u32 s64, s64, s30
	s_lshl_b32 s64, s64, 2
	s_add_u32 s40, s8, s64
	s_addc_u32 s41, s9, 0
	s_lshl_b32 s64, s71, 19
	s_add_u32 s64, s64, 0x600
	s_add_u32 s72, s62, s64
	s_addc_u32 s73, s63, 0
	s_nop 3
	s_waitcnt lgkmcnt(2)
	v_mfma_f32_32x32x16_f16 v[0:15], a[0:3], v[160:163], v[0:15]
	ds_read_b128 v[160:163], v192 offset:8192
	v_exp_f32_e32 v200, v96
	v_mfma_f32_32x32x16_f16 v[16:31], a[0:3], v[164:167], v[16:31]
	ds_read_b128 v[164:167], v192 offset:9216
	s_lshl_b32 s64, s71, 3
	s_add_u32 s64, s64, s29
	s_lshl_b32 s64, s64, 7
	s_add_u32 s38, s8, s64
	s_addc_u32 s39, s9, 0
	global_load_dword v251, v196, s[38:39] sc1
	v_exp_f32_e32 v201, v97
	v_add_f32_e32 v200, 1.0, v200
	v_mfma_f32_32x32x16_f16 v[0:15], a[4:7], v[168:171], v[0:15]
	ds_read_b128 v[168:171], v192 offset:10240
	v_exp_f32_e32 v202, v98
	v_add_f32_e32 v201, 1.0, v201
	v_mfma_f32_32x32x16_f16 v[16:31], a[4:7], v[172:175], v[16:31]
	ds_read_b128 v[172:175], v192 offset:11264
	global_load_lds_dwordx4 v192, s[44:45] offset:1024 sc1
	v_exp_f32_e32 v203, v99
	v_add_f32_e32 v202, 1.0, v202
	v_mfma_f32_32x32x16_f16 v[0:15], a[8:11], v[176:179], v[0:15]
	ds_read_b128 v[176:179], v192 offset:12288
	v_exp_f32_e32 v204, v100
	v_add_f32_e32 v203, 1.0, v203
	v_mfma_f32_32x32x16_f16 v[16:31], a[8:11], v[180:183], v[16:31]
	ds_read_b128 v[180:183], v192 offset:13312
	v_exp_f32_e32 v205, v101
	v_add_f32_e32 v204, 1.0, v204
	s_waitcnt lgkmcnt(2)
	v_mfma_f32_32x32x16_f16 v[0:15], a[12:15], v[184:187], v[0:15]
	ds_read_b128 v[184:187], v192 offset:14336
	v_exp_f32_e32 v206, v102
	v_add_f32_e32 v205, 1.0, v205
	v_mfma_f32_32x32x16_f16 v[16:31], a[12:15], v[188:191], v[16:31]
	ds_read_b128 v[188:191], v192 offset:15360
	global_load_lds_dwordx4 v192, s[44:45] offset:2048 sc1
	v_exp_f32_e32 v207, v103
	v_add_f32_e32 v206, 1.0, v206
	v_mfma_f32_32x32x16_f16 v[0:15], a[16:19], v[160:163], v[0:15]
	ds_read_b128 v[160:163], v192 offset:16384
	v_exp_f32_e32 v208, v104
	v_add_f32_e32 v207, 1.0, v207
	v_mfma_f32_32x32x16_f16 v[16:31], a[16:19], v[164:167], v[16:31]
	ds_read_b128 v[164:167], v192 offset:17408
	v_exp_f32_e32 v209, v105
	v_add_f32_e32 v208, 1.0, v208
	v_mfma_f32_32x32x16_f16 v[0:15], a[20:23], v[168:171], v[0:15]
	ds_read_b128 v[168:171], v192 offset:18432
	v_exp_f32_e32 v210, v106
	v_add_f32_e32 v209, 1.0, v209
	v_mfma_f32_32x32x16_f16 v[16:31], a[20:23], v[172:175], v[16:31]
	ds_read_b128 v[172:175], v192 offset:19456
	global_load_lds_dwordx4 v192, s[44:45] offset:3072 sc1
	v_exp_f32_e32 v211, v107
	v_add_f32_e32 v210, 1.0, v210
	s_waitcnt lgkmcnt(2)
	v_mfma_f32_32x32x16_f16 v[0:15], a[24:27], v[176:179], v[0:15]
	ds_read_b128 v[176:179], v192 offset:20480
	v_exp_f32_e32 v212, v108
	v_add_f32_e32 v211, 1.0, v211
	v_mfma_f32_32x32x16_f16 v[16:31], a[24:27], v[180:183], v[16:31]
	ds_read_b128 v[180:183], v192 offset:21504
	v_exp_f32_e32 v213, v109
	v_add_f32_e32 v212, 1.0, v212
	v_mfma_f32_32x32x16_f16 v[0:15], a[28:31], v[184:187], v[0:15]
	ds_read_b128 v[184:187], v192 offset:22528
	v_exp_f32_e32 v214, v110
	v_add_f32_e32 v213, 1.0, v213
	v_mfma_f32_32x32x16_f16 v[16:31], a[28:31], v[188:191], v[16:31]
	ds_read_b128 v[188:191], v192 offset:23552
	s_mov_b32 m0, s57
	s_add_u32 s44, s34, 0x11000
	s_addc_u32 s45, s35, 0
	global_load_lds_dwordx4 v192, s[44:45] sc1
	v_exp_f32_e32 v215, v111
	v_add_f32_e32 v214, 1.0, v214
	v_mfma_f32_32x32x16_f16 v[0:15], a[32:35], v[160:163], v[0:15]
	ds_read_b128 v[160:163], v192 offset:24576
	v_add_f32_e32 v215, 1.0, v215
	v_rcp_f32_e32 v200, v200
	v_mfma_f32_32x32x16_f16 v[16:31], a[32:35], v[164:167], v[16:31]
	ds_read_b128 v[164:167], v192 offset:25600
	v_rcp_f32_e32 v201, v201
	s_waitcnt lgkmcnt(2)
	v_mfma_f32_32x32x16_f16 v[0:15], a[36:39], v[168:171], v[0:15]
	ds_read_b128 v[168:171], v192 offset:26624
	v_rcp_f32_e32 v202, v202
	v_mfma_f32_32x32x16_f16 v[16:31], a[36:39], v[172:175], v[16:31]
	ds_read_b128 v[172:175], v192 offset:27648
	global_load_lds_dwordx4 v192, s[44:45] offset:1024 sc1
	v_rcp_f32_e32 v203, v203
	v_mfma_f32_32x32x16_f16 v[0:15], a[40:43], v[176:179], v[0:15]
	ds_read_b128 v[176:179], v192 offset:28672
	v_rcp_f32_e32 v204, v204
	v_mfma_f32_32x32x16_f16 v[16:31], a[40:43], v[180:183], v[16:31]
	ds_read_b128 v[180:183], v192 offset:29696
	v_rcp_f32_e32 v205, v205
	v_mul_f32_e32 v204, v204, v152
	v_mfma_f32_32x32x16_f16 v[0:15], a[44:47], v[184:187], v[0:15]
	ds_read_b128 v[184:187], v192 offset:30720
	v_rcp_f32_e32 v206, v206
	v_mul_f32_e32 v205, v205, v153
	v_mfma_f32_32x32x16_f16 v[16:31], a[44:47], v[188:191], v[16:31]
	ds_read_b128 v[188:191], v192 offset:31744
	global_load_lds_dwordx4 v192, s[44:45] offset:2048 sc1
	v_rcp_f32_e32 v207, v207
	v_mul_f32_e32 v206, v206, v154
	s_waitcnt vmcnt(8)
	s_barrier
	s_waitcnt lgkmcnt(2)
	v_mfma_f32_32x32x16_f16 v[0:15], a[48:51], v[160:163], v[0:15]
	ds_read_b128 v[160:163], v192 offset:32768
	v_rcp_f32_e32 v208, v208
	v_mul_f32_e32 v207, v207, v155
	v_mfma_f32_32x32x16_f16 v[16:31], a[48:51], v[164:167], v[16:31]
	ds_read_b128 v[164:167], v192 offset:33792
	v_rcp_f32_e32 v209, v209
	v_fmamk_f32 v208, v208, 0xc0b8aa3b, v198
	v_mfma_f32_32x32x16_f16 v[0:15], a[52:55], v[168:171], v[0:15]
	ds_read_b128 v[168:171], v192 offset:34816
	v_rcp_f32_e32 v210, v210
	v_fmamk_f32 v209, v209, 0xc0b8aa3b, v198
	v_fma_f32 v152, v200, v208, v204
	v_mfma_f32_32x32x16_f16 v[16:31], a[52:55], v[172:175], v[16:31]
	ds_read_b128 v[172:175], v192 offset:35840
	global_load_lds_dwordx4 v192, s[44:45] offset:3072 sc1
	v_rcp_f32_e32 v211, v211
	v_fmamk_f32 v210, v210, 0xc0b8aa3b, v198
	v_fma_f32 v153, v201, v209, v205
	v_mfma_f32_32x32x16_f16 v[0:15], a[56:59], v[176:179], v[0:15]
	ds_read_b128 v[176:179], v192 offset:36864
	v_rcp_f32_e32 v212, v212
	v_fmamk_f32 v211, v211, 0xc0b8aa3b, v198
	v_fma_f32 v154, v202, v210, v206
	v_mfma_f32_32x32x16_f16 v[16:31], a[56:59], v[180:183], v[16:31]
	ds_read_b128 v[180:183], v192 offset:37888
	v_rcp_f32_e32 v213, v213
	v_fma_f32 v155, v203, v211, v207
	s_waitcnt lgkmcnt(2)
	v_mfma_f32_32x32x16_f16 v[0:15], a[60:63], v[184:187], v[0:15]
	ds_read_b128 v[184:187], v192 offset:38912
	v_rcp_f32_e32 v214, v214
	v_mfma_f32_32x32x16_f16 v[16:31], a[60:63], v[188:191], v[16:31]
	ds_read_b128 v[188:191], v192 offset:39936
	s_mov_b32 m0, s58
	s_add_u32 s44, s34, 0x18000
	s_addc_u32 s45, s35, 0
	global_load_lds_dwordx4 v192, s[44:45] sc1
	v_rcp_f32_e32 v215, v215
	v_mfma_f32_32x32x16_f16 v[0:15], a[64:67], v[160:163], v[0:15]
	ds_read_b128 v[160:163], v192 offset:40960
	v_exp_f32_e32 v200, v152
	v_mfma_f32_32x32x16_f16 v[16:31], a[64:67], v[164:167], v[16:31]
	ds_read_b128 v[164:167], v192 offset:41984
	v_exp_f32_e32 v201, v153
	v_add_f32_e32 v200, 1.0, v200
	v_mfma_f32_32x32x16_f16 v[0:15], a[68:71], v[168:171], v[0:15]
	ds_read_b128 v[168:171], v192 offset:43008
	v_exp_f32_e32 v202, v154
	v_add_f32_e32 v201, 1.0, v201
	v_mfma_f32_32x32x16_f16 v[16:31], a[68:71], v[172:175], v[16:31]
	ds_read_b128 v[172:175], v192 offset:44032
	global_load_lds_dwordx4 v192, s[44:45] offset:1024 sc1
	v_exp_f32_e32 v203, v155
	v_add_f32_e32 v202, 1.0, v202
	s_waitcnt lgkmcnt(2)
	v_mfma_f32_32x32x16_f16 v[0:15], a[72:75], v[176:179], v[0:15]
	ds_read_b128 v[176:179], v192 offset:45056
	v_add_f32_e32 v203, 1.0, v203
	v_rcp_f32_e32 v200, v200
	v_mfma_f32_32x32x16_f16 v[16:31], a[72:75], v[180:183], v[16:31]
	ds_read_b128 v[180:183], v192 offset:46080
	v_rcp_f32_e32 v201, v201
	v_fma_f32 v200, v200, 2.0, -1.0
	v_mfma_f32_32x32x16_f16 v[0:15], a[76:79], v[184:187], v[0:15]
	ds_read_b128 v[184:187], v192 offset:47104
	v_rcp_f32_e32 v202, v202
	v_fma_f32 v201, v201, 2.0, -1.0
	v_mul_f32_e32 v216, v212, v200
	v_mfma_f32_32x32x16_f16 v[16:31], a[76:79], v[188:191], v[16:31]
	ds_read_b128 v[188:191], v192 offset:48128
	global_load_lds_dwordx4 v192, s[44:45] offset:2048 sc1
	v_rcp_f32_e32 v203, v203
	v_fma_f32 v202, v202, 2.0, -1.0
	v_mul_f32_e32 v217, v213, v201
	v_mfma_f32_32x32x16_f16 v[0:15], a[80:83], v[160:163], v[0:15]
	ds_read_b128 v[160:163], v192 offset:49152
	v_fma_f32 v203, v203, 2.0, -1.0
	v_mul_f32_e32 v218, v214, v202
	v_exp_f32_e32 v200, v112
	v_mfma_f32_32x32x16_f16 v[16:31], a[80:83], v[164:167], v[16:31]
	ds_read_b128 v[164:167], v192 offset:50176
	v_mul_f32_e32 v219, v215, v203
	v_mul_f32_e32 v236, v216, v228
	v_exp_f32_e32 v201, v113
	s_waitcnt lgkmcnt(2)
	v_mfma_f32_32x32x16_f16 v[0:15], a[84:87], v[168:171], v[0:15]
	ds_read_b128 v[168:171], v192 offset:51200
	v_mul_f32_e32 v237, v216, v232
	v_fmac_f32_e32 v236, v217, v229
	v_exp_f32_e32 v202, v114
	v_mfma_f32_32x32x16_f16 v[16:31], a[84:87], v[172:175], v[16:31]
	ds_read_b128 v[172:175], v192 offset:52224
	global_load_lds_dwordx4 v192, s[44:45] offset:3072 sc1
	v_fmac_f32_e32 v237, v217, v233
	v_fmac_f32_e32 v236, v218, v230
	v_exp_f32_e32 v203, v115
	v_mfma_f32_32x32x16_f16 v[0:15], a[88:91], v[176:179], v[0:15]
	ds_read_b128 v[176:179], v192 offset:53248
	v_fmac_f32_e32 v237, v218, v234
	v_fmac_f32_e32 v236, v219, v231
	v_exp_f32_e32 v204, v116
	v_mfma_f32_32x32x16_f16 v[16:31], a[88:91], v[180:183], v[16:31]
	ds_read_b128 v[180:183], v192 offset:54272
	v_fmac_f32_e32 v237, v219, v235
	v_mov_b32_e32 v238, v236
	v_exp_f32_e32 v205, v117
	v_mfma_f32_32x32x16_f16 v[0:15], a[92:95], v[184:187], v[0:15]
	ds_read_b128 v[184:187], v192 offset:55296
	v_mov_b32_e32 v239, v236
	v_mov_b32_e32 v240, v237
	v_exp_f32_e32 v206, v118
	v_mfma_f32_32x32x16_f16 v[16:31], a[92:95], v[188:191], v[16:31]
	ds_read_b128 v[188:191], v192 offset:56320
	s_mov_b32 m0, s59
	s_add_u32 s44, s34, 0x19000
	s_addc_u32 s45, s35, 0
	global_load_lds_dwordx4 v192, s[44:45] sc1
	v_mov_b32_e32 v241, v237
	v_cvt_pk_f16_f32 v220, v216, v217
	v_exp_f32_e32 v207, v119
	s_waitcnt lgkmcnt(2)
	v_mfma_f32_32x32x16_f16 v[0:15], a[96:99], v[160:163], v[0:15]
	ds_read_b128 v[160:163], v192 offset:57344
	s_nop 1
	v_permlane32_swap_b32_e32 v238, v239
	v_permlane32_swap_b32_e32 v240, v241
	v_add_f32_e32 v238, v238, v239
	v_add_f32_e32 v239, v240, v241
	ds_write_b64 v248, v[238:239] offset:1536
	v_exp_f32_e32 v208, v120
	v_mfma_f32_32x32x16_f16 v[16:31], a[96:99], v[164:167], v[16:31]
	ds_read_b128 v[164:167], v192 offset:58368
	v_cvt_pk_f16_f32 v221, v218, v219
	v_exp_f32_e32 v209, v121
	v_add_f32_e32 v200, 1.0, v200
	v_mfma_f32_32x32x16_f16 v[0:15], a[100:103], v[168:171], v[0:15]
	ds_read_b128 v[168:171], v192 offset:59392
	v_exp_f32_e32 v210, v122
	v_add_f32_e32 v201, 1.0, v201
	v_add_f32_e32 v202, 1.0, v202
	v_mfma_f32_32x32x16_f16 v[16:31], a[100:103], v[172:175], v[16:31]
	ds_read_b128 v[172:175], v192 offset:60416
	global_load_lds_dwordx4 v192, s[44:45] offset:1024 sc1
	v_exp_f32_e32 v211, v123
	v_add_f32_e32 v203, 1.0, v203
	v_add_f32_e32 v204, 1.0, v204
	v_mfma_f32_32x32x16_f16 v[0:15], a[104:107], v[176:179], v[0:15]
	ds_read_b128 v[176:179], v192 offset:61440
	v_exp_f32_e32 v212, v124
	v_add_f32_e32 v205, 1.0, v205
	v_add_f32_e32 v206, 1.0, v206
	v_mfma_f32_32x32x16_f16 v[16:31], a[104:107], v[180:183], v[16:31]
	ds_read_b128 v[180:183], v192 offset:62464
	v_exp_f32_e32 v213, v125
	v_add_f32_e32 v207, 1.0, v207
	v_add_f32_e32 v208, 1.0, v208
	s_waitcnt lgkmcnt(2)
	v_mfma_f32_32x32x16_f16 v[0:15], a[108:111], v[184:187], v[0:15]
	ds_read_b128 v[184:187], v192 offset:63488
	v_exp_f32_e32 v214, v126
	v_add_f32_e32 v209, 1.0, v209
	v_add_f32_e32 v210, 1.0, v210
	v_mfma_f32_32x32x16_f16 v[16:31], a[108:111], v[188:191], v[16:31]
	ds_read_b128 v[188:191], v192 offset:64512
	global_load_lds_dwordx4 v192, s[44:45] offset:2048 sc1
	v_exp_f32_e32 v215, v127
	v_add_f32_e32 v211, 1.0, v211
	v_add_f32_e32 v212, 1.0, v212
	s_waitcnt vmcnt(7)
	s_barrier
	v_mfma_f32_32x32x16_f16 v[0:15], a[112:115], v[160:163], v[0:15]
	ds_read_b128 v[160:163], v193 offset:0
	v_add_f32_e32 v213, 1.0, v213
	v_add_f32_e32 v214, 1.0, v214
	v_rcp_f32_e32 v200, v200
	v_mfma_f32_32x32x16_f16 v[16:31], a[112:115], v[164:167], v[16:31]
	ds_read_b128 v[164:167], v193 offset:1024
	v_add_f32_e32 v215, 1.0, v215
	v_rcp_f32_e32 v201, v201
	v_mfma_f32_32x32x16_f16 v[0:15], a[116:119], v[168:171], v[0:15]
	ds_read_b128 v[168:171], v193 offset:2048
	v_rcp_f32_e32 v202, v202
	v_mfma_f32_32x32x16_f16 v[16:31], a[116:119], v[172:175], v[16:31]
	ds_read_b128 v[172:175], v193 offset:3072
	global_load_lds_dwordx4 v192, s[44:45] offset:3072 sc1
	v_rcp_f32_e32 v203, v203
	s_waitcnt lgkmcnt(2)
	v_mfma_f32_32x32x16_f16 v[0:15], a[120:123], v[176:179], v[0:15]
	ds_read_b128 v[176:179], v193 offset:4096
	v_rcp_f32_e32 v204, v204
	s_add_u32 s46, s42, 0x4000
	s_addc_u32 s47, s43, 0
	global_load_dwordx4 v[64:67], v192, s[46:47] offset:0
	v_mfma_f32_32x32x16_f16 v[16:31], a[120:123], v[180:183], v[16:31]
	ds_read_b128 v[180:183], v193 offset:5120
	v_rcp_f32_e32 v205, v205
	v_mul_f32_e32 v204, v204, v156
	global_load_dwordx4 v[68:71], v192, s[46:47] offset:1024
	global_load_dwordx4 v[72:75], v192, s[46:47] offset:2048
	v_mfma_f32_32x32x16_f16 v[0:15], a[124:127], v[184:187], v[0:15]
	ds_read_b128 v[184:187], v193 offset:6144
	v_rcp_f32_e32 v206, v206
	v_mul_f32_e32 v205, v205, v157
	global_load_dwordx4 v[76:79], v192, s[46:47] offset:3072
	s_add_u32 s46, s42, 0x5000
	s_addc_u32 s47, s43, 0
	v_mfma_f32_32x32x16_f16 v[16:31], a[124:127], v[188:191], v[16:31]
	ds_read_b128 v[188:191], v193 offset:7168
	v_cmp_gt_u32_e32 vcc, 2, v251
	s_cbranch_vccnz .LD_tpoll21
.LD_tok20:
	s_and_b32 s64, s71, 1
	s_lshl_b32 s64, s64, 22
	s_add_u32 s64, s64, s49
	s_add_u32 s64, s64, 0x20000
	s_add_u32 s34, s6, s64
	s_addc_u32 s35, s7, 0
	s_mov_b32 m0, s52
	s_add_u32 s44, s34, 0x0
	s_addc_u32 s45, s35, 0
	global_load_lds_dwordx4 v192, s[44:45] sc1
	v_rcp_f32_e32 v207, v207
	v_mul_f32_e32 v206, v206, v158
	global_load_dwordx4 v[80:83], v192, s[46:47] offset:0
	global_load_dwordx4 v[84:87], v192, s[46:47] offset:1024
	v_mfma_f32_32x32x16_f16 v[0:15], a[128:131], v[160:163], v[0:15]
	ds_read_b128 v[160:163], v193 offset:8192
	v_rcp_f32_e32 v208, v208
	v_mul_f32_e32 v207, v207, v159
	global_load_dwordx4 v[88:91], v192, s[46:47] offset:2048
	global_load_dwordx4 v[92:95], v192, s[46:47] offset:3072
	v_mfma_f32_32x32x16_f16 v[16:31], a[128:131], v[164:167], v[16:31]
	ds_read_b128 v[164:167], v193 offset:9216
	v_rcp_f32_e32 v209, v209
	v_fmamk_f32 v208, v208, 0xc0b8aa3b, v198
	s_waitcnt lgkmcnt(2)
	v_mfma_f32_32x32x16_f16 v[0:15], a[132:135], v[168:171], v[0:15]
	ds_read_b128 v[168:171], v193 offset:10240
	v_rcp_f32_e32 v210, v210
	v_fmamk_f32 v209, v209, 0xc0b8aa3b, v198
	v_fma_f32 v156, v200, v208, v204
	v_mfma_f32_32x32x16_f16 v[16:31], a[132:135], v[172:175], v[16:31]
	ds_read_b128 v[172:175], v193 offset:11264
	global_load_lds_dwordx4 v192, s[44:45] offset:1024 sc1
	v_rcp_f32_e32 v211, v211
	v_fmamk_f32 v210, v210, 0xc0b8aa3b, v198
	v_fma_f32 v157, v201, v209, v205
	v_mfma_f32_32x32x16_f16 v[0:15], a[136:139], v[176:179], v[0:15]
	ds_read_b128 v[176:179], v193 offset:12288
	v_rcp_f32_e32 v212, v212
	v_fmamk_f32 v211, v211, 0xc0b8aa3b, v198
	v_fma_f32 v158, v202, v210, v206
	v_mfma_f32_32x32x16_f16 v[16:31], a[136:139], v[180:183], v[16:31]
	ds_read_b128 v[180:183], v193 offset:13312
	v_rcp_f32_e32 v213, v213
	v_fma_f32 v159, v203, v211, v207
	v_mfma_f32_32x32x16_f16 v[0:15], a[140:143], v[184:187], v[0:15]
	ds_read_b128 v[184:187], v193 offset:14336
	v_rcp_f32_e32 v214, v214
	v_mfma_f32_32x32x16_f16 v[16:31], a[140:143], v[188:191], v[16:31]
	ds_read_b128 v[188:191], v193 offset:15360
	global_load_lds_dwordx4 v192, s[44:45] offset:2048 sc1
	v_rcp_f32_e32 v215, v215
	s_waitcnt lgkmcnt(2)
	v_mfma_f32_32x32x16_f16 v[0:15], a[144:147], v[160:163], v[0:15]
	ds_read_b128 v[160:163], v193 offset:16384
	v_exp_f32_e32 v200, v156
	v_mfma_f32_32x32x16_f16 v[16:31], a[144:147], v[164:167], v[16:31]
	ds_read_b128 v[164:167], v193 offset:17408
	v_exp_f32_e32 v201, v157
	v_add_f32_e32 v200, 1.0, v200
	v_mfma_f32_32x32x16_f16 v[0:15], a[148:151], v[168:171], v[0:15]
	ds_read_b128 v[168:171], v193 offset:18432
	v_exp_f32_e32 v202, v158
	v_add_f32_e32 v201, 1.0, v201
	v_mfma_f32_32x32x16_f16 v[16:31], a[148:151], v[172:175], v[16:31]
	ds_read_b128 v[172:175], v193 offset:19456
	global_load_lds_dwordx4 v192, s[44:45] offset:3072 sc1
	v_exp_f32_e32 v203, v159
	v_add_f32_e32 v202, 1.0, v202
	v_mfma_f32_32x32x16_f16 v[0:15], a[152:155], v[176:179], v[0:15]
	ds_read_b128 v[176:179], v193 offset:20480
	v_add_f32_e32 v203, 1.0, v203
	v_rcp_f32_e32 v200, v200
	v_mfma_f32_32x32x16_f16 v[16:31], a[152:155], v[180:183], v[16:31]
	ds_read_b128 v[180:183], v193 offset:21504
	v_rcp_f32_e32 v201, v201
	v_fma_f32 v200, v200, 2.0, -1.0
	s_waitcnt lgkmcnt(2)
	v_mfma_f32_32x32x16_f16 v[0:15], a[156:159], v[184:187], v[0:15]
	ds_read_b128 v[184:187], v193 offset:22528
	v_rcp_f32_e32 v202, v202
	v_fma_f32 v201, v201, 2.0, -1.0
	v_mul_f32_e32 v216, v212, v200
	v_mfma_f32_32x32x16_f16 v[16:31], a[156:159], v[188:191], v[16:31]
	ds_read_b128 v[188:191], v193 offset:23552
	s_mov_b32 m0, s53
	s_add_u32 s44, s34, 0x1000
	s_addc_u32 s45, s35, 0
	global_load_lds_dwordx4 v192, s[44:45] sc1
	v_rcp_f32_e32 v203, v203
	v_fma_f32 v202, v202, 2.0, -1.0
	v_mul_f32_e32 v217, v213, v201
	v_mfma_f32_32x32x16_f16 v[0:15], a[160:163], v[160:163], v[0:15]
	ds_read_b128 v[160:163], v193 offset:24576
	v_fma_f32 v203, v203, 2.0, -1.0
	v_mul_f32_e32 v218, v214, v202
	v_mfma_f32_32x32x16_f16 v[16:31], a[160:163], v[164:167], v[16:31]
	ds_read_b128 v[164:167], v193 offset:25600
	v_mul_f32_e32 v219, v215, v203
	v_mul_f32_e32 v236, v216, v228
	v_mfma_f32_32x32x16_f16 v[0:15], a[164:167], v[168:171], v[0:15]
	ds_read_b128 v[168:171], v193 offset:26624
	v_mul_f32_e32 v237, v216, v232
	v_fmac_f32_e32 v236, v217, v229
	v_mfma_f32_32x32x16_f16 v[16:31], a[164:167], v[172:175], v[16:31]
	ds_read_b128 v[172:175], v193 offset:27648
	global_load_lds_dwordx4 v192, s[44:45] offset:1024 sc1
	v_fmac_f32_e32 v237, v217, v233
	v_fmac_f32_e32 v236, v218, v230
	s_waitcnt lgkmcnt(2)
	v_mfma_f32_32x32x16_f16 v[0:15], a[168:171], v[176:179], v[0:15]
	ds_read_b128 v[176:179], v193 offset:28672
	v_fmac_f32_e32 v237, v218, v234
	v_fmac_f32_e32 v236, v219, v231
	v_mfma_f32_32x32x16_f16 v[16:31], a[168:171], v[180:183], v[16:31]
	ds_read_b128 v[180:183], v193 offset:29696
	v_fmac_f32_e32 v237, v219, v235
	v_mov_b32_e32 v238, v236
	v_mfma_f32_32x32x16_f16 v[0:15], a[172:175], v[184:187], v[0:15]
	ds_read_b128 v[184:187], v193 offset:30720
	v_mov_b32_e32 v239, v236
	v_mov_b32_e32 v240, v237
	v_mfma_f32_32x32x16_f16 v[16:31], a[172:175], v[188:191], v[16:31]
	ds_read_b128 v[188:191], v193 offset:31744
	global_load_lds_dwordx4 v192, s[44:45] offset:2048 sc1
	v_mov_b32_e32 v241, v237
	v_cvt_pk_f16_f32 v222, v216, v217
	s_waitcnt vmcnt(15)
	s_barrier
	v_mfma_f32_32x32x16_f16 v[0:15], a[176:179], v[160:163], v[0:15]
	ds_read_b128 v[160:163], v193 offset:32768
	s_nop 1
	v_permlane32_swap_b32_e32 v238, v239
	v_permlane32_swap_b32_e32 v240, v241
	v_add_f32_e32 v238, v238, v239
	v_add_f32_e32 v239, v240, v241
	ds_write_b64 v248, v[238:239] offset:1792
	v_mfma_f32_32x32x16_f16 v[16:31], a[176:179], v[164:167], v[16:31]
	ds_read_b128 v[164:167], v193 offset:33792
	v_cvt_pk_f16_f32 v223, v218, v219
	s_waitcnt lgkmcnt(3)
	v_mfma_f32_32x32x16_f16 v[0:15], a[180:183], v[168:171], v[0:15]
	ds_read_b128 v[168:171], v193 offset:34816
	s_nop 1
	v_permlane32_swap_b32_e32 v220, v222
	v_permlane32_swap_b32_e32 v221, v223
	s_cmp_eq_u32 s31, 0
	s_cbranch_scc1 .LD_slow22
	global_store_dwordx4 v195, v[220:223], s[36:37] offset:0
.LD_join23:
	v_mfma_f32_32x32x16_f16 v[16:31], a[180:183], v[172:175], v[16:31]
	ds_read_b128 v[172:175], v193 offset:35840
	global_load_lds_dwordx4 v192, s[44:45] offset:3072 sc1
	v_mfma_f32_32x32x16_f16 v[0:15], a[184:187], v[176:179], v[0:15]
	ds_read_b128 v[176:179], v193 offset:36864
	v_mfma_f32_32x32x16_f16 v[16:31], a[184:187], v[180:183], v[16:31]
	ds_read_b128 v[180:183], v193 offset:37888
	v_mfma_f32_32x32x16_f16 v[0:15], a[188:191], v[184:187], v[0:15]
	ds_read_b128 v[184:187], v193 offset:38912
	v_mfma_f32_32x32x16_f16 v[16:31], a[188:191], v[188:191], v[16:31]
	ds_read_b128 v[188:191], v193 offset:39936
	s_mov_b32 m0, s54
	s_add_u32 s44, s34, 0x8000
	s_addc_u32 s45, s35, 0
	global_load_lds_dwordx4 v192, s[44:45] sc1
	s_waitcnt lgkmcnt(2)
	v_mfma_f32_32x32x16_f16 v[0:15], a[192:195], v[160:163], v[0:15]
	ds_read_b128 v[160:163], v193 offset:40960
	v_mfma_f32_32x32x16_f16 v[16:31], a[192:195], v[164:167], v[16:31]
	ds_read_b128 v[164:167], v193 offset:41984
	v_mfma_f32_32x32x16_f16 v[0:15], a[196:199], v[168:171], v[0:15]
	ds_read_b128 v[168:171], v193 offset:43008
	v_mfma_f32_32x32x16_f16 v[16:31], a[196:199], v[172:175], v[16:31]
	ds_read_b128 v[172:175], v193 offset:44032
	global_load_lds_dwordx4 v192, s[44:45] offset:1024 sc1
	v_mfma_f32_32x32x16_f16 v[0:15], a[200:203], v[176:179], v[0:15]
	ds_read_b128 v[176:179], v193 offset:45056
	v_mfma_f32_32x32x16_f16 v[16:31], a[200:203], v[180:183], v[16:31]
	ds_read_b128 v[180:183], v193 offset:46080
	s_waitcnt lgkmcnt(2)
	v_mfma_f32_32x32x16_f16 v[0:15], a[204:207], v[184:187], v[0:15]
	ds_read_b128 v[184:187], v193 offset:47104
	v_mfma_f32_32x32x16_f16 v[16:31], a[204:207], v[188:191], v[16:31]
	ds_read_b128 v[188:191], v193 offset:48128
	global_load_lds_dwordx4 v192, s[44:45] offset:2048 sc1
	s_waitcnt vmcnt(4)
	s_barrier
	v_mov_b32_e32 v199, 4
	s_cmp_eq_u32 s31, 0
	s_cbranch_scc1 .LD_slow24
	global_store_dword v197, v199, s[40:41]
.LD_join25:
	ds_read_b64 v[200:201], v249 offset:1536
	ds_read_b64 v[202:203], v249 offset:3584
	ds_read_b64 v[204:205], v249 offset:5632
	ds_read_b64 v[206:207], v249 offset:7680
	v_mfma_f32_32x32x16_f16 v[0:15], a[208:211], v[160:163], v[0:15]
	ds_read_b128 v[160:163], v193 offset:49152
	v_mfma_f32_32x32x16_f16 v[16:31], a[208:211], v[164:167], v[16:31]
	ds_read_b128 v[164:167], v193 offset:50176
	v_mfma_f32_32x32x16_f16 v[0:15], a[212:215], v[168:171], v[0:15]
	ds_read_b128 v[168:171], v193 offset:51200
	v_mfma_f32_32x32x16_f16 v[16:31], a[212:215], v[172:175], v[16:31]
	ds_read_b128 v[172:175], v193 offset:52224
	global_load_lds_dwordx4 v192, s[44:45] offset:3072 sc1
	s_waitcnt lgkmcnt(2)
	v_mfma_f32_32x32x16_f16 v[0:15], a[216:219], v[176:179], v[0:15]
	ds_read_b128 v[176:179], v193 offset:53248
	v_mfma_f32_32x32x16_f16 v[16:31], a[216:219], v[180:183], v[16:31]
	ds_read_b128 v[180:183], v193 offset:54272
	v_mfma_f32_32x32x16_f16 v[0:15], a[220:223], v[184:187], v[0:15]
	ds_read_b128 v[184:187], v193 offset:55296
	v_mfma_f32_32x32x16_f16 v[16:31], a[220:223], v[188:191], v[16:31]
	ds_read_b128 v[188:191], v193 offset:56320
	s_mov_b32 m0, s55
	s_add_u32 s44, s34, 0x9000
	s_addc_u32 s45, s35, 0
	global_load_lds_dwordx4 v192, s[44:45] sc1
	v_mfma_f32_32x32x16_f16 v[0:15], a[224:227], v[160:163], v[0:15]
	ds_read_b128 v[160:163], v193 offset:57344
	v_mfma_f32_32x32x16_f16 v[16:31], a[224:227], v[164:167], v[16:31]
	ds_read_b128 v[164:167], v193 offset:58368
	s_waitcnt lgkmcnt(2)
	v_mfma_f32_32x32x16_f16 v[0:15], a[228:231], v[168:171], v[0:15]
	ds_read_b128 v[168:171], v193 offset:59392
	v_mfma_f32_32x32x16_f16 v[16:31], a[228:231], v[172:175], v[16:31]
	ds_read_b128 v[172:175], v193 offset:60416
	global_load_lds_dwordx4 v192, s[44:45] offset:1024 sc1
	v_add_f32_e32 v200, v200, v202
	v_add_f32_e32 v201, v201, v203
	v_add_f32_e32 v200, v200, v204
	v_add_f32_e32 v201, v201, v205
	v_add_f32_e32 v200, v200, v206
	v_add_f32_e32 v201, v201, v207
	global_store_dwordx2 v250, v[200:201], s[72:73]
	v_mfma_f32_32x32x16_f16 v[0:15], a[232:235], v[176:179], v[0:15]
	ds_read_b128 v[176:179], v193 offset:61440
	v_mfma_f32_32x32x16_f16 v[16:31], a[232:235], v[180:183], v[16:31]
	ds_read_b128 v[180:183], v193 offset:62464
	v_mfma_f32_32x32x16_f16 v[0:15], a[236:239], v[184:187], v[0:15]
	ds_read_b128 v[184:187], v193 offset:63488
	v_mfma_f32_32x32x16_f16 v[16:31], a[236:239], v[188:191], v[16:31]
	ds_read_b128 v[188:191], v193 offset:64512
	global_load_lds_dwordx4 v192, s[44:45] offset:2048 sc1
	s_and_b32 s64, s33, 1
	s_lshl_b32 s64, s64, 22
	s_add_u32 s64, s64, s50
	s_add_u32 s36, s6, s64
	s_addc_u32 s37, s7, 0
	s_lshl_b32 s64, s33, 3
	s_add_u32 s64, s64, s29
	s_lshl_b32 s64, s64, 5
	s_add_u32 s64, s64, s30
	s_lshl_b32 s64, s64, 2
	s_add_u32 s40, s8, s64
	s_addc_u32 s41, s9, 0
	s_lshl_b32 s64, s33, 19
	s_add_u32 s72, s62, s64
	s_addc_u32 s73, s63, 0
	s_waitcnt vmcnt(9)
	s_barrier
	s_waitcnt lgkmcnt(2)
	v_mfma_f32_32x32x16_f16 v[0:15], a[240:243], v[160:163], v[0:15]
	ds_read_b128 v[160:163], v192 offset:0
	v_mfma_f32_32x32x16_f16 v[16:31], a[240:243], v[164:167], v[16:31]
	ds_read_b128 v[164:167], v192 offset:1024
	v_mfma_f32_32x32x16_f16 v[0:15], a[244:247], v[168:171], v[0:15]
	ds_read_b128 v[168:171], v192 offset:2048
	v_mfma_f32_32x32x16_f16 v[16:31], a[244:247], v[172:175], v[16:31]
	ds_read_b128 v[172:175], v192 offset:3072
	global_load_lds_dwordx4 v192, s[44:45] offset:3072 sc1
	v_mfma_f32_32x32x16_f16 v[0:15], a[248:251], v[176:179], v[0:15]
	ds_read_b128 v[176:179], v192 offset:4096
	v_mfma_f32_32x32x16_f16 v[16:31], a[248:251], v[180:183], v[16:31]
	ds_read_b128 v[180:183], v192 offset:5120
	s_waitcnt lgkmcnt(2)
	v_mfma_f32_32x32x16_f16 v[0:15], a[252:255], v[184:187], v[0:15]
	ds_read_b128 v[184:187], v192 offset:6144
	v_mfma_f32_32x32x16_f16 v[16:31], a[252:255], v[188:191], v[16:31]
	ds_read_b128 v[188:191], v192 offset:7168
	s_mov_b32 m0, s56
	s_add_u32 s44, s34, 0x10000
	s_addc_u32 s45, s35, 0
	global_load_lds_dwordx4 v192, s[44:45] sc1
	s_nop 3
	s_waitcnt lgkmcnt(2)
	v_mfma_f32_32x32x16_f16 v[32:47], a[0:3], v[160:163], v[32:47]
	ds_read_b128 v[160:163], v192 offset:8192
	v_exp_f32_e32 v200, v0
	v_mfma_f32_32x32x16_f16 v[48:63], a[0:3], v[164:167], v[48:63]
	ds_read_b128 v[164:167], v192 offset:9216
	s_lshl_b32 s64, s71, 3
	s_add_u32 s64, s64, s29
	s_lshl_b32 s64, s64, 7
	s_add_u32 s38, s8, s64
	s_addc_u32 s39, s9, 0
	global_load_dword v251, v196, s[38:39] sc1
	v_exp_f32_e32 v201, v1
	v_add_f32_e32 v200, 1.0, v200
	v_mfma_f32_32x32x16_f16 v[32:47], a[4:7], v[168:171], v[32:47]
	ds_read_b128 v[168:171], v192 offset:10240
	v_exp_f32_e32 v202, v2
	v_add_f32_e32 v201, 1.0, v201
	v_mfma_f32_32x32x16_f16 v[48:63], a[4:7], v[172:175], v[48:63]
	ds_read_b128 v[172:175], v192 offset:11264
	global_load_lds_dwordx4 v192, s[44:45] offset:1024 sc1
	v_exp_f32_e32 v203, v3
	v_add_f32_e32 v202, 1.0, v202
	v_mfma_f32_32x32x16_f16 v[32:47], a[8:11], v[176:179], v[32:47]
	ds_read_b128 v[176:179], v192 offset:12288
	v_exp_f32_e32 v204, v4
	v_add_f32_e32 v203, 1.0, v203
	v_mfma_f32_32x32x16_f16 v[48:63], a[8:11], v[180:183], v[48:63]
	ds_read_b128 v[180:183], v192 offset:13312
	v_exp_f32_e32 v205, v5
	v_add_f32_e32 v204, 1.0, v204
	s_waitcnt lgkmcnt(2)
	v_mfma_f32_32x32x16_f16 v[32:47], a[12:15], v[184:187], v[32:47]
	ds_read_b128 v[184:187], v192 offset:14336
	v_exp_f32_e32 v206, v6
	v_add_f32_e32 v205, 1.0, v205
	v_mfma_f32_32x32x16_f16 v[48:63], a[12:15], v[188:191], v[48:63]
	ds_read_b128 v[188:191], v192 offset:15360
	global_load_lds_dwordx4 v192, s[44:45] offset:2048 sc1
	v_exp_f32_e32 v207, v7
	v_add_f32_e32 v206, 1.0, v206
	v_mfma_f32_32x32x16_f16 v[32:47], a[16:19], v[160:163], v[32:47]
	ds_read_b128 v[160:163], v192 offset:16384
	v_exp_f32_e32 v208, v8
	v_add_f32_e32 v207, 1.0, v207
	v_mfma_f32_32x32x16_f16 v[48:63], a[16:19], v[164:167], v[48:63]
	ds_read_b128 v[164:167], v192 offset:17408
	v_exp_f32_e32 v209, v9
	v_add_f32_e32 v208, 1.0, v208
	v_mfma_f32_32x32x16_f16 v[32:47], a[20:23], v[168:171], v[32:47]
	ds_read_b128 v[168:171], v192 offset:18432
	v_exp_f32_e32 v210, v10
	v_add_f32_e32 v209, 1.0, v209
	v_mfma_f32_32x32x16_f16 v[48:63], a[20:23], v[172:175], v[48:63]
	ds_read_b128 v[172:175], v192 offset:19456
	global_load_lds_dwordx4 v192, s[44:45] offset:3072 sc1
	v_exp_f32_e32 v211, v11
	v_add_f32_e32 v210, 1.0, v210
	s_waitcnt lgkmcnt(2)
	v_mfma_f32_32x32x16_f16 v[32:47], a[24:27], v[176:179], v[32:47]
	ds_read_b128 v[176:179], v192 offset:20480
	v_exp_f32_e32 v212, v12
	v_add_f32_e32 v211, 1.0, v211
	v_mfma_f32_32x32x16_f16 v[48:63], a[24:27], v[180:183], v[48:63]
	ds_read_b128 v[180:183], v192 offset:21504
	v_exp_f32_e32 v213, v13
	v_add_f32_e32 v212, 1.0, v212
	v_mfma_f32_32x32x16_f16 v[32:47], a[28:31], v[184:187], v[32:47]
	ds_read_b128 v[184:187], v192 offset:22528
	v_exp_f32_e32 v214, v14
	v_add_f32_e32 v213, 1.0, v213
	v_mfma_f32_32x32x16_f16 v[48:63], a[28:31], v[188:191], v[48:63]
	ds_read_b128 v[188:191], v192 offset:23552
	s_mov_b32 m0, s57
	s_add_u32 s44, s34, 0x11000
	s_addc_u32 s45, s35, 0
	global_load_lds_dwordx4 v192, s[44:45] sc1
	v_exp_f32_e32 v215, v15
	v_add_f32_e32 v214, 1.0, v214
	v_mfma_f32_32x32x16_f16 v[32:47], a[32:35], v[160:163], v[32:47]
	ds_read_b128 v[160:163], v192 offset:24576
	v_add_f32_e32 v215, 1.0, v215
	v_rcp_f32_e32 v200, v200
	v_mfma_f32_32x32x16_f16 v[48:63], a[32:35], v[164:167], v[48:63]
	ds_read_b128 v[164:167], v192 offset:25600
	v_rcp_f32_e32 v201, v201
	s_waitcnt lgkmcnt(2)
	v_mfma_f32_32x32x16_f16 v[32:47], a[36:39], v[168:171], v[32:47]
	ds_read_b128 v[168:171], v192 offset:26624
	v_rcp_f32_e32 v202, v202
	v_mfma_f32_32x32x16_f16 v[48:63], a[36:39], v[172:175], v[48:63]
	ds_read_b128 v[172:175], v192 offset:27648
	global_load_lds_dwordx4 v192, s[44:45] offset:1024 sc1
	v_rcp_f32_e32 v203, v203
	v_mfma_f32_32x32x16_f16 v[32:47], a[40:43], v[176:179], v[32:47]
	ds_read_b128 v[176:179], v192 offset:28672
	v_rcp_f32_e32 v204, v204
	v_mfma_f32_32x32x16_f16 v[48:63], a[40:43], v[180:183], v[48:63]
	ds_read_b128 v[180:183], v192 offset:29696
	v_rcp_f32_e32 v205, v205
	v_mul_f32_e32 v204, v204, v128
	v_mfma_f32_32x32x16_f16 v[32:47], a[44:47], v[184:187], v[32:47]
	ds_read_b128 v[184:187], v192 offset:30720
	v_rcp_f32_e32 v206, v206
	v_mul_f32_e32 v205, v205, v129
	v_mfma_f32_32x32x16_f16 v[48:63], a[44:47], v[188:191], v[48:63]
	ds_read_b128 v[188:191], v192 offset:31744
	global_load_lds_dwordx4 v192, s[44:45] offset:2048 sc1
	v_rcp_f32_e32 v207, v207
	v_mul_f32_e32 v206, v206, v130
	s_waitcnt vmcnt(8)
	s_barrier
	s_waitcnt lgkmcnt(2)
	v_mfma_f32_32x32x16_f16 v[32:47], a[48:51], v[160:163], v[32:47]
	ds_read_b128 v[160:163], v192 offset:32768
	v_rcp_f32_e32 v208, v208
	v_mul_f32_e32 v207, v207, v131
	v_mfma_f32_32x32x16_f16 v[48:63], a[48:51], v[164:167], v[48:63]
	ds_read_b128 v[164:167], v192 offset:33792
	v_rcp_f32_e32 v209, v209
	v_fmamk_f32 v208, v208, 0xc0b8aa3b, v198
	v_mfma_f32_32x32x16_f16 v[32:47], a[52:55], v[168:171], v[32:47]
	ds_read_b128 v[168:171], v192 offset:34816
	v_rcp_f32_e32 v210, v210
	v_fmamk_f32 v209, v209, 0xc0b8aa3b, v198
	v_fma_f32 v128, v200, v208, v204
	v_mfma_f32_32x32x16_f16 v[48:63], a[52:55], v[172:175], v[48:63]
	ds_read_b128 v[172:175], v192 offset:35840
	global_load_lds_dwordx4 v192, s[44:45] offset:3072 sc1
	v_rcp_f32_e32 v211, v211
	v_fmamk_f32 v210, v210, 0xc0b8aa3b, v198
	v_fma_f32 v129, v201, v209, v205
	v_mfma_f32_32x32x16_f16 v[32:47], a[56:59], v[176:179], v[32:47]
	ds_read_b128 v[176:179], v192 offset:36864
	v_rcp_f32_e32 v212, v212
	v_fmamk_f32 v211, v211, 0xc0b8aa3b, v198
	v_fma_f32 v130, v202, v210, v206
	v_mfma_f32_32x32x16_f16 v[48:63], a[56:59], v[180:183], v[48:63]
	ds_read_b128 v[180:183], v192 offset:37888
	v_rcp_f32_e32 v213, v213
	v_fma_f32 v131, v203, v211, v207
	s_waitcnt lgkmcnt(2)
	v_mfma_f32_32x32x16_f16 v[32:47], a[60:63], v[184:187], v[32:47]
	ds_read_b128 v[184:187], v192 offset:38912
	v_rcp_f32_e32 v214, v214
	v_mfma_f32_32x32x16_f16 v[48:63], a[60:63], v[188:191], v[48:63]
	ds_read_b128 v[188:191], v192 offset:39936
	s_mov_b32 m0, s58
	s_add_u32 s44, s34, 0x18000
	s_addc_u32 s45, s35, 0
	global_load_lds_dwordx4 v192, s[44:45] sc1
	v_rcp_f32_e32 v215, v215
	v_mfma_f32_32x32x16_f16 v[32:47], a[64:67], v[160:163], v[32:47]
	ds_read_b128 v[160:163], v192 offset:40960
	v_exp_f32_e32 v200, v128
	v_mfma_f32_32x32x16_f16 v[48:63], a[64:67], v[164:167], v[48:63]
	ds_read_b128 v[164:167], v192 offset:41984
	v_exp_f32_e32 v201, v129
	v_add_f32_e32 v200, 1.0, v200
	v_mfma_f32_32x32x16_f16 v[32:47], a[68:71], v[168:171], v[32:47]
	ds_read_b128 v[168:171], v192 offset:43008
	v_exp_f32_e32 v202, v130
	v_add_f32_e32 v201, 1.0, v201
	v_mfma_f32_32x32x16_f16 v[48:63], a[68:71], v[172:175], v[48:63]
	ds_read_b128 v[172:175], v192 offset:44032
	global_load_lds_dwordx4 v192, s[44:45] offset:1024 sc1
	v_exp_f32_e32 v203, v131
	v_add_f32_e32 v202, 1.0, v202
	s_waitcnt lgkmcnt(2)
	v_mfma_f32_32x32x16_f16 v[32:47], a[72:75], v[176:179], v[32:47]
	ds_read_b128 v[176:179], v192 offset:45056
	v_add_f32_e32 v203, 1.0, v203
	v_rcp_f32_e32 v200, v200
	v_mfma_f32_32x32x16_f16 v[48:63], a[72:75], v[180:183], v[48:63]
	ds_read_b128 v[180:183], v192 offset:46080
	v_rcp_f32_e32 v201, v201
	v_fma_f32 v200, v200, 2.0, -1.0
	v_mfma_f32_32x32x16_f16 v[32:47], a[76:79], v[184:187], v[32:47]
	ds_read_b128 v[184:187], v192 offset:47104
	v_rcp_f32_e32 v202, v202
	v_fma_f32 v201, v201, 2.0, -1.0
	v_mul_f32_e32 v216, v212, v200
	v_mfma_f32_32x32x16_f16 v[48:63], a[76:79], v[188:191], v[48:63]
	ds_read_b128 v[188:191], v192 offset:48128
	global_load_lds_dwordx4 v192, s[44:45] offset:2048 sc1
	v_rcp_f32_e32 v203, v203
	v_fma_f32 v202, v202, 2.0, -1.0
	v_mul_f32_e32 v217, v213, v201
	v_mfma_f32_32x32x16_f16 v[32:47], a[80:83], v[160:163], v[32:47]
	ds_read_b128 v[160:163], v192 offset:49152
	v_fma_f32 v203, v203, 2.0, -1.0
	v_mul_f32_e32 v218, v214, v202
	v_exp_f32_e32 v200, v16
	v_mfma_f32_32x32x16_f16 v[48:63], a[80:83], v[164:167], v[48:63]
	ds_read_b128 v[164:167], v192 offset:50176
	v_mul_f32_e32 v219, v215, v203
	v_mul_f32_e32 v236, v216, v228
	v_exp_f32_e32 v201, v17
	s_waitcnt lgkmcnt(2)
	v_mfma_f32_32x32x16_f16 v[32:47], a[84:87], v[168:171], v[32:47]
	ds_read_b128 v[168:171], v192 offset:51200
	v_mul_f32_e32 v237, v216, v232
	v_fmac_f32_e32 v236, v217, v229
	v_exp_f32_e32 v202, v18
	v_mfma_f32_32x32x16_f16 v[48:63], a[84:87], v[172:175], v[48:63]
	ds_read_b128 v[172:175], v192 offset:52224
	global_load_lds_dwordx4 v192, s[44:45] offset:3072 sc1
	v_fmac_f32_e32 v237, v217, v233
	v_fmac_f32_e32 v236, v218, v230
	v_exp_f32_e32 v203, v19
	v_mfma_f32_32x32x16_f16 v[32:47], a[88:91], v[176:179], v[32:47]
	ds_read_b128 v[176:179], v192 offset:53248
	v_fmac_f32_e32 v237, v218, v234
	v_fmac_f32_e32 v236, v219, v231
	v_exp_f32_e32 v204, v20
	v_mfma_f32_32x32x16_f16 v[48:63], a[88:91], v[180:183], v[48:63]
	ds_read_b128 v[180:183], v192 offset:54272
	v_fmac_f32_e32 v237, v219, v235
	v_mov_b32_e32 v238, v236
	v_exp_f32_e32 v205, v21
	v_mfma_f32_32x32x16_f16 v[32:47], a[92:95], v[184:187], v[32:47]
	ds_read_b128 v[184:187], v192 offset:55296
	v_mov_b32_e32 v239, v236
	v_mov_b32_e32 v240, v237
	v_exp_f32_e32 v206, v22
	v_mfma_f32_32x32x16_f16 v[48:63], a[92:95], v[188:191], v[48:63]
	ds_read_b128 v[188:191], v192 offset:56320
	s_mov_b32 m0, s59
	s_add_u32 s44, s34, 0x19000
	s_addc_u32 s45, s35, 0
	global_load_lds_dwordx4 v192, s[44:45] sc1
	v_mov_b32_e32 v241, v237
	v_cvt_pk_f16_f32 v220, v216, v217
	v_exp_f32_e32 v207, v23
	s_waitcnt lgkmcnt(2)
	v_mfma_f32_32x32x16_f16 v[32:47], a[96:99], v[160:163], v[32:47]
	ds_read_b128 v[160:163], v192 offset:57344
	s_nop 1
	v_permlane32_swap_b32_e32 v238, v239
	v_permlane32_swap_b32_e32 v240, v241
	v_add_f32_e32 v238, v238, v239
	v_add_f32_e32 v239, v240, v241
	ds_write_b64 v248, v[238:239] offset:0
	v_exp_f32_e32 v208, v24
	v_mfma_f32_32x32x16_f16 v[48:63], a[96:99], v[164:167], v[48:63]
	ds_read_b128 v[164:167], v192 offset:58368
	v_cvt_pk_f16_f32 v221, v218, v219
	v_exp_f32_e32 v209, v25
	v_add_f32_e32 v200, 1.0, v200
	v_mfma_f32_32x32x16_f16 v[32:47], a[100:103], v[168:171], v[32:47]
	ds_read_b128 v[168:171], v192 offset:59392
	v_exp_f32_e32 v210, v26
	v_add_f32_e32 v201, 1.0, v201
	v_add_f32_e32 v202, 1.0, v202
	v_mfma_f32_32x32x16_f16 v[48:63], a[100:103], v[172:175], v[48:63]
	ds_read_b128 v[172:175], v192 offset:60416
	global_load_lds_dwordx4 v192, s[44:45] offset:1024 sc1
	v_exp_f32_e32 v211, v27
	v_add_f32_e32 v203, 1.0, v203
	v_add_f32_e32 v204, 1.0, v204
	v_mfma_f32_32x32x16_f16 v[32:47], a[104:107], v[176:179], v[32:47]
	ds_read_b128 v[176:179], v192 offset:61440
	v_exp_f32_e32 v212, v28
	v_add_f32_e32 v205, 1.0, v205
	v_add_f32_e32 v206, 1.0, v206
	v_mfma_f32_32x32x16_f16 v[48:63], a[104:107], v[180:183], v[48:63]
	ds_read_b128 v[180:183], v192 offset:62464
	v_exp_f32_e32 v213, v29
	v_add_f32_e32 v207, 1.0, v207
	v_add_f32_e32 v208, 1.0, v208
	s_waitcnt lgkmcnt(2)
	v_mfma_f32_32x32x16_f16 v[32:47], a[108:111], v[184:187], v[32:47]
	ds_read_b128 v[184:187], v192 offset:63488
	v_exp_f32_e32 v214, v30
	v_add_f32_e32 v209, 1.0, v209
	v_add_f32_e32 v210, 1.0, v210
	v_mfma_f32_32x32x16_f16 v[48:63], a[108:111], v[188:191], v[48:63]
	ds_read_b128 v[188:191], v192 offset:64512
	global_load_lds_dwordx4 v192, s[44:45] offset:2048 sc1
	v_exp_f32_e32 v215, v31
	v_add_f32_e32 v211, 1.0, v211
	v_add_f32_e32 v212, 1.0, v212
	s_waitcnt vmcnt(7)
	s_barrier
	v_mfma_f32_32x32x16_f16 v[32:47], a[112:115], v[160:163], v[32:47]
	ds_read_b128 v[160:163], v193 offset:0
	v_add_f32_e32 v213, 1.0, v213
	v_add_f32_e32 v214, 1.0, v214
	v_rcp_f32_e32 v200, v200
	v_mfma_f32_32x32x16_f16 v[48:63], a[112:115], v[164:167], v[48:63]
	ds_read_b128 v[164:167], v193 offset:1024
	v_add_f32_e32 v215, 1.0, v215
	v_rcp_f32_e32 v201, v201
	v_mfma_f32_32x32x16_f16 v[32:47], a[116:119], v[168:171], v[32:47]
	ds_read_b128 v[168:171], v193 offset:2048
	v_rcp_f32_e32 v202, v202
	v_mfma_f32_32x32x16_f16 v[48:63], a[116:119], v[172:175], v[48:63]
	ds_read_b128 v[172:175], v193 offset:3072
	global_load_lds_dwordx4 v192, s[44:45] offset:3072 sc1
	v_rcp_f32_e32 v203, v203
	s_waitcnt lgkmcnt(2)
	v_mfma_f32_32x32x16_f16 v[32:47], a[120:123], v[176:179], v[32:47]
	ds_read_b128 v[176:179], v193 offset:4096
	v_rcp_f32_e32 v204, v204
	s_add_u32 s46, s42, 0x6000
	s_addc_u32 s47, s43, 0
	global_load_dwordx4 v[96:99], v192, s[46:47] offset:0
	v_mfma_f32_32x32x16_f16 v[48:63], a[120:123], v[180:183], v[48:63]
	ds_read_b128 v[180:183], v193 offset:5120
	v_rcp_f32_e32 v205, v205
	v_mul_f32_e32 v204, v204, v132
	global_load_dwordx4 v[100:103], v192, s[46:47] offset:1024
	global_load_dwordx4 v[104:107], v192, s[46:47] offset:2048
	v_mfma_f32_32x32x16_f16 v[32:47], a[124:127], v[184:187], v[32:47]
	ds_read_b128 v[184:187], v193 offset:6144
	v_rcp_f32_e32 v206, v206
	v_mul_f32_e32 v205, v205, v133
	global_load_dwordx4 v[108:111], v192, s[46:47] offset:3072
	s_add_u32 s46, s42, 0x7000
	s_addc_u32 s47, s43, 0
	v_mfma_f32_32x32x16_f16 v[48:63], a[124:127], v[188:191], v[48:63]
	ds_read_b128 v[188:191], v193 offset:7168
	v_cmp_gt_u32_e32 vcc, 3, v251
	s_cbranch_vccnz .LD_tpoll27
.LD_tok26:
	s_and_b32 s64, s71, 1
	s_lshl_b32 s64, s64, 22
	s_add_u32 s64, s64, s49
	s_add_u32 s64, s64, 0x40000
	s_add_u32 s34, s6, s64
	s_addc_u32 s35, s7, 0
	s_mov_b32 m0, s52
	s_add_u32 s44, s34, 0x0
	s_addc_u32 s45, s35, 0
	global_load_lds_dwordx4 v192, s[44:45] sc1
	v_rcp_f32_e32 v207, v207
	v_mul_f32_e32 v206, v206, v134
	global_load_dwordx4 v[112:115], v192, s[46:47] offset:0
	global_load_dwordx4 v[116:119], v192, s[46:47] offset:1024
	v_mfma_f32_32x32x16_f16 v[32:47], a[128:131], v[160:163], v[32:47]
	ds_read_b128 v[160:163], v193 offset:8192
	v_rcp_f32_e32 v208, v208
	v_mul_f32_e32 v207, v207, v135
	global_load_dwordx4 v[120:123], v192, s[46:47] offset:2048
	global_load_dwordx4 v[124:127], v192, s[46:47] offset:3072
	v_mfma_f32_32x32x16_f16 v[48:63], a[128:131], v[164:167], v[48:63]
	ds_read_b128 v[164:167], v193 offset:9216
	v_rcp_f32_e32 v209, v209
	v_fmamk_f32 v208, v208, 0xc0b8aa3b, v198
	s_waitcnt lgkmcnt(2)
	v_mfma_f32_32x32x16_f16 v[32:47], a[132:135], v[168:171], v[32:47]
	ds_read_b128 v[168:171], v193 offset:10240
	v_rcp_f32_e32 v210, v210
	v_fmamk_f32 v209, v209, 0xc0b8aa3b, v198
	v_fma_f32 v132, v200, v208, v204
	v_mfma_f32_32x32x16_f16 v[48:63], a[132:135], v[172:175], v[48:63]
	ds_read_b128 v[172:175], v193 offset:11264
	global_load_lds_dwordx4 v192, s[44:45] offset:1024 sc1
	v_rcp_f32_e32 v211, v211
	v_fmamk_f32 v210, v210, 0xc0b8aa3b, v198
	v_fma_f32 v133, v201, v209, v205
	v_mfma_f32_32x32x16_f16 v[32:47], a[136:139], v[176:179], v[32:47]
	ds_read_b128 v[176:179], v193 offset:12288
	v_rcp_f32_e32 v212, v212
	v_fmamk_f32 v211, v211, 0xc0b8aa3b, v198
	v_fma_f32 v134, v202, v210, v206
	v_mfma_f32_32x32x16_f16 v[48:63], a[136:139], v[180:183], v[48:63]
	ds_read_b128 v[180:183], v193 offset:13312
	v_rcp_f32_e32 v213, v213
	v_fma_f32 v135, v203, v211, v207
	v_mfma_f32_32x32x16_f16 v[32:47], a[140:143], v[184:187], v[32:47]
	ds_read_b128 v[184:187], v193 offset:14336
	v_rcp_f32_e32 v214, v214
	v_mfma_f32_32x32x16_f16 v[48:63], a[140:143], v[188:191], v[48:63]
	ds_read_b128 v[188:191], v193 offset:15360
	global_load_lds_dwordx4 v192, s[44:45] offset:2048 sc1
	v_rcp_f32_e32 v215, v215
	s_waitcnt lgkmcnt(2)
	v_mfma_f32_32x32x16_f16 v[32:47], a[144:147], v[160:163], v[32:47]
	ds_read_b128 v[160:163], v193 offset:16384
	v_exp_f32_e32 v200, v132
	v_mfma_f32_32x32x16_f16 v[48:63], a[144:147], v[164:167], v[48:63]
	ds_read_b128 v[164:167], v193 offset:17408
	v_exp_f32_e32 v201, v133
	v_add_f32_e32 v200, 1.0, v200
	v_mfma_f32_32x32x16_f16 v[32:47], a[148:151], v[168:171], v[32:47]
	ds_read_b128 v[168:171], v193 offset:18432
	v_exp_f32_e32 v202, v134
	v_add_f32_e32 v201, 1.0, v201
	v_mfma_f32_32x32x16_f16 v[48:63], a[148:151], v[172:175], v[48:63]
	ds_read_b128 v[172:175], v193 offset:19456
	global_load_lds_dwordx4 v192, s[44:45] offset:3072 sc1
	v_exp_f32_e32 v203, v135
	v_add_f32_e32 v202, 1.0, v202
	v_mfma_f32_32x32x16_f16 v[32:47], a[152:155], v[176:179], v[32:47]
	ds_read_b128 v[176:179], v193 offset:20480
	v_add_f32_e32 v203, 1.0, v203
	v_rcp_f32_e32 v200, v200
	v_mfma_f32_32x32x16_f16 v[48:63], a[152:155], v[180:183], v[48:63]
	ds_read_b128 v[180:183], v193 offset:21504
	v_rcp_f32_e32 v201, v201
	v_fma_f32 v200, v200, 2.0, -1.0
	s_waitcnt lgkmcnt(2)
	v_mfma_f32_32x32x16_f16 v[32:47], a[156:159], v[184:187], v[32:47]
	ds_read_b128 v[184:187], v193 offset:22528
	v_rcp_f32_e32 v202, v202
	v_fma_f32 v201, v201, 2.0, -1.0
	v_mul_f32_e32 v216, v212, v200
	v_mfma_f32_32x32x16_f16 v[48:63], a[156:159], v[188:191], v[48:63]
	ds_read_b128 v[188:191], v193 offset:23552
	s_mov_b32 m0, s53
	s_add_u32 s44, s34, 0x1000
	s_addc_u32 s45, s35, 0
	global_load_lds_dwordx4 v192, s[44:45] sc1
	v_rcp_f32_e32 v203, v203
	v_fma_f32 v202, v202, 2.0, -1.0
	v_mul_f32_e32 v217, v213, v201
	v_mfma_f32_32x32x16_f16 v[32:47], a[160:163], v[160:163], v[32:47]
	ds_read_b128 v[160:163], v193 offset:24576
	v_fma_f32 v203, v203, 2.0, -1.0
	v_mul_f32_e32 v218, v214, v202
	v_mfma_f32_32x32x16_f16 v[48:63], a[160:163], v[164:167], v[48:63]
	ds_read_b128 v[164:167], v193 offset:25600
	v_mul_f32_e32 v219, v215, v203
	v_mul_f32_e32 v236, v216, v228
	v_mfma_f32_32x32x16_f16 v[32:47], a[164:167], v[168:171], v[32:47]
	ds_read_b128 v[168:171], v193 offset:26624
	v_mul_f32_e32 v237, v216, v232
	v_fmac_f32_e32 v236, v217, v229
	v_mfma_f32_32x32x16_f16 v[48:63], a[164:167], v[172:175], v[48:63]
	ds_read_b128 v[172:175], v193 offset:27648
	global_load_lds_dwordx4 v192, s[44:45] offset:1024 sc1
	v_fmac_f32_e32 v237, v217, v233
	v_fmac_f32_e32 v236, v218, v230
	s_waitcnt lgkmcnt(2)
	v_mfma_f32_32x32x16_f16 v[32:47], a[168:171], v[176:179], v[32:47]
	ds_read_b128 v[176:179], v193 offset:28672
	v_fmac_f32_e32 v237, v218, v234
	v_fmac_f32_e32 v236, v219, v231
	v_mfma_f32_32x32x16_f16 v[48:63], a[168:171], v[180:183], v[48:63]
	ds_read_b128 v[180:183], v193 offset:29696
	v_fmac_f32_e32 v237, v219, v235
	v_mov_b32_e32 v238, v236
	v_mfma_f32_32x32x16_f16 v[32:47], a[172:175], v[184:187], v[32:47]
	ds_read_b128 v[184:187], v193 offset:30720
	v_mov_b32_e32 v239, v236
	v_mov_b32_e32 v240, v237
	v_mfma_f32_32x32x16_f16 v[48:63], a[172:175], v[188:191], v[48:63]
	ds_read_b128 v[188:191], v193 offset:31744
	global_load_lds_dwordx4 v192, s[44:45] offset:2048 sc1
	v_mov_b32_e32 v241, v237
	v_cvt_pk_f16_f32 v222, v216, v217
	s_waitcnt vmcnt(15)
	s_barrier
	v_mfma_f32_32x32x16_f16 v[32:47], a[176:179], v[160:163], v[32:47]
	ds_read_b128 v[160:163], v193 offset:32768
	s_nop 1
	v_permlane32_swap_b32_e32 v238, v239
	v_permlane32_swap_b32_e32 v240, v241
	v_add_f32_e32 v238, v238, v239
	v_add_f32_e32 v239, v240, v241
	ds_write_b64 v248, v[238:239] offset:256
	v_mfma_f32_32x32x16_f16 v[48:63], a[176:179], v[164:167], v[48:63]
	ds_read_b128 v[164:167], v193 offset:33792
	v_cvt_pk_f16_f32 v223, v218, v219
	s_waitcnt lgkmcnt(3)
	v_mfma_f32_32x32x16_f16 v[32:47], a[180:183], v[168:171], v[32:47]
	ds_read_b128 v[168:171], v193 offset:34816
	s_nop 1
	v_permlane32_swap_b32_e32 v220, v222
	v_permlane32_swap_b32_e32 v221, v223
	s_cmp_eq_u32 s31, 0
	s_cbranch_scc1 .LD_slow28
	global_store_dwordx4 v195, v[220:223], s[36:37] offset:0
.LD_join29:
	v_mfma_f32_32x32x16_f16 v[48:63], a[180:183], v[172:175], v[48:63]
	ds_read_b128 v[172:175], v193 offset:35840
	global_load_lds_dwordx4 v192, s[44:45] offset:3072 sc1
	v_mfma_f32_32x32x16_f16 v[32:47], a[184:187], v[176:179], v[32:47]
	ds_read_b128 v[176:179], v193 offset:36864
	v_mfma_f32_32x32x16_f16 v[48:63], a[184:187], v[180:183], v[48:63]
	ds_read_b128 v[180:183], v193 offset:37888
	v_mfma_f32_32x32x16_f16 v[32:47], a[188:191], v[184:187], v[32:47]
	ds_read_b128 v[184:187], v193 offset:38912
	v_mfma_f32_32x32x16_f16 v[48:63], a[188:191], v[188:191], v[48:63]
	ds_read_b128 v[188:191], v193 offset:39936
	s_mov_b32 m0, s54
	s_add_u32 s44, s34, 0x8000
	s_addc_u32 s45, s35, 0
	global_load_lds_dwordx4 v192, s[44:45] sc1
	s_waitcnt lgkmcnt(2)
	v_mfma_f32_32x32x16_f16 v[32:47], a[192:195], v[160:163], v[32:47]
	ds_read_b128 v[160:163], v193 offset:40960
	v_mfma_f32_32x32x16_f16 v[48:63], a[192:195], v[164:167], v[48:63]
	ds_read_b128 v[164:167], v193 offset:41984
	v_mfma_f32_32x32x16_f16 v[32:47], a[196:199], v[168:171], v[32:47]
	ds_read_b128 v[168:171], v193 offset:43008
	v_mfma_f32_32x32x16_f16 v[48:63], a[196:199], v[172:175], v[48:63]
	ds_read_b128 v[172:175], v193 offset:44032
	global_load_lds_dwordx4 v192, s[44:45] offset:1024 sc1
	v_mfma_f32_32x32x16_f16 v[32:47], a[200:203], v[176:179], v[32:47]
	ds_read_b128 v[176:179], v193 offset:45056
	v_mfma_f32_32x32x16_f16 v[48:63], a[200:203], v[180:183], v[48:63]
	ds_read_b128 v[180:183], v193 offset:46080
	s_waitcnt lgkmcnt(2)
	v_mfma_f32_32x32x16_f16 v[32:47], a[204:207], v[184:187], v[32:47]
	ds_read_b128 v[184:187], v193 offset:47104
	v_mfma_f32_32x32x16_f16 v[48:63], a[204:207], v[188:191], v[48:63]
	ds_read_b128 v[188:191], v193 offset:48128
	global_load_lds_dwordx4 v192, s[44:45] offset:2048 sc1
	s_waitcnt vmcnt(4)
	s_barrier
	v_mov_b32_e32 v199, 1
	s_cmp_eq_u32 s31, 0
	s_cbranch_scc1 .LD_slow30
	global_store_dword v197, v199, s[40:41]
.LD_join31:
	ds_read_b64 v[200:201], v249 offset:0
	ds_read_b64 v[202:203], v249 offset:2048
	ds_read_b64 v[204:205], v249 offset:4096
	ds_read_b64 v[206:207], v249 offset:6144
	v_mfma_f32_32x32x16_f16 v[32:47], a[208:211], v[160:163], v[32:47]
	ds_read_b128 v[160:163], v193 offset:49152
	v_mfma_f32_32x32x16_f16 v[48:63], a[208:211], v[164:167], v[48:63]
	ds_read_b128 v[164:167], v193 offset:50176
	v_mfma_f32_32x32x16_f16 v[32:47], a[212:215], v[168:171], v[32:47]
	ds_read_b128 v[168:171], v193 offset:51200
	v_mfma_f32_32x32x16_f16 v[48:63], a[212:215], v[172:175], v[48:63]
	ds_read_b128 v[172:175], v193 offset:52224
	global_load_lds_dwordx4 v192, s[44:45] offset:3072 sc1
	s_waitcnt lgkmcnt(2)
	v_mfma_f32_32x32x16_f16 v[32:47], a[216:219], v[176:179], v[32:47]
	ds_read_b128 v[176:179], v193 offset:53248
	v_mfma_f32_32x32x16_f16 v[48:63], a[216:219], v[180:183], v[48:63]
	ds_read_b128 v[180:183], v193 offset:54272
	v_mfma_f32_32x32x16_f16 v[32:47], a[220:223], v[184:187], v[32:47]
	ds_read_b128 v[184:187], v193 offset:55296
	v_mfma_f32_32x32x16_f16 v[48:63], a[220:223], v[188:191], v[48:63]
	ds_read_b128 v[188:191], v193 offset:56320
	s_mov_b32 m0, s55
	s_add_u32 s44, s34, 0x9000
	s_addc_u32 s45, s35, 0
	global_load_lds_dwordx4 v192, s[44:45] sc1
	v_mfma_f32_32x32x16_f16 v[32:47], a[224:227], v[160:163], v[32:47]
	ds_read_b128 v[160:163], v193 offset:57344
	v_mfma_f32_32x32x16_f16 v[48:63], a[224:227], v[164:167], v[48:63]
	ds_read_b128 v[164:167], v193 offset:58368
	s_waitcnt lgkmcnt(2)
	v_mfma_f32_32x32x16_f16 v[32:47], a[228:231], v[168:171], v[32:47]
	ds_read_b128 v[168:171], v193 offset:59392
	v_mfma_f32_32x32x16_f16 v[48:63], a[228:231], v[172:175], v[48:63]
	ds_read_b128 v[172:175], v193 offset:60416
	global_load_lds_dwordx4 v192, s[44:45] offset:1024 sc1
	v_add_f32_e32 v200, v200, v202
	v_add_f32_e32 v201, v201, v203
	v_add_f32_e32 v200, v200, v204
	v_add_f32_e32 v201, v201, v205
	v_add_f32_e32 v200, v200, v206
	v_add_f32_e32 v201, v201, v207
	global_store_dwordx2 v250, v[200:201], s[72:73]
	v_mfma_f32_32x32x16_f16 v[32:47], a[232:235], v[176:179], v[32:47]
	ds_read_b128 v[176:179], v193 offset:61440
	v_mfma_f32_32x32x16_f16 v[48:63], a[232:235], v[180:183], v[48:63]
	ds_read_b128 v[180:183], v193 offset:62464
	v_mfma_f32_32x32x16_f16 v[32:47], a[236:239], v[184:187], v[32:47]
	ds_read_b128 v[184:187], v193 offset:63488
	v_mfma_f32_32x32x16_f16 v[48:63], a[236:239], v[188:191], v[48:63]
	ds_read_b128 v[188:191], v193 offset:64512
	global_load_lds_dwordx4 v192, s[44:45] offset:2048 sc1
	s_and_b32 s64, s33, 1
	s_lshl_b32 s64, s64, 22
	s_add_u32 s64, s64, s50
	s_add_u32 s64, s64, 0x20000
	s_add_u32 s36, s6, s64
	s_addc_u32 s37, s7, 0
	s_lshl_b32 s64, s33, 3
	s_add_u32 s64, s64, s29
	s_lshl_b32 s64, s64, 5
	s_add_u32 s64, s64, s30
	s_lshl_b32 s64, s64, 2
	s_add_u32 s40, s8, s64
	s_addc_u32 s41, s9, 0
	s_lshl_b32 s64, s33, 19
	s_add_u32 s64, s64, 0x200
	s_add_u32 s72, s62, s64
	s_addc_u32 s73, s63, 0
	s_waitcnt vmcnt(9)
	s_barrier
	s_waitcnt lgkmcnt(2)
	v_mfma_f32_32x32x16_f16 v[32:47], a[240:243], v[160:163], v[32:47]
	ds_read_b128 v[160:163], v192 offset:0
	v_mfma_f32_32x32x16_f16 v[48:63], a[240:243], v[164:167], v[48:63]
	ds_read_b128 v[164:167], v192 offset:1024
	v_mfma_f32_32x32x16_f16 v[32:47], a[244:247], v[168:171], v[32:47]
	ds_read_b128 v[168:171], v192 offset:2048
	v_mfma_f32_32x32x16_f16 v[48:63], a[244:247], v[172:175], v[48:63]
	ds_read_b128 v[172:175], v192 offset:3072
	global_load_lds_dwordx4 v192, s[44:45] offset:3072 sc1
	v_mfma_f32_32x32x16_f16 v[32:47], a[248:251], v[176:179], v[32:47]
	ds_read_b128 v[176:179], v192 offset:4096
	v_mfma_f32_32x32x16_f16 v[48:63], a[248:251], v[180:183], v[48:63]
	ds_read_b128 v[180:183], v192 offset:5120
	s_waitcnt lgkmcnt(2)
	v_mfma_f32_32x32x16_f16 v[32:47], a[252:255], v[184:187], v[32:47]
	ds_read_b128 v[184:187], v192 offset:6144
	v_mfma_f32_32x32x16_f16 v[48:63], a[252:255], v[188:191], v[48:63]
	ds_read_b128 v[188:191], v192 offset:7168
	s_mov_b32 m0, s56
	s_add_u32 s44, s34, 0x10000
	s_addc_u32 s45, s35, 0
	global_load_lds_dwordx4 v192, s[44:45] sc1
	s_nop 3
	s_waitcnt lgkmcnt(2)
	v_mfma_f32_32x32x16_f16 v[64:79], a[0:3], v[160:163], v[64:79]
	ds_read_b128 v[160:163], v192 offset:8192
	v_exp_f32_e32 v200, v32
	v_mfma_f32_32x32x16_f16 v[80:95], a[0:3], v[164:167], v[80:95]
	ds_read_b128 v[164:167], v192 offset:9216
	s_lshl_b32 s64, s71, 3
	s_add_u32 s64, s64, s29
	s_lshl_b32 s64, s64, 7
	s_add_u32 s38, s8, s64
	s_addc_u32 s39, s9, 0
	global_load_dword v251, v196, s[38:39] sc1
	v_exp_f32_e32 v201, v33
	v_add_f32_e32 v200, 1.0, v200
	v_mfma_f32_32x32x16_f16 v[64:79], a[4:7], v[168:171], v[64:79]
	ds_read_b128 v[168:171], v192 offset:10240
	v_exp_f32_e32 v202, v34
	v_add_f32_e32 v201, 1.0, v201
	v_mfma_f32_32x32x16_f16 v[80:95], a[4:7], v[172:175], v[80:95]
	ds_read_b128 v[172:175], v192 offset:11264
	global_load_lds_dwordx4 v192, s[44:45] offset:1024 sc1
	v_exp_f32_e32 v203, v35
	v_add_f32_e32 v202, 1.0, v202
	v_mfma_f32_32x32x16_f16 v[64:79], a[8:11], v[176:179], v[64:79]
	ds_read_b128 v[176:179], v192 offset:12288
	v_exp_f32_e32 v204, v36
	v_add_f32_e32 v203, 1.0, v203
	v_mfma_f32_32x32x16_f16 v[80:95], a[8:11], v[180:183], v[80:95]
	ds_read_b128 v[180:183], v192 offset:13312
	v_exp_f32_e32 v205, v37
	v_add_f32_e32 v204, 1.0, v204
	s_waitcnt lgkmcnt(2)
	v_mfma_f32_32x32x16_f16 v[64:79], a[12:15], v[184:187], v[64:79]
	ds_read_b128 v[184:187], v192 offset:14336
	v_exp_f32_e32 v206, v38
	v_add_f32_e32 v205, 1.0, v205
	v_mfma_f32_32x32x16_f16 v[80:95], a[12:15], v[188:191], v[80:95]
	ds_read_b128 v[188:191], v192 offset:15360
	global_load_lds_dwordx4 v192, s[44:45] offset:2048 sc1
	v_exp_f32_e32 v207, v39
	v_add_f32_e32 v206, 1.0, v206
	v_mfma_f32_32x32x16_f16 v[64:79], a[16:19], v[160:163], v[64:79]
	ds_read_b128 v[160:163], v192 offset:16384
	v_exp_f32_e32 v208, v40
	v_add_f32_e32 v207, 1.0, v207
	v_mfma_f32_32x32x16_f16 v[80:95], a[16:19], v[164:167], v[80:95]
	ds_read_b128 v[164:167], v192 offset:17408
	v_exp_f32_e32 v209, v41
	v_add_f32_e32 v208, 1.0, v208
	v_mfma_f32_32x32x16_f16 v[64:79], a[20:23], v[168:171], v[64:79]
	ds_read_b128 v[168:171], v192 offset:18432
	v_exp_f32_e32 v210, v42
	v_add_f32_e32 v209, 1.0, v209
	v_mfma_f32_32x32x16_f16 v[80:95], a[20:23], v[172:175], v[80:95]
	ds_read_b128 v[172:175], v192 offset:19456
	global_load_lds_dwordx4 v192, s[44:45] offset:3072 sc1
	v_exp_f32_e32 v211, v43
	v_add_f32_e32 v210, 1.0, v210
	s_waitcnt lgkmcnt(2)
	v_mfma_f32_32x32x16_f16 v[64:79], a[24:27], v[176:179], v[64:79]
	ds_read_b128 v[176:179], v192 offset:20480
	v_exp_f32_e32 v212, v44
	v_add_f32_e32 v211, 1.0, v211
	v_mfma_f32_32x32x16_f16 v[80:95], a[24:27], v[180:183], v[80:95]
	ds_read_b128 v[180:183], v192 offset:21504
	v_exp_f32_e32 v213, v45
	v_add_f32_e32 v212, 1.0, v212
	v_mfma_f32_32x32x16_f16 v[64:79], a[28:31], v[184:187], v[64:79]
	ds_read_b128 v[184:187], v192 offset:22528
	v_exp_f32_e32 v214, v46
	v_add_f32_e32 v213, 1.0, v213
	v_mfma_f32_32x32x16_f16 v[80:95], a[28:31], v[188:191], v[80:95]
	ds_read_b128 v[188:191], v192 offset:23552
	s_mov_b32 m0, s57
	s_add_u32 s44, s34, 0x11000
	s_addc_u32 s45, s35, 0
	global_load_lds_dwordx4 v192, s[44:45] sc1
	v_exp_f32_e32 v215, v47
	v_add_f32_e32 v214, 1.0, v214
	v_mfma_f32_32x32x16_f16 v[64:79], a[32:35], v[160:163], v[64:79]
	ds_read_b128 v[160:163], v192 offset:24576
	v_add_f32_e32 v215, 1.0, v215
	v_rcp_f32_e32 v200, v200
	v_mfma_f32_32x32x16_f16 v[80:95], a[32:35], v[164:167], v[80:95]
	ds_read_b128 v[164:167], v192 offset:25600
	v_rcp_f32_e32 v201, v201
	s_waitcnt lgkmcnt(2)
	v_mfma_f32_32x32x16_f16 v[64:79], a[36:39], v[168:171], v[64:79]
	ds_read_b128 v[168:171], v192 offset:26624
	v_rcp_f32_e32 v202, v202
	v_mfma_f32_32x32x16_f16 v[80:95], a[36:39], v[172:175], v[80:95]
	ds_read_b128 v[172:175], v192 offset:27648
	global_load_lds_dwordx4 v192, s[44:45] offset:1024 sc1
	v_rcp_f32_e32 v203, v203
	v_mfma_f32_32x32x16_f16 v[64:79], a[40:43], v[176:179], v[64:79]
	ds_read_b128 v[176:179], v192 offset:28672
	v_rcp_f32_e32 v204, v204
	v_mfma_f32_32x32x16_f16 v[80:95], a[40:43], v[180:183], v[80:95]
	ds_read_b128 v[180:183], v192 offset:29696
	v_rcp_f32_e32 v205, v205
	v_mul_f32_e32 v204, v204, v136
	v_mfma_f32_32x32x16_f16 v[64:79], a[44:47], v[184:187], v[64:79]
	ds_read_b128 v[184:187], v192 offset:30720
	v_rcp_f32_e32 v206, v206
	v_mul_f32_e32 v205, v205, v137
	v_mfma_f32_32x32x16_f16 v[80:95], a[44:47], v[188:191], v[80:95]
	ds_read_b128 v[188:191], v192 offset:31744
	global_load_lds_dwordx4 v192, s[44:45] offset:2048 sc1
	v_rcp_f32_e32 v207, v207
	v_mul_f32_e32 v206, v206, v138
	s_waitcnt vmcnt(8)
	s_barrier
	s_waitcnt lgkmcnt(2)
	v_mfma_f32_32x32x16_f16 v[64:79], a[48:51], v[160:163], v[64:79]
	ds_read_b128 v[160:163], v192 offset:32768
	v_rcp_f32_e32 v208, v208
	v_mul_f32_e32 v207, v207, v139
	v_mfma_f32_32x32x16_f16 v[80:95], a[48:51], v[164:167], v[80:95]
	ds_read_b128 v[164:167], v192 offset:33792
	v_rcp_f32_e32 v209, v209
	v_fmamk_f32 v208, v208, 0xc0b8aa3b, v198
	v_mfma_f32_32x32x16_f16 v[64:79], a[52:55], v[168:171], v[64:79]
	ds_read_b128 v[168:171], v192 offset:34816
	v_rcp_f32_e32 v210, v210
	v_fmamk_f32 v209, v209, 0xc0b8aa3b, v198
	v_fma_f32 v136, v200, v208, v204
	v_mfma_f32_32x32x16_f16 v[80:95], a[52:55], v[172:175], v[80:95]
	ds_read_b128 v[172:175], v192 offset:35840
	global_load_lds_dwordx4 v192, s[44:45] offset:3072 sc1
	v_rcp_f32_e32 v211, v211
	v_fmamk_f32 v210, v210, 0xc0b8aa3b, v198
	v_fma_f32 v137, v201, v209, v205
	v_mfma_f32_32x32x16_f16 v[64:79], a[56:59], v[176:179], v[64:79]
	ds_read_b128 v[176:179], v192 offset:36864
	v_rcp_f32_e32 v212, v212
	v_fmamk_f32 v211, v211, 0xc0b8aa3b, v198
	v_fma_f32 v138, v202, v210, v206
	v_mfma_f32_32x32x16_f16 v[80:95], a[56:59], v[180:183], v[80:95]
	ds_read_b128 v[180:183], v192 offset:37888
	v_rcp_f32_e32 v213, v213
	v_fma_f32 v139, v203, v211, v207
	s_waitcnt lgkmcnt(2)
	v_mfma_f32_32x32x16_f16 v[64:79], a[60:63], v[184:187], v[64:79]
	ds_read_b128 v[184:187], v192 offset:38912
	v_rcp_f32_e32 v214, v214
	v_mfma_f32_32x32x16_f16 v[80:95], a[60:63], v[188:191], v[80:95]
	ds_read_b128 v[188:191], v192 offset:39936
	s_mov_b32 m0, s58
	s_add_u32 s44, s34, 0x18000
	s_addc_u32 s45, s35, 0
	global_load_lds_dwordx4 v192, s[44:45] sc1
	v_rcp_f32_e32 v215, v215
	v_mfma_f32_32x32x16_f16 v[64:79], a[64:67], v[160:163], v[64:79]
	ds_read_b128 v[160:163], v192 offset:40960
	v_exp_f32_e32 v200, v136
	v_mfma_f32_32x32x16_f16 v[80:95], a[64:67], v[164:167], v[80:95]
	ds_read_b128 v[164:167], v192 offset:41984
	v_exp_f32_e32 v201, v137
	v_add_f32_e32 v200, 1.0, v200
	v_mfma_f32_32x32x16_f16 v[64:79], a[68:71], v[168:171], v[64:79]
	ds_read_b128 v[168:171], v192 offset:43008
	v_exp_f32_e32 v202, v138
	v_add_f32_e32 v201, 1.0, v201
	v_mfma_f32_32x32x16_f16 v[80:95], a[68:71], v[172:175], v[80:95]
	ds_read_b128 v[172:175], v192 offset:44032
	global_load_lds_dwordx4 v192, s[44:45] offset:1024 sc1
	v_exp_f32_e32 v203, v139
	v_add_f32_e32 v202, 1.0, v202
	s_waitcnt lgkmcnt(2)
	v_mfma_f32_32x32x16_f16 v[64:79], a[72:75], v[176:179], v[64:79]
	ds_read_b128 v[176:179], v192 offset:45056
	v_add_f32_e32 v203, 1.0, v203
	v_rcp_f32_e32 v200, v200
	v_mfma_f32_32x32x16_f16 v[80:95], a[72:75], v[180:183], v[80:95]
	ds_read_b128 v[180:183], v192 offset:46080
	v_rcp_f32_e32 v201, v201
	v_fma_f32 v200, v200, 2.0, -1.0
	v_mfma_f32_32x32x16_f16 v[64:79], a[76:79], v[184:187], v[64:79]
	ds_read_b128 v[184:187], v192 offset:47104
	v_rcp_f32_e32 v202, v202
	v_fma_f32 v201, v201, 2.0, -1.0
	v_mul_f32_e32 v216, v212, v200
	v_mfma_f32_32x32x16_f16 v[80:95], a[76:79], v[188:191], v[80:95]
	ds_read_b128 v[188:191], v192 offset:48128
	global_load_lds_dwordx4 v192, s[44:45] offset:2048 sc1
	v_rcp_f32_e32 v203, v203
	v_fma_f32 v202, v202, 2.0, -1.0
	v_mul_f32_e32 v217, v213, v201
	v_mfma_f32_32x32x16_f16 v[64:79], a[80:83], v[160:163], v[64:79]
	ds_read_b128 v[160:163], v192 offset:49152
	v_fma_f32 v203, v203, 2.0, -1.0
	v_mul_f32_e32 v218, v214, v202
	v_exp_f32_e32 v200, v48
	v_mfma_f32_32x32x16_f16 v[80:95], a[80:83], v[164:167], v[80:95]
	ds_read_b128 v[164:167], v192 offset:50176
	v_mul_f32_e32 v219, v215, v203
	v_mul_f32_e32 v236, v216, v228
	v_exp_f32_e32 v201, v49
	s_waitcnt lgkmcnt(2)
	v_mfma_f32_32x32x16_f16 v[64:79], a[84:87], v[168:171], v[64:79]
	ds_read_b128 v[168:171], v192 offset:51200
	v_mul_f32_e32 v237, v216, v232
	v_fmac_f32_e32 v236, v217, v229
	v_exp_f32_e32 v202, v50
	v_mfma_f32_32x32x16_f16 v[80:95], a[84:87], v[172:175], v[80:95]
	ds_read_b128 v[172:175], v192 offset:52224
	global_load_lds_dwordx4 v192, s[44:45] offset:3072 sc1
	v_fmac_f32_e32 v237, v217, v233
	v_fmac_f32_e32 v236, v218, v230
	v_exp_f32_e32 v203, v51
	v_mfma_f32_32x32x16_f16 v[64:79], a[88:91], v[176:179], v[64:79]
	ds_read_b128 v[176:179], v192 offset:53248
	v_fmac_f32_e32 v237, v218, v234
	v_fmac_f32_e32 v236, v219, v231
	v_exp_f32_e32 v204, v52
	v_mfma_f32_32x32x16_f16 v[80:95], a[88:91], v[180:183], v[80:95]
	ds_read_b128 v[180:183], v192 offset:54272
	v_fmac_f32_e32 v237, v219, v235
	v_mov_b32_e32 v238, v236
	v_exp_f32_e32 v205, v53
	v_mfma_f32_32x32x16_f16 v[64:79], a[92:95], v[184:187], v[64:79]
	ds_read_b128 v[184:187], v192 offset:55296
	v_mov_b32_e32 v239, v236
	v_mov_b32_e32 v240, v237
	v_exp_f32_e32 v206, v54
	v_mfma_f32_32x32x16_f16 v[80:95], a[92:95], v[188:191], v[80:95]
	ds_read_b128 v[188:191], v192 offset:56320
	s_mov_b32 m0, s59
	s_add_u32 s44, s34, 0x19000
	s_addc_u32 s45, s35, 0
	global_load_lds_dwordx4 v192, s[44:45] sc1
	v_mov_b32_e32 v241, v237
	v_cvt_pk_f16_f32 v220, v216, v217
	v_exp_f32_e32 v207, v55
	s_waitcnt lgkmcnt(2)
	v_mfma_f32_32x32x16_f16 v[64:79], a[96:99], v[160:163], v[64:79]
	ds_read_b128 v[160:163], v192 offset:57344
	s_nop 1
	v_permlane32_swap_b32_e32 v238, v239
	v_permlane32_swap_b32_e32 v240, v241
	v_add_f32_e32 v238, v238, v239
	v_add_f32_e32 v239, v240, v241
	ds_write_b64 v248, v[238:239] offset:512
	v_exp_f32_e32 v208, v56
	v_mfma_f32_32x32x16_f16 v[80:95], a[96:99], v[164:167], v[80:95]
	ds_read_b128 v[164:167], v192 offset:58368
	v_cvt_pk_f16_f32 v221, v218, v219
	v_exp_f32_e32 v209, v57
	v_add_f32_e32 v200, 1.0, v200
	v_mfma_f32_32x32x16_f16 v[64:79], a[100:103], v[168:171], v[64:79]
	ds_read_b128 v[168:171], v192 offset:59392
	v_exp_f32_e32 v210, v58
	v_add_f32_e32 v201, 1.0, v201
	v_add_f32_e32 v202, 1.0, v202
	v_mfma_f32_32x32x16_f16 v[80:95], a[100:103], v[172:175], v[80:95]
	ds_read_b128 v[172:175], v192 offset:60416
	global_load_lds_dwordx4 v192, s[44:45] offset:1024 sc1
	v_exp_f32_e32 v211, v59
	v_add_f32_e32 v203, 1.0, v203
	v_add_f32_e32 v204, 1.0, v204
	v_mfma_f32_32x32x16_f16 v[64:79], a[104:107], v[176:179], v[64:79]
	ds_read_b128 v[176:179], v192 offset:61440
	v_exp_f32_e32 v212, v60
	v_add_f32_e32 v205, 1.0, v205
	v_add_f32_e32 v206, 1.0, v206
	v_mfma_f32_32x32x16_f16 v[80:95], a[104:107], v[180:183], v[80:95]
	ds_read_b128 v[180:183], v192 offset:62464
	v_exp_f32_e32 v213, v61
	v_add_f32_e32 v207, 1.0, v207
	v_add_f32_e32 v208, 1.0, v208
	s_waitcnt lgkmcnt(2)
	v_mfma_f32_32x32x16_f16 v[64:79], a[108:111], v[184:187], v[64:79]
	ds_read_b128 v[184:187], v192 offset:63488
	v_exp_f32_e32 v214, v62
	v_add_f32_e32 v209, 1.0, v209
	v_add_f32_e32 v210, 1.0, v210
	v_mfma_f32_32x32x16_f16 v[80:95], a[108:111], v[188:191], v[80:95]
	ds_read_b128 v[188:191], v192 offset:64512
	global_load_lds_dwordx4 v192, s[44:45] offset:2048 sc1
	v_exp_f32_e32 v215, v63
	v_add_f32_e32 v211, 1.0, v211
	v_add_f32_e32 v212, 1.0, v212
	s_waitcnt vmcnt(7)
	s_barrier
	v_mfma_f32_32x32x16_f16 v[64:79], a[112:115], v[160:163], v[64:79]
	ds_read_b128 v[160:163], v193 offset:0
	v_add_f32_e32 v213, 1.0, v213
	v_add_f32_e32 v214, 1.0, v214
	v_rcp_f32_e32 v200, v200
	v_mfma_f32_32x32x16_f16 v[80:95], a[112:115], v[164:167], v[80:95]
	ds_read_b128 v[164:167], v193 offset:1024
	v_add_f32_e32 v215, 1.0, v215
	v_rcp_f32_e32 v201, v201
	v_mfma_f32_32x32x16_f16 v[64:79], a[116:119], v[168:171], v[64:79]
	ds_read_b128 v[168:171], v193 offset:2048
	v_rcp_f32_e32 v202, v202
	v_mfma_f32_32x32x16_f16 v[80:95], a[116:119], v[172:175], v[80:95]
	ds_read_b128 v[172:175], v193 offset:3072
	global_load_lds_dwordx4 v192, s[44:45] offset:3072 sc1
	v_rcp_f32_e32 v203, v203
	s_waitcnt lgkmcnt(2)
	v_mfma_f32_32x32x16_f16 v[64:79], a[120:123], v[176:179], v[64:79]
	ds_read_b128 v[176:179], v193 offset:4096
	v_rcp_f32_e32 v204, v204
	s_add_u32 s46, s42, 0x0
	s_addc_u32 s47, s43, 0
	global_load_dwordx4 v[0:3], v192, s[46:47] offset:0
	v_mfma_f32_32x32x16_f16 v[80:95], a[120:123], v[180:183], v[80:95]
	ds_read_b128 v[180:183], v193 offset:5120
	v_rcp_f32_e32 v205, v205
	v_mul_f32_e32 v204, v204, v140
	global_load_dwordx4 v[4:7], v192, s[46:47] offset:1024
	global_load_dwordx4 v[8:11], v192, s[46:47] offset:2048
	v_mfma_f32_32x32x16_f16 v[64:79], a[124:127], v[184:187], v[64:79]
	ds_read_b128 v[184:187], v193 offset:6144
	v_rcp_f32_e32 v206, v206
	v_mul_f32_e32 v205, v205, v141
	global_load_dwordx4 v[12:15], v192, s[46:47] offset:3072
	s_add_u32 s46, s42, 0x1000
	s_addc_u32 s47, s43, 0
	v_mfma_f32_32x32x16_f16 v[80:95], a[124:127], v[188:191], v[80:95]
	ds_read_b128 v[188:191], v193 offset:7168
	v_cmp_gt_u32_e32 vcc, 4, v251
	s_cbranch_vccnz .LD_tpoll33
.LD_tok32:
	s_and_b32 s64, s71, 1
	s_lshl_b32 s64, s64, 22
	s_add_u32 s64, s64, s49
	s_add_u32 s64, s64, 0x60000
	s_add_u32 s34, s6, s64
	s_addc_u32 s35, s7, 0
	s_mov_b32 m0, s52
	s_add_u32 s44, s34, 0x0
	s_addc_u32 s45, s35, 0
	global_load_lds_dwordx4 v192, s[44:45] sc1
	v_rcp_f32_e32 v207, v207
	v_mul_f32_e32 v206, v206, v142
	global_load_dwordx4 v[16:19], v192, s[46:47] offset:0
	global_load_dwordx4 v[20:23], v192, s[46:47] offset:1024
	v_mfma_f32_32x32x16_f16 v[64:79], a[128:131], v[160:163], v[64:79]
	ds_read_b128 v[160:163], v193 offset:8192
	v_rcp_f32_e32 v208, v208
	v_mul_f32_e32 v207, v207, v143
	global_load_dwordx4 v[24:27], v192, s[46:47] offset:2048
	global_load_dwordx4 v[28:31], v192, s[46:47] offset:3072
	v_mfma_f32_32x32x16_f16 v[80:95], a[128:131], v[164:167], v[80:95]
	ds_read_b128 v[164:167], v193 offset:9216
	v_rcp_f32_e32 v209, v209
	v_fmamk_f32 v208, v208, 0xc0b8aa3b, v198
	s_waitcnt lgkmcnt(2)
	v_mfma_f32_32x32x16_f16 v[64:79], a[132:135], v[168:171], v[64:79]
	ds_read_b128 v[168:171], v193 offset:10240
	v_rcp_f32_e32 v210, v210
	v_fmamk_f32 v209, v209, 0xc0b8aa3b, v198
	v_fma_f32 v140, v200, v208, v204
	v_mfma_f32_32x32x16_f16 v[80:95], a[132:135], v[172:175], v[80:95]
	ds_read_b128 v[172:175], v193 offset:11264
	global_load_lds_dwordx4 v192, s[44:45] offset:1024 sc1
	v_rcp_f32_e32 v211, v211
	v_fmamk_f32 v210, v210, 0xc0b8aa3b, v198
	v_fma_f32 v141, v201, v209, v205
	v_mfma_f32_32x32x16_f16 v[64:79], a[136:139], v[176:179], v[64:79]
	ds_read_b128 v[176:179], v193 offset:12288
	v_rcp_f32_e32 v212, v212
	v_fmamk_f32 v211, v211, 0xc0b8aa3b, v198
	v_fma_f32 v142, v202, v210, v206
	v_mfma_f32_32x32x16_f16 v[80:95], a[136:139], v[180:183], v[80:95]
	ds_read_b128 v[180:183], v193 offset:13312
	v_rcp_f32_e32 v213, v213
	v_fma_f32 v143, v203, v211, v207
	v_mfma_f32_32x32x16_f16 v[64:79], a[140:143], v[184:187], v[64:79]
	ds_read_b128 v[184:187], v193 offset:14336
	v_rcp_f32_e32 v214, v214
	v_mfma_f32_32x32x16_f16 v[80:95], a[140:143], v[188:191], v[80:95]
	ds_read_b128 v[188:191], v193 offset:15360
	global_load_lds_dwordx4 v192, s[44:45] offset:2048 sc1
	v_rcp_f32_e32 v215, v215
	s_waitcnt lgkmcnt(2)
	v_mfma_f32_32x32x16_f16 v[64:79], a[144:147], v[160:163], v[64:79]
	ds_read_b128 v[160:163], v193 offset:16384
	v_exp_f32_e32 v200, v140
	v_mfma_f32_32x32x16_f16 v[80:95], a[144:147], v[164:167], v[80:95]
	ds_read_b128 v[164:167], v193 offset:17408
	v_exp_f32_e32 v201, v141
	v_add_f32_e32 v200, 1.0, v200
	v_mfma_f32_32x32x16_f16 v[64:79], a[148:151], v[168:171], v[64:79]
	ds_read_b128 v[168:171], v193 offset:18432
	v_exp_f32_e32 v202, v142
	v_add_f32_e32 v201, 1.0, v201
	v_mfma_f32_32x32x16_f16 v[80:95], a[148:151], v[172:175], v[80:95]
	ds_read_b128 v[172:175], v193 offset:19456
	global_load_lds_dwordx4 v192, s[44:45] offset:3072 sc1
	v_exp_f32_e32 v203, v143
	v_add_f32_e32 v202, 1.0, v202
	v_mfma_f32_32x32x16_f16 v[64:79], a[152:155], v[176:179], v[64:79]
	ds_read_b128 v[176:179], v193 offset:20480
	v_add_f32_e32 v203, 1.0, v203
	v_rcp_f32_e32 v200, v200
	v_mfma_f32_32x32x16_f16 v[80:95], a[152:155], v[180:183], v[80:95]
	ds_read_b128 v[180:183], v193 offset:21504
	v_rcp_f32_e32 v201, v201
	v_fma_f32 v200, v200, 2.0, -1.0
	s_waitcnt lgkmcnt(2)
	v_mfma_f32_32x32x16_f16 v[64:79], a[156:159], v[184:187], v[64:79]
	ds_read_b128 v[184:187], v193 offset:22528
	v_rcp_f32_e32 v202, v202
	v_fma_f32 v201, v201, 2.0, -1.0
	v_mul_f32_e32 v216, v212, v200
	v_mfma_f32_32x32x16_f16 v[80:95], a[156:159], v[188:191], v[80:95]
	ds_read_b128 v[188:191], v193 offset:23552
	s_mov_b32 m0, s53
	s_add_u32 s44, s34, 0x1000
	s_addc_u32 s45, s35, 0
	global_load_lds_dwordx4 v192, s[44:45] sc1
	v_rcp_f32_e32 v203, v203
	v_fma_f32 v202, v202, 2.0, -1.0
	v_mul_f32_e32 v217, v213, v201
	v_mfma_f32_32x32x16_f16 v[64:79], a[160:163], v[160:163], v[64:79]
	ds_read_b128 v[160:163], v193 offset:24576
	v_fma_f32 v203, v203, 2.0, -1.0
	v_mul_f32_e32 v218, v214, v202
	v_mfma_f32_32x32x16_f16 v[80:95], a[160:163], v[164:167], v[80:95]
	ds_read_b128 v[164:167], v193 offset:25600
	v_mul_f32_e32 v219, v215, v203
	v_mul_f32_e32 v236, v216, v228
	v_mfma_f32_32x32x16_f16 v[64:79], a[164:167], v[168:171], v[64:79]
	ds_read_b128 v[168:171], v193 offset:26624
	v_mul_f32_e32 v237, v216, v232
	v_fmac_f32_e32 v236, v217, v229
	v_mfma_f32_32x32x16_f16 v[80:95], a[164:167], v[172:175], v[80:95]
	ds_read_b128 v[172:175], v193 offset:27648
	global_load_lds_dwordx4 v192, s[44:45] offset:1024 sc1
	v_fmac_f32_e32 v237, v217, v233
	v_fmac_f32_e32 v236, v218, v230
	s_waitcnt lgkmcnt(2)
	v_mfma_f32_32x32x16_f16 v[64:79], a[168:171], v[176:179], v[64:79]
	ds_read_b128 v[176:179], v193 offset:28672
	v_fmac_f32_e32 v237, v218, v234
	v_fmac_f32_e32 v236, v219, v231
	v_mfma_f32_32x32x16_f16 v[80:95], a[168:171], v[180:183], v[80:95]
	ds_read_b128 v[180:183], v193 offset:29696
	v_fmac_f32_e32 v237, v219, v235
	v_mov_b32_e32 v238, v236
	v_mfma_f32_32x32x16_f16 v[64:79], a[172:175], v[184:187], v[64:79]
	ds_read_b128 v[184:187], v193 offset:30720
	v_mov_b32_e32 v239, v236
	v_mov_b32_e32 v240, v237
	v_mfma_f32_32x32x16_f16 v[80:95], a[172:175], v[188:191], v[80:95]
	ds_read_b128 v[188:191], v193 offset:31744
	global_load_lds_dwordx4 v192, s[44:45] offset:2048 sc1
	v_mov_b32_e32 v241, v237
	v_cvt_pk_f16_f32 v222, v216, v217
	s_waitcnt vmcnt(15)
	s_barrier
	v_mfma_f32_32x32x16_f16 v[64:79], a[176:179], v[160:163], v[64:79]
	ds_read_b128 v[160:163], v193 offset:32768
	s_nop 1
	v_permlane32_swap_b32_e32 v238, v239
	v_permlane32_swap_b32_e32 v240, v241
	v_add_f32_e32 v238, v238, v239
	v_add_f32_e32 v239, v240, v241
	ds_write_b64 v248, v[238:239] offset:768
	v_mfma_f32_32x32x16_f16 v[80:95], a[176:179], v[164:167], v[80:95]
	ds_read_b128 v[164:167], v193 offset:33792
	v_cvt_pk_f16_f32 v223, v218, v219
	s_waitcnt lgkmcnt(3)
	v_mfma_f32_32x32x16_f16 v[64:79], a[180:183], v[168:171], v[64:79]
	ds_read_b128 v[168:171], v193 offset:34816
	s_nop 1
	v_permlane32_swap_b32_e32 v220, v222
	v_permlane32_swap_b32_e32 v221, v223
	s_cmp_eq_u32 s31, 0
	s_cbranch_scc1 .LD_slow34
	global_store_dwordx4 v195, v[220:223], s[36:37] offset:0
.LD_join35:
	v_mfma_f32_32x32x16_f16 v[80:95], a[180:183], v[172:175], v[80:95]
	ds_read_b128 v[172:175], v193 offset:35840
	global_load_lds_dwordx4 v192, s[44:45] offset:3072 sc1
	v_mfma_f32_32x32x16_f16 v[64:79], a[184:187], v[176:179], v[64:79]
	ds_read_b128 v[176:179], v193 offset:36864
	v_mfma_f32_32x32x16_f16 v[80:95], a[184:187], v[180:183], v[80:95]
	ds_read_b128 v[180:183], v193 offset:37888
	v_mfma_f32_32x32x16_f16 v[64:79], a[188:191], v[184:187], v[64:79]
	ds_read_b128 v[184:187], v193 offset:38912
	v_mfma_f32_32x32x16_f16 v[80:95], a[188:191], v[188:191], v[80:95]
	ds_read_b128 v[188:191], v193 offset:39936
	s_mov_b32 m0, s54
	s_add_u32 s44, s34, 0x8000
	s_addc_u32 s45, s35, 0
	global_load_lds_dwordx4 v192, s[44:45] sc1
	s_waitcnt lgkmcnt(2)
	v_mfma_f32_32x32x16_f16 v[64:79], a[192:195], v[160:163], v[64:79]
	ds_read_b128 v[160:163], v193 offset:40960
	v_mfma_f32_32x32x16_f16 v[80:95], a[192:195], v[164:167], v[80:95]
	ds_read_b128 v[164:167], v193 offset:41984
	v_mfma_f32_32x32x16_f16 v[64:79], a[196:199], v[168:171], v[64:79]
	ds_read_b128 v[168:171], v193 offset:43008
	v_mfma_f32_32x32x16_f16 v[80:95], a[196:199], v[172:175], v[80:95]
	ds_read_b128 v[172:175], v193 offset:44032
	global_load_lds_dwordx4 v192, s[44:45] offset:1024 sc1
	v_mfma_f32_32x32x16_f16 v[64:79], a[200:203], v[176:179], v[64:79]
	ds_read_b128 v[176:179], v193 offset:45056
	v_mfma_f32_32x32x16_f16 v[80:95], a[200:203], v[180:183], v[80:95]
	ds_read_b128 v[180:183], v193 offset:46080
	s_waitcnt lgkmcnt(2)
	v_mfma_f32_32x32x16_f16 v[64:79], a[204:207], v[184:187], v[64:79]
	ds_read_b128 v[184:187], v193 offset:47104
	v_mfma_f32_32x32x16_f16 v[80:95], a[204:207], v[188:191], v[80:95]
	ds_read_b128 v[188:191], v193 offset:48128
	global_load_lds_dwordx4 v192, s[44:45] offset:2048 sc1
	s_waitcnt vmcnt(4)
	s_barrier
	v_mov_b32_e32 v199, 2
	s_cmp_eq_u32 s31, 0
	s_cbranch_scc1 .LD_slow36
	global_store_dword v197, v199, s[40:41]
.LD_join37:
	ds_read_b64 v[200:201], v249 offset:512
	ds_read_b64 v[202:203], v249 offset:2560
	ds_read_b64 v[204:205], v249 offset:4608
	ds_read_b64 v[206:207], v249 offset:6656
	v_mfma_f32_32x32x16_f16 v[64:79], a[208:211], v[160:163], v[64:79]
	ds_read_b128 v[160:163], v193 offset:49152
	v_mfma_f32_32x32x16_f16 v[80:95], a[208:211], v[164:167], v[80:95]
	ds_read_b128 v[164:167], v193 offset:50176
	v_mfma_f32_32x32x16_f16 v[64:79], a[212:215], v[168:171], v[64:79]
	ds_read_b128 v[168:171], v193 offset:51200
	v_mfma_f32_32x32x16_f16 v[80:95], a[212:215], v[172:175], v[80:95]
	ds_read_b128 v[172:175], v193 offset:52224
	global_load_lds_dwordx4 v192, s[44:45] offset:3072 sc1
	s_waitcnt lgkmcnt(2)
	v_mfma_f32_32x32x16_f16 v[64:79], a[216:219], v[176:179], v[64:79]
	ds_read_b128 v[176:179], v193 offset:53248
	v_mfma_f32_32x32x16_f16 v[80:95], a[216:219], v[180:183], v[80:95]
	ds_read_b128 v[180:183], v193 offset:54272
	v_mfma_f32_32x32x16_f16 v[64:79], a[220:223], v[184:187], v[64:79]
	ds_read_b128 v[184:187], v193 offset:55296
	v_mfma_f32_32x32x16_f16 v[80:95], a[220:223], v[188:191], v[80:95]
	ds_read_b128 v[188:191], v193 offset:56320
	s_mov_b32 m0, s55
	s_add_u32 s44, s34, 0x9000
	s_addc_u32 s45, s35, 0
	global_load_lds_dwordx4 v192, s[44:45] sc1
	v_mfma_f32_32x32x16_f16 v[64:79], a[224:227], v[160:163], v[64:79]
	ds_read_b128 v[160:163], v193 offset:57344
	v_mfma_f32_32x32x16_f16 v[80:95], a[224:227], v[164:167], v[80:95]
	ds_read_b128 v[164:167], v193 offset:58368
	s_waitcnt lgkmcnt(2)
	v_mfma_f32_32x32x16_f16 v[64:79], a[228:231], v[168:171], v[64:79]
	ds_read_b128 v[168:171], v193 offset:59392
	v_mfma_f32_32x32x16_f16 v[80:95], a[228:231], v[172:175], v[80:95]
	ds_read_b128 v[172:175], v193 offset:60416
	global_load_lds_dwordx4 v192, s[44:45] offset:1024 sc1
	v_add_f32_e32 v200, v200, v202
	v_add_f32_e32 v201, v201, v203
	v_add_f32_e32 v200, v200, v204
	v_add_f32_e32 v201, v201, v205
	v_add_f32_e32 v200, v200, v206
	v_add_f32_e32 v201, v201, v207
	global_store_dwordx2 v250, v[200:201], s[72:73]
	v_mfma_f32_32x32x16_f16 v[64:79], a[232:235], v[176:179], v[64:79]
	ds_read_b128 v[176:179], v193 offset:61440
	v_mfma_f32_32x32x16_f16 v[80:95], a[232:235], v[180:183], v[80:95]
	ds_read_b128 v[180:183], v193 offset:62464
	v_mfma_f32_32x32x16_f16 v[64:79], a[236:239], v[184:187], v[64:79]
	ds_read_b128 v[184:187], v193 offset:63488
	v_mfma_f32_32x32x16_f16 v[80:95], a[236:239], v[188:191], v[80:95]
	ds_read_b128 v[188:191], v193 offset:64512
	global_load_lds_dwordx4 v192, s[44:45] offset:2048 sc1
	s_and_b32 s64, s33, 1
	s_lshl_b32 s64, s64, 22
	s_add_u32 s64, s64, s50
	s_add_u32 s64, s64, 0x40000
	s_add_u32 s36, s6, s64
	s_addc_u32 s37, s7, 0
	s_lshl_b32 s64, s33, 3
	s_add_u32 s64, s64, s29
	s_lshl_b32 s64, s64, 5
	s_add_u32 s64, s64, s30
	s_lshl_b32 s64, s64, 2
	s_add_u32 s40, s8, s64
	s_addc_u32 s41, s9, 0
	s_lshl_b32 s64, s33, 19
	s_add_u32 s64, s64, 0x400
	s_add_u32 s72, s62, s64
	s_addc_u32 s73, s63, 0
	s_waitcnt vmcnt(9)
	s_barrier
	s_waitcnt lgkmcnt(2)
	v_mfma_f32_32x32x16_f16 v[64:79], a[240:243], v[160:163], v[64:79]
	ds_read_b128 v[160:163], v192 offset:0
	v_mfma_f32_32x32x16_f16 v[80:95], a[240:243], v[164:167], v[80:95]
	ds_read_b128 v[164:167], v192 offset:1024
	v_mfma_f32_32x32x16_f16 v[64:79], a[244:247], v[168:171], v[64:79]
	ds_read_b128 v[168:171], v192 offset:2048
	v_mfma_f32_32x32x16_f16 v[80:95], a[244:247], v[172:175], v[80:95]
	ds_read_b128 v[172:175], v192 offset:3072
	global_load_lds_dwordx4 v192, s[44:45] offset:3072 sc1
	v_mfma_f32_32x32x16_f16 v[64:79], a[248:251], v[176:179], v[64:79]
	ds_read_b128 v[176:179], v192 offset:4096
	v_mfma_f32_32x32x16_f16 v[80:95], a[248:251], v[180:183], v[80:95]
	ds_read_b128 v[180:183], v192 offset:5120
	s_waitcnt lgkmcnt(2)
	v_mfma_f32_32x32x16_f16 v[64:79], a[252:255], v[184:187], v[64:79]
	ds_read_b128 v[184:187], v192 offset:6144
	v_mfma_f32_32x32x16_f16 v[80:95], a[252:255], v[188:191], v[80:95]
	ds_read_b128 v[188:191], v192 offset:7168
	s_mov_b32 m0, s56
	s_add_u32 s44, s34, 0x10000
	s_addc_u32 s45, s35, 0
	global_load_lds_dwordx4 v192, s[44:45] sc1
	s_nop 3
	s_waitcnt lgkmcnt(2)
	v_mfma_f32_32x32x16_f16 v[96:111], a[0:3], v[160:163], v[96:111]
	ds_read_b128 v[160:163], v192 offset:8192
	v_exp_f32_e32 v200, v64
	v_mfma_f32_32x32x16_f16 v[112:127], a[0:3], v[164:167], v[112:127]
	ds_read_b128 v[164:167], v192 offset:9216
	s_lshl_b32 s64, s33, 3
	s_add_u32 s64, s64, s29
	s_lshl_b32 s64, s64, 7
	s_add_u32 s38, s8, s64
	s_addc_u32 s39, s9, 0
	global_load_dword v251, v196, s[38:39] sc1
	v_exp_f32_e32 v201, v65
	v_add_f32_e32 v200, 1.0, v200
	v_mfma_f32_32x32x16_f16 v[96:111], a[4:7], v[168:171], v[96:111]
	ds_read_b128 v[168:171], v192 offset:10240
	v_exp_f32_e32 v202, v66
	v_add_f32_e32 v201, 1.0, v201
	v_mfma_f32_32x32x16_f16 v[112:127], a[4:7], v[172:175], v[112:127]
	ds_read_b128 v[172:175], v192 offset:11264
	global_load_lds_dwordx4 v192, s[44:45] offset:1024 sc1
	v_exp_f32_e32 v203, v67
	v_add_f32_e32 v202, 1.0, v202
	v_mfma_f32_32x32x16_f16 v[96:111], a[8:11], v[176:179], v[96:111]
	ds_read_b128 v[176:179], v192 offset:12288
	v_exp_f32_e32 v204, v68
	v_add_f32_e32 v203, 1.0, v203
	v_mfma_f32_32x32x16_f16 v[112:127], a[8:11], v[180:183], v[112:127]
	ds_read_b128 v[180:183], v192 offset:13312
	v_exp_f32_e32 v205, v69
	v_add_f32_e32 v204, 1.0, v204
	s_waitcnt lgkmcnt(2)
	v_mfma_f32_32x32x16_f16 v[96:111], a[12:15], v[184:187], v[96:111]
	ds_read_b128 v[184:187], v192 offset:14336
	v_exp_f32_e32 v206, v70
	v_add_f32_e32 v205, 1.0, v205
	v_mfma_f32_32x32x16_f16 v[112:127], a[12:15], v[188:191], v[112:127]
	ds_read_b128 v[188:191], v192 offset:15360
	global_load_lds_dwordx4 v192, s[44:45] offset:2048 sc1
	v_exp_f32_e32 v207, v71
	v_add_f32_e32 v206, 1.0, v206
	v_mfma_f32_32x32x16_f16 v[96:111], a[16:19], v[160:163], v[96:111]
	ds_read_b128 v[160:163], v192 offset:16384
	v_exp_f32_e32 v208, v72
	v_add_f32_e32 v207, 1.0, v207
	v_mfma_f32_32x32x16_f16 v[112:127], a[16:19], v[164:167], v[112:127]
	ds_read_b128 v[164:167], v192 offset:17408
	v_exp_f32_e32 v209, v73
	v_add_f32_e32 v208, 1.0, v208
	v_mfma_f32_32x32x16_f16 v[96:111], a[20:23], v[168:171], v[96:111]
	ds_read_b128 v[168:171], v192 offset:18432
	v_exp_f32_e32 v210, v74
	v_add_f32_e32 v209, 1.0, v209
	v_mfma_f32_32x32x16_f16 v[112:127], a[20:23], v[172:175], v[112:127]
	ds_read_b128 v[172:175], v192 offset:19456
	global_load_lds_dwordx4 v192, s[44:45] offset:3072 sc1
	v_exp_f32_e32 v211, v75
	v_add_f32_e32 v210, 1.0, v210
	s_waitcnt lgkmcnt(2)
	v_mfma_f32_32x32x16_f16 v[96:111], a[24:27], v[176:179], v[96:111]
	ds_read_b128 v[176:179], v192 offset:20480
	v_exp_f32_e32 v212, v76
	v_add_f32_e32 v211, 1.0, v211
	v_mfma_f32_32x32x16_f16 v[112:127], a[24:27], v[180:183], v[112:127]
	ds_read_b128 v[180:183], v192 offset:21504
	v_exp_f32_e32 v213, v77
	v_add_f32_e32 v212, 1.0, v212
	v_mfma_f32_32x32x16_f16 v[96:111], a[28:31], v[184:187], v[96:111]
	ds_read_b128 v[184:187], v192 offset:22528
	v_exp_f32_e32 v214, v78
	v_add_f32_e32 v213, 1.0, v213
	v_mfma_f32_32x32x16_f16 v[112:127], a[28:31], v[188:191], v[112:127]
	ds_read_b128 v[188:191], v192 offset:23552
	s_mov_b32 m0, s57
	s_add_u32 s44, s34, 0x11000
	s_addc_u32 s45, s35, 0
	global_load_lds_dwordx4 v192, s[44:45] sc1
	v_exp_f32_e32 v215, v79
	v_add_f32_e32 v214, 1.0, v214
	v_mfma_f32_32x32x16_f16 v[96:111], a[32:35], v[160:163], v[96:111]
	ds_read_b128 v[160:163], v192 offset:24576
	v_add_f32_e32 v215, 1.0, v215
	v_rcp_f32_e32 v200, v200
	v_mfma_f32_32x32x16_f16 v[112:127], a[32:35], v[164:167], v[112:127]
	ds_read_b128 v[164:167], v192 offset:25600
	v_rcp_f32_e32 v201, v201
	s_waitcnt lgkmcnt(2)
	v_mfma_f32_32x32x16_f16 v[96:111], a[36:39], v[168:171], v[96:111]
	ds_read_b128 v[168:171], v192 offset:26624
	v_rcp_f32_e32 v202, v202
	v_mfma_f32_32x32x16_f16 v[112:127], a[36:39], v[172:175], v[112:127]
	ds_read_b128 v[172:175], v192 offset:27648
	global_load_lds_dwordx4 v192, s[44:45] offset:1024 sc1
	v_rcp_f32_e32 v203, v203
	v_mfma_f32_32x32x16_f16 v[96:111], a[40:43], v[176:179], v[96:111]
	ds_read_b128 v[176:179], v192 offset:28672
	v_rcp_f32_e32 v204, v204
	v_mfma_f32_32x32x16_f16 v[112:127], a[40:43], v[180:183], v[112:127]
	ds_read_b128 v[180:183], v192 offset:29696
	v_rcp_f32_e32 v205, v205
	v_mul_f32_e32 v204, v204, v144
	v_mfma_f32_32x32x16_f16 v[96:111], a[44:47], v[184:187], v[96:111]
	ds_read_b128 v[184:187], v192 offset:30720
	v_rcp_f32_e32 v206, v206
	v_mul_f32_e32 v205, v205, v145
	v_mfma_f32_32x32x16_f16 v[112:127], a[44:47], v[188:191], v[112:127]
	ds_read_b128 v[188:191], v192 offset:31744
	global_load_lds_dwordx4 v192, s[44:45] offset:2048 sc1
	v_rcp_f32_e32 v207, v207
	v_mul_f32_e32 v206, v206, v146
	s_waitcnt vmcnt(8)
	s_barrier
	s_waitcnt lgkmcnt(2)
	v_mfma_f32_32x32x16_f16 v[96:111], a[48:51], v[160:163], v[96:111]
	ds_read_b128 v[160:163], v192 offset:32768
	v_rcp_f32_e32 v208, v208
	v_mul_f32_e32 v207, v207, v147
	v_mfma_f32_32x32x16_f16 v[112:127], a[48:51], v[164:167], v[112:127]
	ds_read_b128 v[164:167], v192 offset:33792
	v_rcp_f32_e32 v209, v209
	v_fmamk_f32 v208, v208, 0xc0b8aa3b, v198
	v_mfma_f32_32x32x16_f16 v[96:111], a[52:55], v[168:171], v[96:111]
	ds_read_b128 v[168:171], v192 offset:34816
	v_rcp_f32_e32 v210, v210
	v_fmamk_f32 v209, v209, 0xc0b8aa3b, v198
	v_fma_f32 v144, v200, v208, v204
	v_mfma_f32_32x32x16_f16 v[112:127], a[52:55], v[172:175], v[112:127]
	ds_read_b128 v[172:175], v192 offset:35840
	global_load_lds_dwordx4 v192, s[44:45] offset:3072 sc1
	v_rcp_f32_e32 v211, v211
	v_fmamk_f32 v210, v210, 0xc0b8aa3b, v198
	v_fma_f32 v145, v201, v209, v205
	v_mfma_f32_32x32x16_f16 v[96:111], a[56:59], v[176:179], v[96:111]
	ds_read_b128 v[176:179], v192 offset:36864
	v_rcp_f32_e32 v212, v212
	v_fmamk_f32 v211, v211, 0xc0b8aa3b, v198
	v_fma_f32 v146, v202, v210, v206
	v_mfma_f32_32x32x16_f16 v[112:127], a[56:59], v[180:183], v[112:127]
	ds_read_b128 v[180:183], v192 offset:37888
	v_rcp_f32_e32 v213, v213
	v_fma_f32 v147, v203, v211, v207
	s_waitcnt lgkmcnt(2)
	v_mfma_f32_32x32x16_f16 v[96:111], a[60:63], v[184:187], v[96:111]
	ds_read_b128 v[184:187], v192 offset:38912
	v_rcp_f32_e32 v214, v214
	v_mfma_f32_32x32x16_f16 v[112:127], a[60:63], v[188:191], v[112:127]
	ds_read_b128 v[188:191], v192 offset:39936
	s_mov_b32 m0, s58
	s_add_u32 s44, s34, 0x18000
	s_addc_u32 s45, s35, 0
	global_load_lds_dwordx4 v192, s[44:45] sc1
	v_rcp_f32_e32 v215, v215
	v_mfma_f32_32x32x16_f16 v[96:111], a[64:67], v[160:163], v[96:111]
	ds_read_b128 v[160:163], v192 offset:40960
	v_exp_f32_e32 v200, v144
	v_mfma_f32_32x32x16_f16 v[112:127], a[64:67], v[164:167], v[112:127]
	ds_read_b128 v[164:167], v192 offset:41984
	v_exp_f32_e32 v201, v145
	v_add_f32_e32 v200, 1.0, v200
	v_mfma_f32_32x32x16_f16 v[96:111], a[68:71], v[168:171], v[96:111]
	ds_read_b128 v[168:171], v192 offset:43008
	v_exp_f32_e32 v202, v146
	v_add_f32_e32 v201, 1.0, v201
	v_mfma_f32_32x32x16_f16 v[112:127], a[68:71], v[172:175], v[112:127]
	ds_read_b128 v[172:175], v192 offset:44032
	global_load_lds_dwordx4 v192, s[44:45] offset:1024 sc1
	v_exp_f32_e32 v203, v147
	v_add_f32_e32 v202, 1.0, v202
	s_waitcnt lgkmcnt(2)
	v_mfma_f32_32x32x16_f16 v[96:111], a[72:75], v[176:179], v[96:111]
	ds_read_b128 v[176:179], v192 offset:45056
	v_add_f32_e32 v203, 1.0, v203
	v_rcp_f32_e32 v200, v200
	v_mfma_f32_32x32x16_f16 v[112:127], a[72:75], v[180:183], v[112:127]
	ds_read_b128 v[180:183], v192 offset:46080
	v_rcp_f32_e32 v201, v201
	v_fma_f32 v200, v200, 2.0, -1.0
	v_mfma_f32_32x32x16_f16 v[96:111], a[76:79], v[184:187], v[96:111]
	ds_read_b128 v[184:187], v192 offset:47104
	v_rcp_f32_e32 v202, v202
	v_fma_f32 v201, v201, 2.0, -1.0
	v_mul_f32_e32 v216, v212, v200
	v_mfma_f32_32x32x16_f16 v[112:127], a[76:79], v[188:191], v[112:127]
	ds_read_b128 v[188:191], v192 offset:48128
	global_load_lds_dwordx4 v192, s[44:45] offset:2048 sc1
	v_rcp_f32_e32 v203, v203
	v_fma_f32 v202, v202, 2.0, -1.0
	v_mul_f32_e32 v217, v213, v201
	v_mfma_f32_32x32x16_f16 v[96:111], a[80:83], v[160:163], v[96:111]
	ds_read_b128 v[160:163], v192 offset:49152
	v_fma_f32 v203, v203, 2.0, -1.0
	v_mul_f32_e32 v218, v214, v202
	v_exp_f32_e32 v200, v80
	v_mfma_f32_32x32x16_f16 v[112:127], a[80:83], v[164:167], v[112:127]
	ds_read_b128 v[164:167], v192 offset:50176
	v_mul_f32_e32 v219, v215, v203
	v_mul_f32_e32 v236, v216, v228
	v_exp_f32_e32 v201, v81
	s_waitcnt lgkmcnt(2)
	v_mfma_f32_32x32x16_f16 v[96:111], a[84:87], v[168:171], v[96:111]
	ds_read_b128 v[168:171], v192 offset:51200
	v_mul_f32_e32 v237, v216, v232
	v_fmac_f32_e32 v236, v217, v229
	v_exp_f32_e32 v202, v82
	v_mfma_f32_32x32x16_f16 v[112:127], a[84:87], v[172:175], v[112:127]
	ds_read_b128 v[172:175], v192 offset:52224
	global_load_lds_dwordx4 v192, s[44:45] offset:3072 sc1
	v_fmac_f32_e32 v237, v217, v233
	v_fmac_f32_e32 v236, v218, v230
	v_exp_f32_e32 v203, v83
	v_mfma_f32_32x32x16_f16 v[96:111], a[88:91], v[176:179], v[96:111]
	ds_read_b128 v[176:179], v192 offset:53248
	v_fmac_f32_e32 v237, v218, v234
	v_fmac_f32_e32 v236, v219, v231
	v_exp_f32_e32 v204, v84
	v_mfma_f32_32x32x16_f16 v[112:127], a[88:91], v[180:183], v[112:127]
	ds_read_b128 v[180:183], v192 offset:54272
	v_fmac_f32_e32 v237, v219, v235
	v_mov_b32_e32 v238, v236
	v_exp_f32_e32 v205, v85
	v_mfma_f32_32x32x16_f16 v[96:111], a[92:95], v[184:187], v[96:111]
	ds_read_b128 v[184:187], v192 offset:55296
	v_mov_b32_e32 v239, v236
	v_mov_b32_e32 v240, v237
	v_exp_f32_e32 v206, v86
	v_mfma_f32_32x32x16_f16 v[112:127], a[92:95], v[188:191], v[112:127]
	ds_read_b128 v[188:191], v192 offset:56320
	s_mov_b32 m0, s59
	s_add_u32 s44, s34, 0x19000
	s_addc_u32 s45, s35, 0
	global_load_lds_dwordx4 v192, s[44:45] sc1
	v_mov_b32_e32 v241, v237
	v_cvt_pk_f16_f32 v220, v216, v217
	v_exp_f32_e32 v207, v87
	s_waitcnt lgkmcnt(2)
	v_mfma_f32_32x32x16_f16 v[96:111], a[96:99], v[160:163], v[96:111]
	ds_read_b128 v[160:163], v192 offset:57344
	s_nop 1
	v_permlane32_swap_b32_e32 v238, v239
	v_permlane32_swap_b32_e32 v240, v241
	v_add_f32_e32 v238, v238, v239
	v_add_f32_e32 v239, v240, v241
	ds_write_b64 v248, v[238:239] offset:1024
	v_exp_f32_e32 v208, v88
	v_mfma_f32_32x32x16_f16 v[112:127], a[96:99], v[164:167], v[112:127]
	ds_read_b128 v[164:167], v192 offset:58368
	v_cvt_pk_f16_f32 v221, v218, v219
	v_exp_f32_e32 v209, v89
	v_add_f32_e32 v200, 1.0, v200
	v_mfma_f32_32x32x16_f16 v[96:111], a[100:103], v[168:171], v[96:111]
	ds_read_b128 v[168:171], v192 offset:59392
	v_exp_f32_e32 v210, v90
	v_add_f32_e32 v201, 1.0, v201
	v_add_f32_e32 v202, 1.0, v202
	v_mfma_f32_32x32x16_f16 v[112:127], a[100:103], v[172:175], v[112:127]
	ds_read_b128 v[172:175], v192 offset:60416
	global_load_lds_dwordx4 v192, s[44:45] offset:1024 sc1
	v_exp_f32_e32 v211, v91
	v_add_f32_e32 v203, 1.0, v203
	v_add_f32_e32 v204, 1.0, v204
	v_mfma_f32_32x32x16_f16 v[96:111], a[104:107], v[176:179], v[96:111]
	ds_read_b128 v[176:179], v192 offset:61440
	v_exp_f32_e32 v212, v92
	v_add_f32_e32 v205, 1.0, v205
	v_add_f32_e32 v206, 1.0, v206
	v_mfma_f32_32x32x16_f16 v[112:127], a[104:107], v[180:183], v[112:127]
	ds_read_b128 v[180:183], v192 offset:62464
	v_exp_f32_e32 v213, v93
	v_add_f32_e32 v207, 1.0, v207
	v_add_f32_e32 v208, 1.0, v208
	s_waitcnt lgkmcnt(2)
	v_mfma_f32_32x32x16_f16 v[96:111], a[108:111], v[184:187], v[96:111]
	ds_read_b128 v[184:187], v192 offset:63488
	v_exp_f32_e32 v214, v94
	v_add_f32_e32 v209, 1.0, v209
	v_add_f32_e32 v210, 1.0, v210
	v_mfma_f32_32x32x16_f16 v[112:127], a[108:111], v[188:191], v[112:127]
	ds_read_b128 v[188:191], v192 offset:64512
	global_load_lds_dwordx4 v192, s[44:45] offset:2048 sc1
	v_exp_f32_e32 v215, v95
	v_add_f32_e32 v211, 1.0, v211
	v_add_f32_e32 v212, 1.0, v212
	s_waitcnt vmcnt(7)
	s_barrier
	v_mfma_f32_32x32x16_f16 v[96:111], a[112:115], v[160:163], v[96:111]
	ds_read_b128 v[160:163], v193 offset:0
	v_add_f32_e32 v213, 1.0, v213
	v_add_f32_e32 v214, 1.0, v214
	v_rcp_f32_e32 v200, v200
	v_mfma_f32_32x32x16_f16 v[112:127], a[112:115], v[164:167], v[112:127]
	ds_read_b128 v[164:167], v193 offset:1024
	v_add_f32_e32 v215, 1.0, v215
	v_rcp_f32_e32 v201, v201
	v_mfma_f32_32x32x16_f16 v[96:111], a[116:119], v[168:171], v[96:111]
	ds_read_b128 v[168:171], v193 offset:2048
	v_rcp_f32_e32 v202, v202
	v_mfma_f32_32x32x16_f16 v[112:127], a[116:119], v[172:175], v[112:127]
	ds_read_b128 v[172:175], v193 offset:3072
	global_load_lds_dwordx4 v192, s[44:45] offset:3072 sc1
	v_rcp_f32_e32 v203, v203
	s_waitcnt lgkmcnt(2)
	v_mfma_f32_32x32x16_f16 v[96:111], a[120:123], v[176:179], v[96:111]
	ds_read_b128 v[176:179], v193 offset:4096
	v_rcp_f32_e32 v204, v204
	s_add_u32 s46, s42, 0x2000
	s_addc_u32 s47, s43, 0
	global_load_dwordx4 v[32:35], v192, s[46:47] offset:0
	v_mfma_f32_32x32x16_f16 v[112:127], a[120:123], v[180:183], v[112:127]
	ds_read_b128 v[180:183], v193 offset:5120
	v_rcp_f32_e32 v205, v205
	v_mul_f32_e32 v204, v204, v148
	global_load_dwordx4 v[36:39], v192, s[46:47] offset:1024
	global_load_dwordx4 v[40:43], v192, s[46:47] offset:2048
	v_mfma_f32_32x32x16_f16 v[96:111], a[124:127], v[184:187], v[96:111]
	ds_read_b128 v[184:187], v193 offset:6144
	v_rcp_f32_e32 v206, v206
	v_mul_f32_e32 v205, v205, v149
	global_load_dwordx4 v[44:47], v192, s[46:47] offset:3072
	s_add_u32 s46, s42, 0x3000
	s_addc_u32 s47, s43, 0
	v_mfma_f32_32x32x16_f16 v[112:127], a[124:127], v[188:191], v[112:127]
	ds_read_b128 v[188:191], v193 offset:7168
	v_cmp_gt_u32_e32 vcc, 1, v251
	s_cbranch_vccnz .LD_tpoll39
.LD_tok38:
	s_and_b32 s64, s33, 1
	s_lshl_b32 s64, s64, 22
	s_add_u32 s64, s64, s49
	s_add_u32 s34, s6, s64
	s_addc_u32 s35, s7, 0
	s_mov_b32 m0, s52
	s_add_u32 s44, s34, 0x0
	s_addc_u32 s45, s35, 0
	global_load_lds_dwordx4 v192, s[44:45] sc1
	v_rcp_f32_e32 v207, v207
	v_mul_f32_e32 v206, v206, v150
	global_load_dwordx4 v[48:51], v192, s[46:47] offset:0
	global_load_dwordx4 v[52:55], v192, s[46:47] offset:1024
	v_mfma_f32_32x32x16_f16 v[96:111], a[128:131], v[160:163], v[96:111]
	ds_read_b128 v[160:163], v193 offset:8192
	v_rcp_f32_e32 v208, v208
	v_mul_f32_e32 v207, v207, v151
	global_load_dwordx4 v[56:59], v192, s[46:47] offset:2048
	global_load_dwordx4 v[60:63], v192, s[46:47] offset:3072
	v_mfma_f32_32x32x16_f16 v[112:127], a[128:131], v[164:167], v[112:127]
	ds_read_b128 v[164:167], v193 offset:9216
	v_rcp_f32_e32 v209, v209
	v_fmamk_f32 v208, v208, 0xc0b8aa3b, v198
	s_waitcnt lgkmcnt(2)
	v_mfma_f32_32x32x16_f16 v[96:111], a[132:135], v[168:171], v[96:111]
	ds_read_b128 v[168:171], v193 offset:10240
	v_rcp_f32_e32 v210, v210
	v_fmamk_f32 v209, v209, 0xc0b8aa3b, v198
	v_fma_f32 v148, v200, v208, v204
	v_mfma_f32_32x32x16_f16 v[112:127], a[132:135], v[172:175], v[112:127]
	ds_read_b128 v[172:175], v193 offset:11264
	global_load_lds_dwordx4 v192, s[44:45] offset:1024 sc1
	v_rcp_f32_e32 v211, v211
	v_fmamk_f32 v210, v210, 0xc0b8aa3b, v198
	v_fma_f32 v149, v201, v209, v205
	v_mfma_f32_32x32x16_f16 v[96:111], a[136:139], v[176:179], v[96:111]
	ds_read_b128 v[176:179], v193 offset:12288
	v_rcp_f32_e32 v212, v212
	v_fmamk_f32 v211, v211, 0xc0b8aa3b, v198
	v_fma_f32 v150, v202, v210, v206
	v_mfma_f32_32x32x16_f16 v[112:127], a[136:139], v[180:183], v[112:127]
	ds_read_b128 v[180:183], v193 offset:13312
	v_rcp_f32_e32 v213, v213
	v_fma_f32 v151, v203, v211, v207
	v_mfma_f32_32x32x16_f16 v[96:111], a[140:143], v[184:187], v[96:111]
	ds_read_b128 v[184:187], v193 offset:14336
	v_rcp_f32_e32 v214, v214
	v_mfma_f32_32x32x16_f16 v[112:127], a[140:143], v[188:191], v[112:127]
	ds_read_b128 v[188:191], v193 offset:15360
	global_load_lds_dwordx4 v192, s[44:45] offset:2048 sc1
	v_rcp_f32_e32 v215, v215
	s_waitcnt lgkmcnt(2)
	v_mfma_f32_32x32x16_f16 v[96:111], a[144:147], v[160:163], v[96:111]
	ds_read_b128 v[160:163], v193 offset:16384
	v_exp_f32_e32 v200, v148
	v_mfma_f32_32x32x16_f16 v[112:127], a[144:147], v[164:167], v[112:127]
	ds_read_b128 v[164:167], v193 offset:17408
	v_exp_f32_e32 v201, v149
	v_add_f32_e32 v200, 1.0, v200
	v_mfma_f32_32x32x16_f16 v[96:111], a[148:151], v[168:171], v[96:111]
	ds_read_b128 v[168:171], v193 offset:18432
	v_exp_f32_e32 v202, v150
	v_add_f32_e32 v201, 1.0, v201
	v_mfma_f32_32x32x16_f16 v[112:127], a[148:151], v[172:175], v[112:127]
	ds_read_b128 v[172:175], v193 offset:19456
	global_load_lds_dwordx4 v192, s[44:45] offset:3072 sc1
	v_exp_f32_e32 v203, v151
	v_add_f32_e32 v202, 1.0, v202
	v_mfma_f32_32x32x16_f16 v[96:111], a[152:155], v[176:179], v[96:111]
	ds_read_b128 v[176:179], v193 offset:20480
	v_add_f32_e32 v203, 1.0, v203
	v_rcp_f32_e32 v200, v200
	v_mfma_f32_32x32x16_f16 v[112:127], a[152:155], v[180:183], v[112:127]
	ds_read_b128 v[180:183], v193 offset:21504
	v_rcp_f32_e32 v201, v201
	v_fma_f32 v200, v200, 2.0, -1.0
	s_waitcnt lgkmcnt(2)
	v_mfma_f32_32x32x16_f16 v[96:111], a[156:159], v[184:187], v[96:111]
	ds_read_b128 v[184:187], v193 offset:22528
	v_rcp_f32_e32 v202, v202
	v_fma_f32 v201, v201, 2.0, -1.0
	v_mul_f32_e32 v216, v212, v200
	v_mfma_f32_32x32x16_f16 v[112:127], a[156:159], v[188:191], v[112:127]
	ds_read_b128 v[188:191], v193 offset:23552
	s_mov_b32 m0, s53
	s_add_u32 s44, s34, 0x1000
	s_addc_u32 s45, s35, 0
	global_load_lds_dwordx4 v192, s[44:45] sc1
	v_rcp_f32_e32 v203, v203
	v_fma_f32 v202, v202, 2.0, -1.0
	v_mul_f32_e32 v217, v213, v201
	v_mfma_f32_32x32x16_f16 v[96:111], a[160:163], v[160:163], v[96:111]
	ds_read_b128 v[160:163], v193 offset:24576
	v_fma_f32 v203, v203, 2.0, -1.0
	v_mul_f32_e32 v218, v214, v202
	v_mfma_f32_32x32x16_f16 v[112:127], a[160:163], v[164:167], v[112:127]
	ds_read_b128 v[164:167], v193 offset:25600
	v_mul_f32_e32 v219, v215, v203
	v_mul_f32_e32 v236, v216, v228
	v_mfma_f32_32x32x16_f16 v[96:111], a[164:167], v[168:171], v[96:111]
	ds_read_b128 v[168:171], v193 offset:26624
	v_mul_f32_e32 v237, v216, v232
	v_fmac_f32_e32 v236, v217, v229
	v_mfma_f32_32x32x16_f16 v[112:127], a[164:167], v[172:175], v[112:127]
	ds_read_b128 v[172:175], v193 offset:27648
	global_load_lds_dwordx4 v192, s[44:45] offset:1024 sc1
	v_fmac_f32_e32 v237, v217, v233
	v_fmac_f32_e32 v236, v218, v230
	s_waitcnt lgkmcnt(2)
	v_mfma_f32_32x32x16_f16 v[96:111], a[168:171], v[176:179], v[96:111]
	ds_read_b128 v[176:179], v193 offset:28672
	v_fmac_f32_e32 v237, v218, v234
	v_fmac_f32_e32 v236, v219, v231
	v_mfma_f32_32x32x16_f16 v[112:127], a[168:171], v[180:183], v[112:127]
	ds_read_b128 v[180:183], v193 offset:29696
	v_fmac_f32_e32 v237, v219, v235
	v_mov_b32_e32 v238, v236
	v_mfma_f32_32x32x16_f16 v[96:111], a[172:175], v[184:187], v[96:111]
	ds_read_b128 v[184:187], v193 offset:30720
	v_mov_b32_e32 v239, v236
	v_mov_b32_e32 v240, v237
	v_mfma_f32_32x32x16_f16 v[112:127], a[172:175], v[188:191], v[112:127]
	ds_read_b128 v[188:191], v193 offset:31744
	global_load_lds_dwordx4 v192, s[44:45] offset:2048 sc1
	v_mov_b32_e32 v241, v237
	v_cvt_pk_f16_f32 v222, v216, v217
	s_waitcnt vmcnt(15)
	s_barrier
	v_mfma_f32_32x32x16_f16 v[96:111], a[176:179], v[160:163], v[96:111]
	ds_read_b128 v[160:163], v193 offset:32768
	s_nop 1
	v_permlane32_swap_b32_e32 v238, v239
	v_permlane32_swap_b32_e32 v240, v241
	v_add_f32_e32 v238, v238, v239
	v_add_f32_e32 v239, v240, v241
	ds_write_b64 v248, v[238:239] offset:1280
	v_mfma_f32_32x32x16_f16 v[112:127], a[176:179], v[164:167], v[112:127]
	ds_read_b128 v[164:167], v193 offset:33792
	v_cvt_pk_f16_f32 v223, v218, v219
	s_waitcnt lgkmcnt(3)
	v_mfma_f32_32x32x16_f16 v[96:111], a[180:183], v[168:171], v[96:111]
	ds_read_b128 v[168:171], v193 offset:34816
	s_nop 1
	v_permlane32_swap_b32_e32 v220, v222
	v_permlane32_swap_b32_e32 v221, v223
	s_cmp_eq_u32 s31, 0
	s_cbranch_scc1 .LD_slow40
	global_store_dwordx4 v195, v[220:223], s[36:37] offset:0
.LD_join41:
	v_mfma_f32_32x32x16_f16 v[112:127], a[180:183], v[172:175], v[112:127]
	ds_read_b128 v[172:175], v193 offset:35840
	global_load_lds_dwordx4 v192, s[44:45] offset:3072 sc1
	v_mfma_f32_32x32x16_f16 v[96:111], a[184:187], v[176:179], v[96:111]
	ds_read_b128 v[176:179], v193 offset:36864
	v_mfma_f32_32x32x16_f16 v[112:127], a[184:187], v[180:183], v[112:127]
	ds_read_b128 v[180:183], v193 offset:37888
	v_mfma_f32_32x32x16_f16 v[96:111], a[188:191], v[184:187], v[96:111]
	ds_read_b128 v[184:187], v193 offset:38912
	v_mfma_f32_32x32x16_f16 v[112:127], a[188:191], v[188:191], v[112:127]
	ds_read_b128 v[188:191], v193 offset:39936
	s_mov_b32 m0, s54
	s_add_u32 s44, s34, 0x8000
	s_addc_u32 s45, s35, 0
	global_load_lds_dwordx4 v192, s[44:45] sc1
	s_waitcnt lgkmcnt(2)
	v_mfma_f32_32x32x16_f16 v[96:111], a[192:195], v[160:163], v[96:111]
	ds_read_b128 v[160:163], v193 offset:40960
	v_mfma_f32_32x32x16_f16 v[112:127], a[192:195], v[164:167], v[112:127]
	ds_read_b128 v[164:167], v193 offset:41984
	v_mfma_f32_32x32x16_f16 v[96:111], a[196:199], v[168:171], v[96:111]
	ds_read_b128 v[168:171], v193 offset:43008
	v_mfma_f32_32x32x16_f16 v[112:127], a[196:199], v[172:175], v[112:127]
	ds_read_b128 v[172:175], v193 offset:44032
	global_load_lds_dwordx4 v192, s[44:45] offset:1024 sc1
	v_mfma_f32_32x32x16_f16 v[96:111], a[200:203], v[176:179], v[96:111]
	ds_read_b128 v[176:179], v193 offset:45056
	v_mfma_f32_32x32x16_f16 v[112:127], a[200:203], v[180:183], v[112:127]
	ds_read_b128 v[180:183], v193 offset:46080
	s_waitcnt lgkmcnt(2)
	v_mfma_f32_32x32x16_f16 v[96:111], a[204:207], v[184:187], v[96:111]
	ds_read_b128 v[184:187], v193 offset:47104
	v_mfma_f32_32x32x16_f16 v[112:127], a[204:207], v[188:191], v[112:127]
	ds_read_b128 v[188:191], v193 offset:48128
	global_load_lds_dwordx4 v192, s[44:45] offset:2048 sc1
	s_waitcnt vmcnt(4)
	s_barrier
	v_mov_b32_e32 v199, 3
	s_cmp_eq_u32 s31, 0
	s_cbranch_scc1 .LD_slow42
	global_store_dword v197, v199, s[40:41]
.LD_join43:
	ds_read_b64 v[200:201], v249 offset:1024
	ds_read_b64 v[202:203], v249 offset:3072
	ds_read_b64 v[204:205], v249 offset:5120
	ds_read_b64 v[206:207], v249 offset:7168
	v_mfma_f32_32x32x16_f16 v[96:111], a[208:211], v[160:163], v[96:111]
	ds_read_b128 v[160:163], v193 offset:49152
	v_mfma_f32_32x32x16_f16 v[112:127], a[208:211], v[164:167], v[112:127]
	ds_read_b128 v[164:167], v193 offset:50176
	v_mfma_f32_32x32x16_f16 v[96:111], a[212:215], v[168:171], v[96:111]
	ds_read_b128 v[168:171], v193 offset:51200
	v_mfma_f32_32x32x16_f16 v[112:127], a[212:215], v[172:175], v[112:127]
	ds_read_b128 v[172:175], v193 offset:52224
	global_load_lds_dwordx4 v192, s[44:45] offset:3072 sc1
	s_waitcnt lgkmcnt(2)
	v_mfma_f32_32x32x16_f16 v[96:111], a[216:219], v[176:179], v[96:111]
	ds_read_b128 v[176:179], v193 offset:53248
	v_mfma_f32_32x32x16_f16 v[112:127], a[216:219], v[180:183], v[112:127]
	ds_read_b128 v[180:183], v193 offset:54272
	v_mfma_f32_32x32x16_f16 v[96:111], a[220:223], v[184:187], v[96:111]
	ds_read_b128 v[184:187], v193 offset:55296
	v_mfma_f32_32x32x16_f16 v[112:127], a[220:223], v[188:191], v[112:127]
	ds_read_b128 v[188:191], v193 offset:56320
	s_mov_b32 m0, s55
	s_add_u32 s44, s34, 0x9000
	s_addc_u32 s45, s35, 0
	global_load_lds_dwordx4 v192, s[44:45] sc1
	v_mfma_f32_32x32x16_f16 v[96:111], a[224:227], v[160:163], v[96:111]
	ds_read_b128 v[160:163], v193 offset:57344
	v_mfma_f32_32x32x16_f16 v[112:127], a[224:227], v[164:167], v[112:127]
	ds_read_b128 v[164:167], v193 offset:58368
	s_waitcnt lgkmcnt(2)
	v_mfma_f32_32x32x16_f16 v[96:111], a[228:231], v[168:171], v[96:111]
	ds_read_b128 v[168:171], v193 offset:59392
	v_mfma_f32_32x32x16_f16 v[112:127], a[228:231], v[172:175], v[112:127]
	ds_read_b128 v[172:175], v193 offset:60416
	global_load_lds_dwordx4 v192, s[44:45] offset:1024 sc1
	v_add_f32_e32 v200, v200, v202
	v_add_f32_e32 v201, v201, v203
	v_add_f32_e32 v200, v200, v204
	v_add_f32_e32 v201, v201, v205
	v_add_f32_e32 v200, v200, v206
	v_add_f32_e32 v201, v201, v207
	global_store_dwordx2 v250, v[200:201], s[72:73]
	v_mfma_f32_32x32x16_f16 v[96:111], a[232:235], v[176:179], v[96:111]
	ds_read_b128 v[176:179], v193 offset:61440
	v_mfma_f32_32x32x16_f16 v[112:127], a[232:235], v[180:183], v[112:127]
	ds_read_b128 v[180:183], v193 offset:62464
	v_mfma_f32_32x32x16_f16 v[96:111], a[236:239], v[184:187], v[96:111]
	ds_read_b128 v[184:187], v193 offset:63488
	v_mfma_f32_32x32x16_f16 v[112:127], a[236:239], v[188:191], v[112:127]
	ds_read_b128 v[188:191], v193 offset:64512
	global_load_lds_dwordx4 v192, s[44:45] offset:2048 sc1
	s_waitcnt vmcnt(9)
	s_barrier
	s_waitcnt lgkmcnt(2)
	v_mfma_f32_32x32x16_f16 v[96:111], a[240:243], v[160:163], v[96:111]
	ds_read_b128 v[160:163], v192 offset:0
	v_mfma_f32_32x32x16_f16 v[112:127], a[240:243], v[164:167], v[112:127]
	ds_read_b128 v[164:167], v192 offset:1024
	v_mfma_f32_32x32x16_f16 v[96:111], a[244:247], v[168:171], v[96:111]
	ds_read_b128 v[168:171], v192 offset:2048
	v_mfma_f32_32x32x16_f16 v[112:127], a[244:247], v[172:175], v[112:127]
	ds_read_b128 v[172:175], v192 offset:3072
	global_load_lds_dwordx4 v192, s[44:45] offset:3072 sc1
	v_mfma_f32_32x32x16_f16 v[96:111], a[248:251], v[176:179], v[96:111]
	ds_read_b128 v[176:179], v192 offset:4096
	v_mfma_f32_32x32x16_f16 v[112:127], a[248:251], v[180:183], v[112:127]
	ds_read_b128 v[180:183], v192 offset:5120
	s_waitcnt lgkmcnt(2)
	v_mfma_f32_32x32x16_f16 v[96:111], a[252:255], v[184:187], v[96:111]
	ds_read_b128 v[184:187], v192 offset:6144
	v_mfma_f32_32x32x16_f16 v[112:127], a[252:255], v[188:191], v[112:127]
	ds_read_b128 v[188:191], v192 offset:7168
	s_mov_b32 m0, s56
	s_add_u32 s44, s34, 0x10000
	s_addc_u32 s45, s35, 0
	global_load_lds_dwordx4 v192, s[44:45] sc1
	s_add_u32 s33, s33, 1
	s_cmp_lt_u32 s33, s28
	s_cbranch_scc1 .LD_loop16
